# scan epilogue: mask-and + or3 fused into v_and_or_b32 with per-chunk index SGPRs (94 of 96 loop sites)
# baseline (speedup 1.0000x reference)
.LBB1_6:
	s_or_b64 exec, exec, s[4:5]
	v_mov_b32_e32 v6, 0x18010
	v_mov_b32_e32 v2, 0x18000
	s_waitcnt lgkmcnt(0)
	s_barrier
	s_waitcnt vmcnt(8)
	ds_read_b128 v[2:5], v2
	ds_read_b128 v[6:9], v6
	s_load_dwordx4 s[36:39], s[0:1], 0x20
	s_movk_i32 s0, 0x2000
	v_lshrrev_b32_e32 v125, 4, v131
	s_waitcnt lgkmcnt(0)
	v_mov_b32_e32 v14, v2
	v_mov_b32_e32 v15, v6
	v_mov_b32_e32 v6, v3
	v_pk_add_f32 v[2:3], v[14:15], v[6:7]
	v_mov_b32_e32 v6, v4
	v_mov_b32_e32 v7, v8
	v_mov_b32_e32 v8, v5
	v_pk_add_f32 v[4:5], v[6:7], v[8:9]
	v_mov_b32_e32 v14, 0x18060
	v_pk_add_f32 v[2:3], v[2:3], v[4:5]
	v_add_co_u32_e32 v42, vcc, s0, v82
	v_add_f32_e32 v2, v2, v3
	v_mul_f32_e32 v132, 0x3a800000, v2
	v_and_b32_e32 v107, 15, v0
	v_mov_b32_e32 v2, 0x18020
	v_mov_b32_e32 v3, 0x18030
	v_lshl_add_u32 v13, v13, 2, v14
	v_pk_add_f32 v[10:11], v[10:11], v[132:133] op_sel_hi:[1,0] neg_lo:[0,1] neg_hi:[0,1]
	v_lshlrev_b32_e32 v85, 13, v1
	v_xor_b32_e32 v114, v125, v0
	v_addc_co_u32_e32 v43, vcc, 0, v83, vcc
	s_movk_i32 s0, 0x3000
	ds_read_b128 v[6:9], v2
	ds_read_b128 v[2:5], v3
	ds_write_b64 v13, v[10:11]
	v_lshl_or_b32 v84, v107, 9, v85
	v_lshlrev_b32_e32 v10, 4, v114
	s_movk_i32 s41, 0xf0
	v_add_co_u32_e32 v44, vcc, s0, v82
	v_lshlrev_b32_e32 v130, 2, v12
	v_and_or_b32 v115, v10, s41, v84
	v_addc_co_u32_e32 v45, vcc, 0, v83, vcc
	global_load_dwordx4 v[34:37], v[42:43], off offset:1024 nt
	global_load_dwordx4 v[30:33], v[42:43], off offset:2048 nt
	global_load_dwordx4 v[26:29], v[42:43], off offset:3072 nt
	global_load_dwordx4 v[38:41], v[44:45], off offset:-4096 nt
	global_load_dwordx4 v[22:25], v[44:45], off nt
	global_load_dwordx4 v[18:21], v[44:45], off offset:1024 nt
	global_load_dwordx4 v[14:17], v[44:45], off offset:2048 nt
	global_load_dwordx4 v[10:13], v[44:45], off offset:3072 nt
	s_waitcnt vmcnt(15)
	v_add_f32_e32 v42, v78, v79
	v_add_f32_e32 v43, v80, v81
	v_add_f32_e32 v42, v42, v43
	s_waitcnt vmcnt(14)
	v_add_f32_e32 v43, v74, v75
	v_add_f32_e32 v44, v76, v77
	v_add_f32_e32 v43, v43, v44
	s_waitcnt vmcnt(13)
	v_add_f32_e32 v44, v70, v71
	v_add_f32_e32 v45, v72, v73
	v_add_f32_e32 v44, v44, v45
	s_waitcnt vmcnt(12)
	v_add_f32_e32 v45, v66, v67
	v_add_f32_e32 v49, v68, v69
	v_add_f32_e32 v45, v45, v49
	s_waitcnt vmcnt(11)
	v_add_f32_e32 v49, v62, v63
	v_add_f32_e32 v86, v64, v65
	v_and_b32_e32 v46, 1, v0
	v_add_f32_e32 v49, v49, v86
	s_waitcnt vmcnt(10)
	v_add_f32_e32 v86, v58, v59
	v_add_f32_e32 v88, v60, v61
	v_add_f32_e32 v86, v86, v88
	s_waitcnt vmcnt(9)
	v_add_f32_e32 v88, v54, v55
	v_add_f32_e32 v89, v56, v57
	v_cmp_eq_u32_e64 s[4:5], 1, v46
	v_add_f32_e32 v88, v88, v89
	s_waitcnt vmcnt(8)
	v_add_f32_e32 v89, v50, v51
	v_add_f32_e32 v90, v52, v53
	v_cndmask_b32_e64 v46, v43, v42, s[4:5]
	v_cndmask_b32_e64 v42, v42, v43, s[4:5]
	v_cndmask_b32_e64 v43, v45, v44, s[4:5]
	v_cndmask_b32_e64 v44, v44, v45, s[4:5]
	v_add_f32_e32 v89, v89, v90
	v_cndmask_b32_e64 v45, v49, v86, s[4:5]
	v_add_f32_dpp v43, v43, v44 quad_perm:[1,0,3,2] row_mask:0xf bank_mask:0xf bound_ctrl:1
	v_cndmask_b32_e64 v44, v86, v49, s[4:5]
	v_and_b32_e32 v47, 2, v0
	v_add_f32_dpp v42, v46, v42 quad_perm:[1,0,3,2] row_mask:0xf bank_mask:0xf bound_ctrl:1
	v_add_f32_dpp v44, v44, v45 quad_perm:[1,0,3,2] row_mask:0xf bank_mask:0xf bound_ctrl:1
	v_cndmask_b32_e64 v45, v89, v88, s[4:5]
	v_cndmask_b32_e64 v46, v88, v89, s[4:5]
	v_cmp_eq_u16_e64 s[6:7], 0, v47
	v_and_b32_e32 v48, 4, v0
	v_add_f32_dpp v45, v45, v46 quad_perm:[1,0,3,2] row_mask:0xf bank_mask:0xf bound_ctrl:1
	v_cndmask_b32_e64 v46, v42, v43, s[6:7]
	v_cndmask_b32_e64 v42, v43, v42, s[6:7]
	v_cndmask_b32_e64 v43, v44, v45, s[6:7]
	v_cndmask_b32_e64 v44, v45, v44, s[6:7]
	v_add_f32_dpp v42, v46, v42 quad_perm:[2,3,0,1] row_mask:0xf bank_mask:0xf bound_ctrl:1
	v_cmp_eq_u16_e64 s[8:9], 0, v48
	v_add_f32_dpp v43, v43, v44 quad_perm:[2,3,0,1] row_mask:0xf bank_mask:0xf bound_ctrl:1
	v_lshlrev_b32_e32 v86, 3, v131
	v_cndmask_b32_e64 v44, v42, v43, s[8:9]
	v_cndmask_b32_e64 v42, v43, v42, s[8:9]
	v_mov_b32_e32 v43, v44
	v_and_b32_e32 v87, 8, v87
	v_mov_b32_e32 v116, 0x3727c5ac
	v_mov_b32_dpp v43, v43 row_shl:4 row_mask:0xf bank_mask:0x5
	v_mov_b32_e32 v117, 0x260
	v_bitop3_b32 v141, v125, v0, 4 bitop3:0x36
	v_mov_b32_dpp v43, v44 row_shr:4 row_mask:0xf bank_mask:0xa
	v_add_f32_e32 v42, v42, v43
	v_bitop3_b32 v142, v125, v0, 8 bitop3:0x36
	v_bitop3_b32 v143, v125, v0, 12 bitop3:0x36
	v_add_f32_dpp v42, v42, v42 row_ror:8 row_mask:0xf bank_mask:0xf bound_ctrl:1
	v_mov_b32_e32 v43, v42
	s_nop 1
	v_permlane16_swap_b32_e32 v42, v43
	v_add_f32_e32 v42, v42, v43
	v_mov_b32_e32 v43, v42
	s_nop 1
	v_permlane32_swap_b32_e32 v42, v43
	v_add_f32_e32 v42, v42, v43
	v_mul_f32_e32 v42, 0x3b800000, v42
	s_mov_b32 s3, 0
	v_readlane_b32 s40, v42, 0
	v_readlane_b32 s42, v42, 1
	v_readlane_b32 s44, v42, 2
	v_readlane_b32 s46, v42, 3
	v_readlane_b32 s48, v42, 4
	v_readlane_b32 s50, v42, 5
	v_readlane_b32 s34, v42, 6
	v_readlane_b32 s0, v42, 7
	global_load_dwordx4 v[42:45], v130, s[22:23]
	global_load_dwordx4 v[46:49], v130, s[24:25]
	v_pk_add_f32 v[90:91], v[78:79], s[40:41] op_sel_hi:[1,0] neg_lo:[0,1] neg_hi:[0,1]
	v_pk_add_f32 v[80:81], v[80:81], s[40:41] op_sel_hi:[1,0] neg_lo:[0,1] neg_hi:[0,1]
	v_and_b32_e32 v78, 0x1f0, v86
	v_pk_add_f32 v[76:77], v[76:77], s[42:43] op_sel_hi:[1,0] neg_lo:[0,1] neg_hi:[0,1]
	v_mul_f32_e32 v88, v81, v81
	v_or3_b32 v140, v85, v78, v87
	v_pk_add_f32 v[78:79], v[74:75], s[42:43] op_sel_hi:[1,0] neg_lo:[0,1] neg_hi:[0,1]
	v_mul_f32_e32 v74, v77, v77
	v_fmac_f32_e32 v88, v80, v80
	v_fmac_f32_e32 v74, v76, v76
	v_fmac_f32_e32 v88, v91, v91
	v_fmac_f32_e32 v74, v79, v79
	v_fmac_f32_e32 v88, v90, v90
	v_fmac_f32_e32 v74, v78, v78
	v_cndmask_b32_e64 v75, v74, v88, s[4:5]
	v_cndmask_b32_e64 v74, v88, v74, s[4:5]
	v_mov_b32_e32 v88, 0x1f0
	v_pk_add_f32 v[72:73], v[72:73], s[44:45] op_sel_hi:[1,0] neg_lo:[0,1] neg_hi:[0,1]
	v_add_f32_dpp v89, v75, v74 quad_perm:[1,0,3,2] row_mask:0xf bank_mask:0xf bound_ctrl:1
	v_bitop3_b32 v74, v86, 16, v88 bitop3:0x6c
	v_or3_b32 v138, v85, v74, v87
	v_pk_add_f32 v[74:75], v[70:71], s[44:45] op_sel_hi:[1,0] neg_lo:[0,1] neg_hi:[0,1]
	v_bitop3_b32 v70, v86, 32, v88 bitop3:0x6c
	v_pk_add_f32 v[68:69], v[68:69], s[46:47] op_sel_hi:[1,0] neg_lo:[0,1] neg_hi:[0,1]
	v_mul_f32_e32 v92, v73, v73
	v_or3_b32 v135, v85, v70, v87
	v_pk_add_f32 v[70:71], v[66:67], s[46:47] op_sel_hi:[1,0] neg_lo:[0,1] neg_hi:[0,1]
	v_mul_f32_e32 v66, v69, v69
	v_fmac_f32_e32 v92, v72, v72
	v_fmac_f32_e32 v66, v68, v68
	v_fmac_f32_e32 v92, v75, v75
	v_fmac_f32_e32 v66, v71, v71
	v_fmac_f32_e32 v92, v74, v74
	v_fmac_f32_e32 v66, v70, v70
	v_cndmask_b32_e64 v67, v66, v92, s[4:5]
	v_cndmask_b32_e64 v66, v92, v66, s[4:5]
	v_pk_add_f32 v[64:65], v[64:65], s[48:49] op_sel_hi:[1,0] neg_lo:[0,1] neg_hi:[0,1]
	v_pk_add_f32 v[60:61], v[60:61], s[50:51] op_sel_hi:[1,0] neg_lo:[0,1] neg_hi:[0,1]
	v_add_f32_dpp v66, v67, v66 quad_perm:[1,0,3,2] row_mask:0xf bank_mask:0xf bound_ctrl:1
	v_cndmask_b32_e64 v67, v89, v66, s[6:7]
	v_cndmask_b32_e64 v66, v66, v89, s[6:7]
	v_mul_f32_e32 v92, v65, v65
	v_fmac_f32_e32 v92, v64, v64
	v_add_f32_dpp v89, v67, v66 quad_perm:[2,3,0,1] row_mask:0xf bank_mask:0xf bound_ctrl:1
	v_bitop3_b32 v66, v86, 48, v88 bitop3:0x6c
	v_or3_b32 v134, v85, v66, v87
	v_pk_add_f32 v[66:67], v[62:63], s[48:49] op_sel_hi:[1,0] neg_lo:[0,1] neg_hi:[0,1]
	v_bitop3_b32 v62, v86, 64, v88 bitop3:0x6c
	v_or3_b32 v120, v85, v62, v87
	v_pk_add_f32 v[62:63], v[58:59], s[50:51] op_sel_hi:[1,0] neg_lo:[0,1] neg_hi:[0,1]
	v_mul_f32_e32 v58, v61, v61
	v_fmac_f32_e32 v58, v60, v60
	v_fmac_f32_e32 v92, v67, v67
	v_fmac_f32_e32 v58, v63, v63
	v_fmac_f32_e32 v92, v66, v66
	v_fmac_f32_e32 v58, v62, v62
	v_cndmask_b32_e64 v59, v58, v92, s[4:5]
	v_cndmask_b32_e64 v58, v92, v58, s[4:5]
	v_pk_add_f32 v[56:57], v[56:57], s[34:35] op_sel_hi:[1,0] neg_lo:[0,1] neg_hi:[0,1]
	s_mov_b32 s25, 0x3e6d3387
	v_add_f32_dpp v92, v59, v58 quad_perm:[1,0,3,2] row_mask:0xf bank_mask:0xf bound_ctrl:1
	v_pk_add_f32 v[58:59], v[54:55], s[34:35] op_sel_hi:[1,0] neg_lo:[0,1] neg_hi:[0,1]
	v_pk_add_f32 v[54:55], v[50:51], s[0:1] op_sel_hi:[1,0] neg_lo:[0,1] neg_hi:[0,1]
	v_pk_add_f32 v[50:51], v[52:53], s[0:1] op_sel_hi:[1,0] neg_lo:[0,1] neg_hi:[0,1]
	v_mul_f32_e32 v93, v57, v57
	v_mul_f32_e32 v52, v51, v51
	v_fmac_f32_e32 v93, v56, v56
	v_fmac_f32_e32 v52, v50, v50
	v_fmac_f32_e32 v93, v59, v59
	v_fmac_f32_e32 v52, v55, v55
	v_fmac_f32_e32 v93, v58, v58
	v_fmac_f32_e32 v52, v54, v54
	v_cndmask_b32_e64 v53, v52, v93, s[4:5]
	v_cndmask_b32_e64 v52, v93, v52, s[4:5]
	s_mov_b32 s35, 0xf800000
	s_movk_i32 s0, 0x50
	v_add_f32_dpp v52, v53, v52 quad_perm:[1,0,3,2] row_mask:0xf bank_mask:0xf bound_ctrl:1
	v_cndmask_b32_e64 v53, v92, v52, s[6:7]
	v_cndmask_b32_e64 v52, v52, v92, s[6:7]
	s_mov_b32 s24, 0xbf3a00e3
	s_mov_b32 s22, 0x3f07dc22
	v_add_f32_dpp v52, v53, v52 quad_perm:[2,3,0,1] row_mask:0xf bank_mask:0xf bound_ctrl:1
	v_cndmask_b32_e64 v53, v89, v52, s[8:9]
	v_cndmask_b32_e64 v52, v52, v89, s[8:9]
	v_mov_b32_e32 v89, v53
	s_mov_b32 s34, 0xbe11a98e
	s_mov_b32 s40, 0x3e027906
	v_mov_b32_dpp v89, v89 row_shl:4 row_mask:0xf bank_mask:0x5
	s_mov_b32 s33, 5
	s_nop 0
	v_mov_b32_dpp v89, v53 row_shr:4 row_mask:0xf bank_mask:0xa
	v_add_f32_e32 v52, v52, v89
	v_bitop3_b32 v89, v86, s0, v88 bitop3:0x6c
	v_or3_b32 v121, v85, v89, v87
	v_add_f32_dpp v52, v52, v52 row_ror:8 row_mask:0xf bank_mask:0xf bound_ctrl:1
	v_mov_b32_e32 v53, v52
	s_nop 1
	v_permlane16_swap_b32_e32 v52, v53
	v_add_f32_e32 v52, v52, v53
	v_mov_b32_e32 v53, v52
	s_nop 1
	v_permlane32_swap_b32_e32 v52, v53
	v_add_f32_e32 v52, v52, v53
	v_fmamk_f32 v52, v52, 0x3b800000, v116
	v_mul_f32_e32 v53, 0x4f800000, v52
	v_cmp_gt_f32_e32 vcc, s35, v52
	s_nop 1
	v_cndmask_b32_e32 v52, v52, v53, vcc
	v_sqrt_f32_e32 v53, v52
	s_nop 0
	v_add_u32_e32 v89, -1, v53
	v_fma_f32 v92, -v89, v53, v52
	v_cmp_ge_f32_e64 s[0:1], 0, v92
	v_add_u32_e32 v92, 1, v53
	s_nop 0
	v_cndmask_b32_e64 v89, v53, v89, s[0:1]
	v_fma_f32 v53, -v92, v53, v52
	v_cmp_lt_f32_e64 s[0:1], 0, v53
	s_nop 1
	v_cndmask_b32_e64 v53, v89, v92, s[0:1]
	v_mul_f32_e32 v89, 0x37800000, v53
	v_cndmask_b32_e32 v53, v53, v89, vcc
	v_cmp_class_f32_e32 vcc, v52, v117
	s_nop 1
	v_cndmask_b32_e32 v52, v53, v52, vcc
	v_div_scale_f32 v53, s[0:1], v52, v52, 1.0
	v_rcp_f32_e32 v89, v53
	s_movk_i32 s0, 0x60
	v_bitop3_b32 v92, v86, s0, v88 bitop3:0x6c
	v_or3_b32 v118, v85, v92, v87
	v_fma_f32 v92, -v53, v89, 1.0
	v_fmac_f32_e32 v89, v92, v89
	v_div_scale_f32 v92, vcc, 1.0, v52, 1.0
	v_mul_f32_e32 v93, v92, v89
	v_fma_f32 v94, -v53, v93, v92
	v_fmac_f32_e32 v93, v94, v89
	v_fma_f32 v53, -v53, v93, v92
	v_div_fmas_f32 v53, v53, v89, v93
	v_div_fixup_f32 v52, v53, v52, 1.0
	s_waitcnt vmcnt(6)
	v_add_f32_e32 v89, v38, v39
	v_readlane_b32 s0, v52, 0
	s_nop 1
	v_pk_mul_f32 v[90:91], s[0:1], v[90:91] op_sel_hi:[0,1]
	s_waitcnt vmcnt(0)
	v_pk_fma_f32 v[92:93], v[90:91], v[42:43], v[46:47]
	v_mov_b64_e32 v[90:91], s[24:25]
	v_fma_f32 v53, |v92|, s25, 1.0
	v_pk_mul_f32 v[98:99], v[92:93], v[92:93]
	v_rcp_f32_e32 v96, v53
	v_mul_f32_e32 v53, 0xbf38aa3b, v98
	v_exp_f32_e32 v98, v53
	v_fma_f32 v53, |v93|, s25, 1.0
	v_rcp_f32_e32 v97, v53
	s_mov_b32 s24, 0x3f35f0e3
	v_pk_mul_f32 v[80:81], s[0:1], v[80:81] op_sel_hi:[0,1]
	v_mul_f32_e32 v53, 0xbf38aa3b, v99
	v_pk_fma_f32 v[100:101], v[96:97], s[22:23], v[90:91] op_sel_hi:[1,0,0]
	v_pk_fma_f32 v[80:81], v[80:81], v[44:45], v[48:49]
	v_pk_fma_f32 v[100:101], v[96:97], v[100:101], s[24:25] op_sel_hi:[1,1,0]
	v_and_b32_e32 v95, 0x7fffffff, v93
	v_pk_fma_f32 v[100:101], v[96:97], v[100:101], s[34:35] op_sel_hi:[1,1,0]
	v_and_b32_e32 v94, 0x7fffffff, v92
	v_pk_fma_f32 v[100:101], v[96:97], v[100:101], s[40:41] op_sel_hi:[1,1,0]
	v_exp_f32_e32 v99, v53
	v_pk_mul_f32 v[96:97], v[96:97], v[100:101]
	v_fma_f32 v53, |v80|, s25, 1.0
	v_pk_mul_f32 v[94:95], v[94:95], v[96:97]
	v_rcp_f32_e32 v96, v53
	v_fma_f32 v53, |v81|, s25, 1.0
	v_rcp_f32_e32 v97, v53
	v_max_f32_e32 v92, 0, v92
	v_max_f32_e32 v93, 0, v93
	v_pk_fma_f32 v[92:93], v[98:99], v[94:95], v[92:93] neg_lo:[1,0,0] neg_hi:[1,0,0]
	v_pk_mul_f32 v[98:99], v[80:81], v[80:81]
	v_pk_fma_f32 v[100:101], v[96:97], s[22:23], v[90:91] op_sel_hi:[1,0,0]
	v_mul_f32_e32 v53, 0xbf38aa3b, v98
	v_exp_f32_e32 v98, v53
	v_pk_fma_f32 v[100:101], v[96:97], v[100:101], s[24:25] op_sel_hi:[1,1,0]
	v_mul_f32_e32 v53, 0xbf38aa3b, v99
	v_pk_fma_f32 v[100:101], v[96:97], v[100:101], s[34:35] op_sel_hi:[1,1,0]
	v_exp_f32_e32 v99, v53
	v_pk_fma_f32 v[100:101], v[96:97], v[100:101], s[40:41] op_sel_hi:[1,1,0]
	v_and_b32_e32 v95, 0x7fffffff, v81
	v_and_b32_e32 v94, 0x7fffffff, v80
	v_pk_mul_f32 v[96:97], v[96:97], v[100:101]
	v_readlane_b32 s0, v52, 1
	v_max_f32_e32 v80, 0, v80
	v_max_f32_e32 v81, 0, v81
	v_pk_mul_f32 v[94:95], v[94:95], v[96:97]
	v_pk_mul_f32 v[78:79], s[0:1], v[78:79] op_sel_hi:[0,1]
	v_pk_fma_f32 v[80:81], v[98:99], v[94:95], v[80:81] neg_lo:[1,0,0] neg_hi:[1,0,0]
	v_pk_fma_f32 v[78:79], v[78:79], v[42:43], v[46:47]
	v_cvt_pk_f16_f32 v92, v92, v93
	v_cvt_pk_f16_f32 v93, v80, v81
	v_fma_f32 v53, |v78|, s25, 1.0
	ds_write_b64 v140, v[92:93] offset:32768
	v_rcp_f32_e32 v92, v53
	v_fma_f32 v53, |v79|, s25, 1.0
	v_rcp_f32_e32 v93, v53
	v_pk_mul_f32 v[94:95], v[78:79], v[78:79]
	v_pk_mul_f32 v[76:77], s[0:1], v[76:77] op_sel_hi:[0,1]
	v_mul_f32_e32 v53, 0xbf38aa3b, v94
	v_pk_fma_f32 v[96:97], v[92:93], s[22:23], v[90:91] op_sel_hi:[1,0,0]
	v_exp_f32_e32 v94, v53
	v_pk_fma_f32 v[96:97], v[92:93], v[96:97], s[24:25] op_sel_hi:[1,1,0]
	v_mul_f32_e32 v53, 0xbf38aa3b, v95
	v_pk_fma_f32 v[96:97], v[92:93], v[96:97], s[34:35] op_sel_hi:[1,1,0]
	v_pk_fma_f32 v[76:77], v[76:77], v[44:45], v[48:49]
	v_pk_fma_f32 v[96:97], v[92:93], v[96:97], s[40:41] op_sel_hi:[1,1,0]
	v_and_b32_e32 v81, 0x7fffffff, v79
	v_and_b32_e32 v80, 0x7fffffff, v78
	v_exp_f32_e32 v95, v53
	v_pk_mul_f32 v[92:93], v[92:93], v[96:97]
	v_fma_f32 v53, |v76|, s25, 1.0
	v_pk_mul_f32 v[80:81], v[80:81], v[92:93]
	v_rcp_f32_e32 v92, v53
	v_fma_f32 v53, |v77|, s25, 1.0
	v_rcp_f32_e32 v93, v53
	v_max_f32_e32 v78, 0, v78
	v_max_f32_e32 v79, 0, v79
	v_pk_fma_f32 v[78:79], v[94:95], v[80:81], v[78:79] neg_lo:[1,0,0] neg_hi:[1,0,0]
	v_pk_mul_f32 v[94:95], v[76:77], v[76:77]
	v_pk_fma_f32 v[96:97], v[92:93], s[22:23], v[90:91] op_sel_hi:[1,0,0]
	v_mul_f32_e32 v53, 0xbf38aa3b, v94
	v_exp_f32_e32 v94, v53
	v_pk_fma_f32 v[96:97], v[92:93], v[96:97], s[24:25] op_sel_hi:[1,1,0]
	v_mul_f32_e32 v53, 0xbf38aa3b, v95
	v_pk_fma_f32 v[96:97], v[92:93], v[96:97], s[34:35] op_sel_hi:[1,1,0]
	v_exp_f32_e32 v95, v53
	v_pk_fma_f32 v[96:97], v[92:93], v[96:97], s[40:41] op_sel_hi:[1,1,0]
	v_and_b32_e32 v81, 0x7fffffff, v77
	v_and_b32_e32 v80, 0x7fffffff, v76
	v_pk_mul_f32 v[92:93], v[92:93], v[96:97]
	v_readlane_b32 s0, v52, 2
	v_max_f32_e32 v76, 0, v76
	v_max_f32_e32 v77, 0, v77
	v_pk_mul_f32 v[80:81], v[80:81], v[92:93]
	v_pk_mul_f32 v[74:75], s[0:1], v[74:75] op_sel_hi:[0,1]
	v_pk_fma_f32 v[76:77], v[94:95], v[80:81], v[76:77] neg_lo:[1,0,0] neg_hi:[1,0,0]
	v_pk_fma_f32 v[74:75], v[74:75], v[42:43], v[46:47]
	v_cvt_pk_f16_f32 v78, v78, v79
	v_cvt_pk_f16_f32 v79, v76, v77
	v_fma_f32 v53, |v74|, s25, 1.0
	ds_write_b64 v138, v[78:79] offset:33280
	v_rcp_f32_e32 v78, v53
	v_fma_f32 v53, |v75|, s25, 1.0
	v_rcp_f32_e32 v79, v53
	v_pk_mul_f32 v[80:81], v[74:75], v[74:75]
	v_pk_mul_f32 v[72:73], s[0:1], v[72:73] op_sel_hi:[0,1]
	v_mul_f32_e32 v53, 0xbf38aa3b, v80
	v_pk_fma_f32 v[92:93], v[78:79], s[22:23], v[90:91] op_sel_hi:[1,0,0]
	v_exp_f32_e32 v80, v53
	v_pk_fma_f32 v[92:93], v[78:79], v[92:93], s[24:25] op_sel_hi:[1,1,0]
	v_mul_f32_e32 v53, 0xbf38aa3b, v81
	v_pk_fma_f32 v[92:93], v[78:79], v[92:93], s[34:35] op_sel_hi:[1,1,0]
	v_pk_fma_f32 v[72:73], v[72:73], v[44:45], v[48:49]
	v_pk_fma_f32 v[92:93], v[78:79], v[92:93], s[40:41] op_sel_hi:[1,1,0]
	v_and_b32_e32 v77, 0x7fffffff, v75
	v_and_b32_e32 v76, 0x7fffffff, v74
	v_exp_f32_e32 v81, v53
	v_pk_mul_f32 v[78:79], v[78:79], v[92:93]
	v_fma_f32 v53, |v72|, s25, 1.0
	v_pk_mul_f32 v[76:77], v[76:77], v[78:79]
	v_rcp_f32_e32 v78, v53
	v_fma_f32 v53, |v73|, s25, 1.0
	v_rcp_f32_e32 v79, v53
	v_max_f32_e32 v74, 0, v74
	v_max_f32_e32 v75, 0, v75
	v_pk_fma_f32 v[74:75], v[80:81], v[76:77], v[74:75] neg_lo:[1,0,0] neg_hi:[1,0,0]
	v_pk_mul_f32 v[80:81], v[72:73], v[72:73]
	v_pk_fma_f32 v[92:93], v[78:79], s[22:23], v[90:91] op_sel_hi:[1,0,0]
	v_mul_f32_e32 v53, 0xbf38aa3b, v80
	v_exp_f32_e32 v80, v53
	v_pk_fma_f32 v[92:93], v[78:79], v[92:93], s[24:25] op_sel_hi:[1,1,0]
	v_mul_f32_e32 v53, 0xbf38aa3b, v81
	v_pk_fma_f32 v[92:93], v[78:79], v[92:93], s[34:35] op_sel_hi:[1,1,0]
	v_exp_f32_e32 v81, v53
	v_pk_fma_f32 v[92:93], v[78:79], v[92:93], s[40:41] op_sel_hi:[1,1,0]
	v_and_b32_e32 v77, 0x7fffffff, v73
	v_and_b32_e32 v76, 0x7fffffff, v72
	v_pk_mul_f32 v[78:79], v[78:79], v[92:93]
	v_readlane_b32 s0, v52, 3
	v_max_f32_e32 v72, 0, v72
	v_max_f32_e32 v73, 0, v73
	v_pk_mul_f32 v[76:77], v[76:77], v[78:79]
	v_pk_mul_f32 v[70:71], s[0:1], v[70:71] op_sel_hi:[0,1]
	v_pk_fma_f32 v[72:73], v[80:81], v[76:77], v[72:73] neg_lo:[1,0,0] neg_hi:[1,0,0]
	v_pk_fma_f32 v[70:71], v[70:71], v[42:43], v[46:47]
	v_cvt_pk_f16_f32 v74, v74, v75
	v_cvt_pk_f16_f32 v75, v72, v73
	v_fma_f32 v53, |v70|, s25, 1.0
	ds_write_b64 v135, v[74:75] offset:33792
	v_rcp_f32_e32 v74, v53
	v_fma_f32 v53, |v71|, s25, 1.0
	v_rcp_f32_e32 v75, v53
	v_pk_mul_f32 v[76:77], v[70:71], v[70:71]
	v_pk_mul_f32 v[68:69], s[0:1], v[68:69] op_sel_hi:[0,1]
	v_mul_f32_e32 v53, 0xbf38aa3b, v76
	v_pk_fma_f32 v[78:79], v[74:75], s[22:23], v[90:91] op_sel_hi:[1,0,0]
	v_exp_f32_e32 v76, v53
	v_pk_fma_f32 v[78:79], v[74:75], v[78:79], s[24:25] op_sel_hi:[1,1,0]
	v_mul_f32_e32 v53, 0xbf38aa3b, v77
	v_pk_fma_f32 v[78:79], v[74:75], v[78:79], s[34:35] op_sel_hi:[1,1,0]
	v_pk_fma_f32 v[68:69], v[68:69], v[44:45], v[48:49]
	v_pk_fma_f32 v[78:79], v[74:75], v[78:79], s[40:41] op_sel_hi:[1,1,0]
	v_and_b32_e32 v73, 0x7fffffff, v71
	v_and_b32_e32 v72, 0x7fffffff, v70
	v_exp_f32_e32 v77, v53
	v_pk_mul_f32 v[74:75], v[74:75], v[78:79]
	v_fma_f32 v53, |v68|, s25, 1.0
	v_pk_mul_f32 v[72:73], v[72:73], v[74:75]
	v_rcp_f32_e32 v74, v53
	v_fma_f32 v53, |v69|, s25, 1.0
	v_rcp_f32_e32 v75, v53
	v_max_f32_e32 v70, 0, v70
	v_max_f32_e32 v71, 0, v71
	v_pk_fma_f32 v[70:71], v[76:77], v[72:73], v[70:71] neg_lo:[1,0,0] neg_hi:[1,0,0]
	v_pk_mul_f32 v[76:77], v[68:69], v[68:69]
	v_pk_fma_f32 v[78:79], v[74:75], s[22:23], v[90:91] op_sel_hi:[1,0,0]
	v_mul_f32_e32 v53, 0xbf38aa3b, v76
	v_exp_f32_e32 v76, v53
	v_pk_fma_f32 v[78:79], v[74:75], v[78:79], s[24:25] op_sel_hi:[1,1,0]
	v_mul_f32_e32 v53, 0xbf38aa3b, v77
	v_pk_fma_f32 v[78:79], v[74:75], v[78:79], s[34:35] op_sel_hi:[1,1,0]
	v_exp_f32_e32 v77, v53
	v_pk_fma_f32 v[78:79], v[74:75], v[78:79], s[40:41] op_sel_hi:[1,1,0]
	v_and_b32_e32 v73, 0x7fffffff, v69
	v_and_b32_e32 v72, 0x7fffffff, v68
	v_pk_mul_f32 v[74:75], v[74:75], v[78:79]
	v_readlane_b32 s0, v52, 4
	v_max_f32_e32 v68, 0, v68
	v_max_f32_e32 v69, 0, v69
	v_pk_mul_f32 v[72:73], v[72:73], v[74:75]
	v_pk_mul_f32 v[66:67], s[0:1], v[66:67] op_sel_hi:[0,1]
	v_pk_fma_f32 v[68:69], v[76:77], v[72:73], v[68:69] neg_lo:[1,0,0] neg_hi:[1,0,0]
	v_pk_fma_f32 v[66:67], v[66:67], v[42:43], v[46:47]
	v_cvt_pk_f16_f32 v70, v70, v71
	v_cvt_pk_f16_f32 v71, v68, v69
	v_fma_f32 v53, |v66|, s25, 1.0
	ds_write_b64 v134, v[70:71] offset:34304
	v_rcp_f32_e32 v70, v53
	v_fma_f32 v53, |v67|, s25, 1.0
	v_rcp_f32_e32 v71, v53
	v_pk_mul_f32 v[72:73], v[66:67], v[66:67]
	v_pk_mul_f32 v[64:65], s[0:1], v[64:65] op_sel_hi:[0,1]
	v_mul_f32_e32 v53, 0xbf38aa3b, v72
	v_pk_fma_f32 v[74:75], v[70:71], s[22:23], v[90:91] op_sel_hi:[1,0,0]
	v_exp_f32_e32 v72, v53
	v_pk_fma_f32 v[74:75], v[70:71], v[74:75], s[24:25] op_sel_hi:[1,1,0]
	v_mul_f32_e32 v53, 0xbf38aa3b, v73
	v_pk_fma_f32 v[74:75], v[70:71], v[74:75], s[34:35] op_sel_hi:[1,1,0]
	v_pk_fma_f32 v[64:65], v[64:65], v[44:45], v[48:49]
	v_pk_fma_f32 v[74:75], v[70:71], v[74:75], s[40:41] op_sel_hi:[1,1,0]
	v_and_b32_e32 v69, 0x7fffffff, v67
	v_and_b32_e32 v68, 0x7fffffff, v66
	v_exp_f32_e32 v73, v53
	v_pk_mul_f32 v[70:71], v[70:71], v[74:75]
	v_fma_f32 v53, |v64|, s25, 1.0
	v_pk_mul_f32 v[68:69], v[68:69], v[70:71]
	v_rcp_f32_e32 v70, v53
	v_fma_f32 v53, |v65|, s25, 1.0
	v_rcp_f32_e32 v71, v53
	v_max_f32_e32 v66, 0, v66
	v_max_f32_e32 v67, 0, v67
	v_pk_fma_f32 v[66:67], v[72:73], v[68:69], v[66:67] neg_lo:[1,0,0] neg_hi:[1,0,0]
	v_pk_mul_f32 v[72:73], v[64:65], v[64:65]
	v_pk_fma_f32 v[74:75], v[70:71], s[22:23], v[90:91] op_sel_hi:[1,0,0]
	v_mul_f32_e32 v53, 0xbf38aa3b, v72
	v_exp_f32_e32 v72, v53
	v_pk_fma_f32 v[74:75], v[70:71], v[74:75], s[24:25] op_sel_hi:[1,1,0]
	v_mul_f32_e32 v53, 0xbf38aa3b, v73
	v_pk_fma_f32 v[74:75], v[70:71], v[74:75], s[34:35] op_sel_hi:[1,1,0]
	v_exp_f32_e32 v73, v53
	v_pk_fma_f32 v[74:75], v[70:71], v[74:75], s[40:41] op_sel_hi:[1,1,0]
	v_and_b32_e32 v69, 0x7fffffff, v65
	v_and_b32_e32 v68, 0x7fffffff, v64
	v_pk_mul_f32 v[70:71], v[70:71], v[74:75]
	v_readlane_b32 s0, v52, 5
	v_max_f32_e32 v64, 0, v64
	v_max_f32_e32 v65, 0, v65
	v_pk_mul_f32 v[68:69], v[68:69], v[70:71]
	v_pk_mul_f32 v[62:63], s[0:1], v[62:63] op_sel_hi:[0,1]
	v_pk_fma_f32 v[64:65], v[72:73], v[68:69], v[64:65] neg_lo:[1,0,0] neg_hi:[1,0,0]
	v_pk_fma_f32 v[62:63], v[62:63], v[42:43], v[46:47]
	v_cvt_pk_f16_f32 v66, v66, v67
	v_cvt_pk_f16_f32 v67, v64, v65
	v_fma_f32 v53, |v62|, s25, 1.0
	ds_write_b64 v120, v[66:67] offset:34816
	v_rcp_f32_e32 v66, v53
	v_fma_f32 v53, |v63|, s25, 1.0
	v_rcp_f32_e32 v67, v53
	v_pk_mul_f32 v[68:69], v[62:63], v[62:63]
	v_pk_mul_f32 v[60:61], s[0:1], v[60:61] op_sel_hi:[0,1]
	v_mul_f32_e32 v53, 0xbf38aa3b, v68
	v_pk_fma_f32 v[70:71], v[66:67], s[22:23], v[90:91] op_sel_hi:[1,0,0]
	v_exp_f32_e32 v68, v53
	v_pk_fma_f32 v[70:71], v[66:67], v[70:71], s[24:25] op_sel_hi:[1,1,0]
	v_mul_f32_e32 v53, 0xbf38aa3b, v69
	v_pk_fma_f32 v[70:71], v[66:67], v[70:71], s[34:35] op_sel_hi:[1,1,0]
	v_pk_fma_f32 v[60:61], v[60:61], v[44:45], v[48:49]
	v_pk_fma_f32 v[70:71], v[66:67], v[70:71], s[40:41] op_sel_hi:[1,1,0]
	v_and_b32_e32 v65, 0x7fffffff, v63
	v_and_b32_e32 v64, 0x7fffffff, v62
	v_exp_f32_e32 v69, v53
	v_pk_mul_f32 v[66:67], v[66:67], v[70:71]
	v_fma_f32 v53, |v60|, s25, 1.0
	v_pk_mul_f32 v[64:65], v[64:65], v[66:67]
	v_rcp_f32_e32 v66, v53
	v_fma_f32 v53, |v61|, s25, 1.0
	v_rcp_f32_e32 v67, v53
	v_max_f32_e32 v62, 0, v62
	v_max_f32_e32 v63, 0, v63
	v_pk_fma_f32 v[62:63], v[68:69], v[64:65], v[62:63] neg_lo:[1,0,0] neg_hi:[1,0,0]
	v_pk_mul_f32 v[68:69], v[60:61], v[60:61]
	v_pk_fma_f32 v[70:71], v[66:67], s[22:23], v[90:91] op_sel_hi:[1,0,0]
	v_mul_f32_e32 v53, 0xbf38aa3b, v68
	v_exp_f32_e32 v68, v53
	v_pk_fma_f32 v[70:71], v[66:67], v[70:71], s[24:25] op_sel_hi:[1,1,0]
	v_mul_f32_e32 v53, 0xbf38aa3b, v69
	v_pk_fma_f32 v[70:71], v[66:67], v[70:71], s[34:35] op_sel_hi:[1,1,0]
	v_exp_f32_e32 v69, v53
	v_pk_fma_f32 v[70:71], v[66:67], v[70:71], s[40:41] op_sel_hi:[1,1,0]
	v_and_b32_e32 v65, 0x7fffffff, v61
	v_and_b32_e32 v64, 0x7fffffff, v60
	v_pk_mul_f32 v[66:67], v[66:67], v[70:71]
	v_readlane_b32 s0, v52, 6
	v_max_f32_e32 v60, 0, v60
	v_max_f32_e32 v61, 0, v61
	v_pk_mul_f32 v[64:65], v[64:65], v[66:67]
	v_pk_mul_f32 v[58:59], s[0:1], v[58:59] op_sel_hi:[0,1]
	v_pk_fma_f32 v[60:61], v[68:69], v[64:65], v[60:61] neg_lo:[1,0,0] neg_hi:[1,0,0]
	v_pk_fma_f32 v[58:59], v[58:59], v[42:43], v[46:47]
	v_cvt_pk_f16_f32 v62, v62, v63
	v_cvt_pk_f16_f32 v63, v60, v61
	v_fma_f32 v53, |v58|, s25, 1.0
	ds_write_b64 v121, v[62:63] offset:35328
	v_rcp_f32_e32 v62, v53
	v_fma_f32 v53, |v59|, s25, 1.0
	v_rcp_f32_e32 v63, v53
	v_pk_mul_f32 v[64:65], v[58:59], v[58:59]
	v_pk_mul_f32 v[56:57], s[0:1], v[56:57] op_sel_hi:[0,1]
	v_mul_f32_e32 v53, 0xbf38aa3b, v64
	v_pk_fma_f32 v[66:67], v[62:63], s[22:23], v[90:91] op_sel_hi:[1,0,0]
	v_exp_f32_e32 v64, v53
	v_pk_fma_f32 v[66:67], v[62:63], v[66:67], s[24:25] op_sel_hi:[1,1,0]
	v_mul_f32_e32 v53, 0xbf38aa3b, v65
	v_pk_fma_f32 v[66:67], v[62:63], v[66:67], s[34:35] op_sel_hi:[1,1,0]
	v_pk_fma_f32 v[56:57], v[56:57], v[44:45], v[48:49]
	v_pk_fma_f32 v[66:67], v[62:63], v[66:67], s[40:41] op_sel_hi:[1,1,0]
	v_and_b32_e32 v61, 0x7fffffff, v59
	v_and_b32_e32 v60, 0x7fffffff, v58
	v_exp_f32_e32 v65, v53
	v_pk_mul_f32 v[62:63], v[62:63], v[66:67]
	v_fma_f32 v53, |v56|, s25, 1.0
	v_pk_mul_f32 v[60:61], v[60:61], v[62:63]
	v_rcp_f32_e32 v62, v53
	v_fma_f32 v53, |v57|, s25, 1.0
	v_rcp_f32_e32 v63, v53
	v_max_f32_e32 v58, 0, v58
	v_max_f32_e32 v59, 0, v59
	v_pk_fma_f32 v[58:59], v[64:65], v[60:61], v[58:59] neg_lo:[1,0,0] neg_hi:[1,0,0]
	v_pk_mul_f32 v[64:65], v[56:57], v[56:57]
	v_pk_fma_f32 v[66:67], v[62:63], s[22:23], v[90:91] op_sel_hi:[1,0,0]
	v_mul_f32_e32 v53, 0xbf38aa3b, v64
	v_exp_f32_e32 v64, v53
	v_pk_fma_f32 v[66:67], v[62:63], v[66:67], s[24:25] op_sel_hi:[1,1,0]
	v_mul_f32_e32 v53, 0xbf38aa3b, v65
	v_pk_fma_f32 v[66:67], v[62:63], v[66:67], s[34:35] op_sel_hi:[1,1,0]
	v_exp_f32_e32 v65, v53
	v_pk_fma_f32 v[66:67], v[62:63], v[66:67], s[40:41] op_sel_hi:[1,1,0]
	v_and_b32_e32 v61, 0x7fffffff, v57
	v_and_b32_e32 v60, 0x7fffffff, v56
	v_pk_mul_f32 v[62:63], v[62:63], v[66:67]
	v_readlane_b32 s0, v52, 7
	v_max_f32_e32 v56, 0, v56
	v_max_f32_e32 v57, 0, v57
	v_pk_mul_f32 v[60:61], v[60:61], v[62:63]
	v_pk_mul_f32 v[52:53], s[0:1], v[54:55] op_sel_hi:[0,1]
	v_pk_fma_f32 v[56:57], v[64:65], v[60:61], v[56:57] neg_lo:[1,0,0] neg_hi:[1,0,0]
	v_pk_fma_f32 v[52:53], v[52:53], v[42:43], v[46:47]
	v_cvt_pk_f16_f32 v58, v58, v59
	v_cvt_pk_f16_f32 v59, v56, v57
	v_fma_f32 v56, |v52|, s25, 1.0
	v_fma_f32 v57, |v53|, s25, 1.0
	v_rcp_f32_e32 v56, v56
	v_rcp_f32_e32 v57, v57
	ds_write_b64 v118, v[58:59] offset:35840
	v_pk_mul_f32 v[58:59], v[52:53], v[52:53]
	v_and_b32_e32 v55, 0x7fffffff, v53
	v_pk_fma_f32 v[60:61], v[56:57], s[22:23], v[90:91] op_sel_hi:[1,0,0]
	v_mul_f32_e32 v58, 0xbf38aa3b, v58
	v_pk_fma_f32 v[60:61], v[56:57], v[60:61], s[24:25] op_sel_hi:[1,1,0]
	v_mul_f32_e32 v59, 0xbf38aa3b, v59
	v_exp_f32_e32 v58, v58
	v_pk_fma_f32 v[60:61], v[56:57], v[60:61], s[34:35] op_sel_hi:[1,1,0]
	v_exp_f32_e32 v59, v59
	v_pk_fma_f32 v[60:61], v[56:57], v[60:61], s[40:41] op_sel_hi:[1,1,0]
	v_and_b32_e32 v54, 0x7fffffff, v52
	v_pk_mul_f32 v[56:57], v[56:57], v[60:61]
	v_max_f32_e32 v52, 0, v52
	v_max_f32_e32 v53, 0, v53
	v_pk_mul_f32 v[54:55], v[54:55], v[56:57]
	v_pk_mul_f32 v[50:51], s[0:1], v[50:51] op_sel_hi:[0,1]
	v_pk_fma_f32 v[52:53], v[58:59], v[54:55], v[52:53] neg_lo:[1,0,0] neg_hi:[1,0,0]
	v_pk_fma_f32 v[50:51], v[50:51], v[44:45], v[48:49]
	v_cvt_pk_f16_f32 v52, v52, v53
	v_fma_f32 v53, |v50|, s25, 1.0
	v_rcp_f32_e32 v56, v53
	v_fma_f32 v53, |v51|, s25, 1.0
	v_rcp_f32_e32 v57, v53
	v_pk_mul_f32 v[58:59], v[50:51], v[50:51]
	v_and_b32_e32 v55, 0x7fffffff, v51
	v_mul_f32_e32 v53, 0xbf38aa3b, v58
	v_pk_fma_f32 v[60:61], v[56:57], s[22:23], v[90:91] op_sel_hi:[1,0,0]
	v_exp_f32_e32 v58, v53
	v_pk_fma_f32 v[60:61], v[56:57], v[60:61], s[24:25] op_sel_hi:[1,1,0]
	v_mul_f32_e32 v53, 0xbf38aa3b, v59
	v_pk_fma_f32 v[60:61], v[56:57], v[60:61], s[34:35] op_sel_hi:[1,1,0]
	v_exp_f32_e32 v59, v53
	v_pk_fma_f32 v[60:61], v[56:57], v[60:61], s[40:41] op_sel_hi:[1,1,0]
	v_and_b32_e32 v54, 0x7fffffff, v50
	v_pk_mul_f32 v[56:57], v[56:57], v[60:61]
	v_max_f32_e32 v50, 0, v50
	v_max_f32_e32 v51, 0, v51
	v_pk_mul_f32 v[54:55], v[54:55], v[56:57]
	s_movk_i32 s0, 0x70
	v_pk_fma_f32 v[50:51], v[58:59], v[54:55], v[50:51] neg_lo:[1,0,0] neg_hi:[1,0,0]
	v_add_f32_e32 v96, v24, v25
	v_cvt_pk_f16_f32 v53, v50, v51
	v_bitop3_b32 v50, v86, s0, v88 bitop3:0x6c
	s_movk_i32 s0, 0x4000
	v_add_co_u32_e32 v92, vcc, s0, v82
	s_movk_i32 s0, 0x5000
	s_nop 0
	v_addc_co_u32_e32 v93, vcc, 0, v83, vcc
	v_or3_b32 v144, v85, v50, v87
	v_add_co_u32_e32 v94, vcc, s0, v82
	ds_write_b64 v144, v[52:53] offset:36352
	s_nop 0
	v_addc_co_u32_e32 v95, vcc, 0, v83, vcc
	global_load_dwordx4 v[78:81], v[94:95], off offset:-4096 nt
	global_load_dwordx4 v[74:77], v[92:93], off offset:1024 nt
	global_load_dwordx4 v[70:73], v[92:93], off offset:2048 nt
	global_load_dwordx4 v[66:69], v[92:93], off offset:3072 nt
	global_load_dwordx4 v[62:65], v[94:95], off nt
	global_load_dwordx4 v[58:61], v[94:95], off offset:1024 nt
	global_load_dwordx4 v[54:57], v[94:95], off offset:2048 nt
	global_load_dwordx4 v[50:53], v[94:95], off offset:3072 nt
	v_add_f32_e32 v92, v40, v41
	v_add_f32_e32 v89, v89, v92
	v_add_f32_e32 v92, v34, v35
	v_add_f32_e32 v93, v36, v37
	v_add_f32_e32 v92, v92, v93
	v_add_f32_e32 v93, v30, v31
	v_add_f32_e32 v94, v32, v33
	v_add_f32_e32 v93, v93, v94
	v_add_f32_e32 v94, v26, v27
	v_add_f32_e32 v95, v28, v29
	v_add_f32_e32 v94, v94, v95
	v_add_f32_e32 v95, v22, v23
	v_add_f32_e32 v95, v95, v96
	v_add_f32_e32 v96, v18, v19
	v_add_f32_e32 v97, v20, v21
	v_add_f32_e32 v96, v96, v97
	v_add_f32_e32 v97, v14, v15
	v_add_f32_e32 v98, v16, v17
	v_add_f32_e32 v97, v97, v98
	v_add_f32_e32 v98, v10, v11
	v_add_f32_e32 v99, v12, v13
	v_add_f32_e32 v98, v98, v99
	v_cndmask_b32_e64 v99, v92, v89, s[4:5]
	v_cndmask_b32_e64 v89, v89, v92, s[4:5]
	v_cndmask_b32_e64 v92, v94, v93, s[4:5]
	v_cndmask_b32_e64 v93, v93, v94, s[4:5]
	v_cndmask_b32_e64 v94, v95, v96, s[4:5]
	v_add_f32_dpp v89, v99, v89 quad_perm:[1,0,3,2] row_mask:0xf bank_mask:0xf bound_ctrl:1
	v_add_f32_dpp v92, v92, v93 quad_perm:[1,0,3,2] row_mask:0xf bank_mask:0xf bound_ctrl:1
	v_cndmask_b32_e64 v93, v96, v95, s[4:5]
	v_cndmask_b32_e64 v95, v97, v98, s[4:5]
	s_movk_i32 s1, 0x80
	v_add_f32_dpp v93, v93, v94 quad_perm:[1,0,3,2] row_mask:0xf bank_mask:0xf bound_ctrl:1
	v_cndmask_b32_e64 v94, v98, v97, s[4:5]
	s_movk_i32 s23, 0x90
	s_nop 0
	v_add_f32_dpp v94, v94, v95 quad_perm:[1,0,3,2] row_mask:0xf bank_mask:0xf bound_ctrl:1
	v_cndmask_b32_e64 v95, v89, v92, s[6:7]
	v_cndmask_b32_e64 v89, v92, v89, s[6:7]
	v_cndmask_b32_e64 v92, v93, v94, s[6:7]
	v_cndmask_b32_e64 v93, v94, v93, s[6:7]
	v_add_f32_dpp v89, v95, v89 quad_perm:[2,3,0,1] row_mask:0xf bank_mask:0xf bound_ctrl:1
	s_nop 0
	v_add_f32_dpp v92, v92, v93 quad_perm:[2,3,0,1] row_mask:0xf bank_mask:0xf bound_ctrl:1
	v_cndmask_b32_e64 v93, v89, v92, s[8:9]
	v_cndmask_b32_e64 v89, v92, v89, s[8:9]
	v_mov_b32_e32 v92, v93
	s_nop 1
	v_mov_b32_dpp v92, v92 row_shl:4 row_mask:0xf bank_mask:0x5
	s_nop 1
	v_mov_b32_dpp v92, v93 row_shr:4 row_mask:0xf bank_mask:0xa
	v_add_f32_e32 v89, v89, v92
	s_nop 1
	v_add_f32_dpp v89, v89, v89 row_ror:8 row_mask:0xf bank_mask:0xf bound_ctrl:1
	v_mov_b32_e32 v92, v89
	s_nop 1
	v_permlane16_swap_b32_e32 v89, v92
	v_add_f32_e32 v89, v89, v92
	v_mov_b32_e32 v92, v89
	s_nop 1
	v_permlane32_swap_b32_e32 v89, v92
	v_add_f32_e32 v89, v89, v92
	v_mul_f32_e32 v89, 0x3b800000, v89
	v_bitop3_b32 v92, v86, s1, v88 bitop3:0x6c
	v_readlane_b32 s44, v89, 0
	v_readlane_b32 s46, v89, 1
	v_readlane_b32 s48, v89, 2
	v_pk_add_f32 v[40:41], v[40:41], s[44:45] op_sel_hi:[1,0] neg_lo:[0,1] neg_hi:[0,1]
	v_pk_add_f32 v[36:37], v[36:37], s[46:47] op_sel_hi:[1,0] neg_lo:[0,1] neg_hi:[0,1]
	v_readlane_b32 s50, v89, 3
	v_readlane_b32 s52, v89, 4
	v_readlane_b32 s54, v89, 5
	v_readlane_b32 s42, v89, 6
	v_readlane_b32 s0, v89, 7
	v_mul_f32_e32 v89, v41, v41
	v_or3_b32 v145, v85, v92, v87
	v_pk_add_f32 v[92:93], v[34:35], s[46:47] op_sel_hi:[1,0] neg_lo:[0,1] neg_hi:[0,1]
	v_mul_f32_e32 v34, v37, v37
	v_pk_add_f32 v[38:39], v[38:39], s[44:45] op_sel_hi:[1,0] neg_lo:[0,1] neg_hi:[0,1]
	v_fmac_f32_e32 v89, v40, v40
	v_fmac_f32_e32 v34, v36, v36
	v_fmac_f32_e32 v89, v39, v39
	v_fmac_f32_e32 v34, v93, v93
	v_fmac_f32_e32 v89, v38, v38
	v_fmac_f32_e32 v34, v92, v92
	v_cndmask_b32_e64 v35, v34, v89, s[4:5]
	v_cndmask_b32_e64 v34, v89, v34, s[4:5]
	s_movk_i32 s1, 0xa0
	v_pk_add_f32 v[32:33], v[32:33], s[48:49] op_sel_hi:[1,0] neg_lo:[0,1] neg_hi:[0,1]
	v_add_f32_dpp v89, v35, v34 quad_perm:[1,0,3,2] row_mask:0xf bank_mask:0xf bound_ctrl:1
	v_bitop3_b32 v34, v86, s23, v88 bitop3:0x6c
	v_or3_b32 v139, v85, v34, v87
	v_pk_add_f32 v[34:35], v[30:31], s[48:49] op_sel_hi:[1,0] neg_lo:[0,1] neg_hi:[0,1]
	v_bitop3_b32 v30, v86, s1, v88 bitop3:0x6c
	v_pk_add_f32 v[28:29], v[28:29], s[50:51] op_sel_hi:[1,0] neg_lo:[0,1] neg_hi:[0,1]
	v_mul_f32_e32 v94, v33, v33
	v_or3_b32 v137, v85, v30, v87
	v_pk_add_f32 v[30:31], v[26:27], s[50:51] op_sel_hi:[1,0] neg_lo:[0,1] neg_hi:[0,1]
	v_mul_f32_e32 v26, v29, v29
	v_fmac_f32_e32 v94, v32, v32
	v_fmac_f32_e32 v26, v28, v28
	v_fmac_f32_e32 v94, v35, v35
	v_fmac_f32_e32 v26, v31, v31
	v_fmac_f32_e32 v94, v34, v34
	v_fmac_f32_e32 v26, v30, v30
	v_cndmask_b32_e64 v27, v26, v94, s[4:5]
	v_cndmask_b32_e64 v26, v94, v26, s[4:5]
	s_movk_i32 s1, 0xb0
	v_pk_add_f32 v[24:25], v[24:25], s[52:53] op_sel_hi:[1,0] neg_lo:[0,1] neg_hi:[0,1]
	v_add_f32_dpp v26, v27, v26 quad_perm:[1,0,3,2] row_mask:0xf bank_mask:0xf bound_ctrl:1
	v_cndmask_b32_e64 v27, v89, v26, s[6:7]
	v_cndmask_b32_e64 v26, v26, v89, s[6:7]
	v_pk_add_f32 v[20:21], v[20:21], s[54:55] op_sel_hi:[1,0] neg_lo:[0,1] neg_hi:[0,1]
	v_mul_f32_e32 v94, v25, v25
	v_add_f32_dpp v89, v27, v26 quad_perm:[2,3,0,1] row_mask:0xf bank_mask:0xf bound_ctrl:1
	v_bitop3_b32 v26, v86, s1, v88 bitop3:0x6c
	s_movk_i32 s1, 0xc0
	v_or3_b32 v136, v85, v26, v87
	v_pk_add_f32 v[26:27], v[22:23], s[52:53] op_sel_hi:[1,0] neg_lo:[0,1] neg_hi:[0,1]
	v_bitop3_b32 v22, v86, s1, v88 bitop3:0x6c
	v_or3_b32 v123, v85, v22, v87
	v_pk_add_f32 v[22:23], v[18:19], s[54:55] op_sel_hi:[1,0] neg_lo:[0,1] neg_hi:[0,1]
	v_mul_f32_e32 v18, v21, v21
	v_fmac_f32_e32 v94, v24, v24
	v_fmac_f32_e32 v18, v20, v20
	v_fmac_f32_e32 v94, v27, v27
	v_fmac_f32_e32 v18, v23, v23
	v_fmac_f32_e32 v94, v26, v26
	v_fmac_f32_e32 v18, v22, v22
	v_cndmask_b32_e64 v19, v18, v94, s[4:5]
	v_cndmask_b32_e64 v18, v94, v18, s[4:5]
	v_pk_add_f32 v[16:17], v[16:17], s[42:43] op_sel_hi:[1,0] neg_lo:[0,1] neg_hi:[0,1]
	s_nop 0
	v_add_f32_dpp v94, v19, v18 quad_perm:[1,0,3,2] row_mask:0xf bank_mask:0xf bound_ctrl:1
	v_pk_add_f32 v[18:19], v[14:15], s[42:43] op_sel_hi:[1,0] neg_lo:[0,1] neg_hi:[0,1]
	v_pk_add_f32 v[14:15], v[10:11], s[0:1] op_sel_hi:[1,0] neg_lo:[0,1] neg_hi:[0,1]
	v_pk_add_f32 v[10:11], v[12:13], s[0:1] op_sel_hi:[1,0] neg_lo:[0,1] neg_hi:[0,1]
	v_mul_f32_e32 v95, v17, v17
	v_mul_f32_e32 v12, v11, v11
	v_fmac_f32_e32 v95, v16, v16
	v_fmac_f32_e32 v12, v10, v10
	v_fmac_f32_e32 v95, v19, v19
	v_fmac_f32_e32 v12, v15, v15
	v_fmac_f32_e32 v95, v18, v18
	v_fmac_f32_e32 v12, v14, v14
	v_cndmask_b32_e64 v13, v12, v95, s[4:5]
	v_cndmask_b32_e64 v12, v95, v12, s[4:5]
	s_movk_i32 s0, 0xd0
	s_nop 0
	v_add_f32_dpp v12, v13, v12 quad_perm:[1,0,3,2] row_mask:0xf bank_mask:0xf bound_ctrl:1
	v_cndmask_b32_e64 v13, v94, v12, s[6:7]
	v_cndmask_b32_e64 v12, v12, v94, s[6:7]
	s_nop 1
	v_add_f32_dpp v12, v13, v12 quad_perm:[2,3,0,1] row_mask:0xf bank_mask:0xf bound_ctrl:1
	v_cndmask_b32_e64 v13, v89, v12, s[8:9]
	v_cndmask_b32_e64 v12, v12, v89, s[8:9]
	v_mov_b32_e32 v89, v13
	s_nop 1
	v_mov_b32_dpp v89, v89 row_shl:4 row_mask:0xf bank_mask:0x5
	s_nop 1
	v_mov_b32_dpp v89, v13 row_shr:4 row_mask:0xf bank_mask:0xa
	v_add_f32_e32 v12, v12, v89
	v_bitop3_b32 v89, v86, s0, v88 bitop3:0x6c
	v_or3_b32 v133, v85, v89, v87
	v_add_f32_dpp v12, v12, v12 row_ror:8 row_mask:0xf bank_mask:0xf bound_ctrl:1
	v_mov_b32_e32 v13, v12
	s_nop 1
	v_permlane16_swap_b32_e32 v12, v13
	v_add_f32_e32 v12, v12, v13
	v_mov_b32_e32 v13, v12
	s_nop 1
	v_permlane32_swap_b32_e32 v12, v13
	v_add_f32_e32 v12, v12, v13
	v_fmamk_f32 v12, v12, 0x3b800000, v116
	v_mul_f32_e32 v13, 0x4f800000, v12
	v_cmp_gt_f32_e32 vcc, s35, v12
	s_nop 1
	v_cndmask_b32_e32 v12, v12, v13, vcc
	v_sqrt_f32_e32 v13, v12
	s_nop 0
	v_add_u32_e32 v89, -1, v13
	v_fma_f32 v94, -v89, v13, v12
	v_cmp_ge_f32_e64 s[0:1], 0, v94
	v_add_u32_e32 v94, 1, v13
	s_nop 0
	v_cndmask_b32_e64 v89, v13, v89, s[0:1]
	v_fma_f32 v13, -v94, v13, v12
	v_cmp_lt_f32_e64 s[0:1], 0, v13
	s_nop 1
	v_cndmask_b32_e64 v13, v89, v94, s[0:1]
	v_mul_f32_e32 v89, 0x37800000, v13
	v_cndmask_b32_e32 v13, v13, v89, vcc
	v_cmp_class_f32_e32 vcc, v12, v117
	s_nop 1
	v_cndmask_b32_e32 v12, v13, v12, vcc
	v_div_scale_f32 v13, s[0:1], v12, v12, 1.0
	v_rcp_f32_e32 v89, v13
	s_movk_i32 s0, 0xe0
	v_bitop3_b32 v94, v86, s0, v88 bitop3:0x6c
	v_or3_b32 v119, v85, v94, v87
	v_fma_f32 v94, -v13, v89, 1.0
	v_fmac_f32_e32 v89, v94, v89
	v_div_scale_f32 v94, vcc, 1.0, v12, 1.0
	v_mul_f32_e32 v95, v94, v89
	v_fma_f32 v96, -v13, v95, v94
	v_fmac_f32_e32 v95, v96, v89
	v_fma_f32 v13, -v13, v95, v94
	v_div_fmas_f32 v13, v13, v89, v95
	v_div_fixup_f32 v12, v13, v12, 1.0
	s_nop 0
	v_readlane_b32 s0, v12, 0
	s_nop 1
	v_pk_mul_f32 v[38:39], s[0:1], v[38:39] op_sel_hi:[0,1]
	v_pk_fma_f32 v[38:39], v[38:39], v[42:43], v[46:47]
	v_pk_mul_f32 v[40:41], s[0:1], v[40:41] op_sel_hi:[0,1]
	v_fma_f32 v13, |v38|, s25, 1.0
	v_rcp_f32_e32 v96, v13
	v_fma_f32 v13, |v39|, s25, 1.0
	v_rcp_f32_e32 v97, v13
	v_pk_mul_f32 v[98:99], v[38:39], v[38:39]
	v_pk_fma_f32 v[40:41], v[40:41], v[44:45], v[48:49]
	v_mul_f32_e32 v13, 0xbf38aa3b, v98
	v_pk_fma_f32 v[100:101], v[96:97], s[22:23], v[90:91] op_sel_hi:[1,0,0]
	v_exp_f32_e32 v98, v13
	v_pk_fma_f32 v[100:101], v[96:97], v[100:101], s[24:25] op_sel_hi:[1,1,0]
	v_mul_f32_e32 v13, 0xbf38aa3b, v99
	v_pk_fma_f32 v[100:101], v[96:97], v[100:101], s[34:35] op_sel_hi:[1,1,0]
	v_and_b32_e32 v95, 0x7fffffff, v39
	v_pk_fma_f32 v[100:101], v[96:97], v[100:101], s[40:41] op_sel_hi:[1,1,0]
	v_and_b32_e32 v94, 0x7fffffff, v38
	v_exp_f32_e32 v99, v13
	v_pk_mul_f32 v[96:97], v[96:97], v[100:101]
	v_fma_f32 v13, |v40|, s25, 1.0
	v_pk_mul_f32 v[94:95], v[94:95], v[96:97]
	v_rcp_f32_e32 v96, v13
	v_fma_f32 v13, |v41|, s25, 1.0
	v_rcp_f32_e32 v97, v13
	v_max_f32_e32 v38, 0, v38
	v_max_f32_e32 v39, 0, v39
	v_pk_fma_f32 v[38:39], v[98:99], v[94:95], v[38:39] neg_lo:[1,0,0] neg_hi:[1,0,0]
	v_pk_mul_f32 v[98:99], v[40:41], v[40:41]
	v_pk_fma_f32 v[100:101], v[96:97], s[22:23], v[90:91] op_sel_hi:[1,0,0]
	v_mul_f32_e32 v13, 0xbf38aa3b, v98
	v_exp_f32_e32 v98, v13
	v_pk_fma_f32 v[100:101], v[96:97], v[100:101], s[24:25] op_sel_hi:[1,1,0]
	v_mul_f32_e32 v13, 0xbf38aa3b, v99
	v_pk_fma_f32 v[100:101], v[96:97], v[100:101], s[34:35] op_sel_hi:[1,1,0]
	v_exp_f32_e32 v99, v13
	v_pk_fma_f32 v[100:101], v[96:97], v[100:101], s[40:41] op_sel_hi:[1,1,0]
	v_and_b32_e32 v95, 0x7fffffff, v41
	v_and_b32_e32 v94, 0x7fffffff, v40
	v_pk_mul_f32 v[96:97], v[96:97], v[100:101]
	v_max_f32_e32 v40, 0, v40
	v_max_f32_e32 v41, 0, v41
	v_pk_mul_f32 v[94:95], v[94:95], v[96:97]
	v_cvt_pk_f16_f32 v38, v38, v39
	v_pk_fma_f32 v[40:41], v[98:99], v[94:95], v[40:41] neg_lo:[1,0,0] neg_hi:[1,0,0]
	v_readlane_b32 s0, v12, 1
	v_cvt_pk_f16_f32 v39, v40, v41
	ds_write_b64 v145, v[38:39] offset:36864
	v_pk_mul_f32 v[38:39], s[0:1], v[92:93] op_sel_hi:[0,1]
	v_pk_fma_f32 v[38:39], v[38:39], v[42:43], v[46:47]
	v_pk_mul_f32 v[36:37], s[0:1], v[36:37] op_sel_hi:[0,1]
	v_fma_f32 v13, |v38|, s25, 1.0
	v_rcp_f32_e32 v92, v13
	v_fma_f32 v13, |v39|, s25, 1.0
	v_rcp_f32_e32 v93, v13
	v_pk_mul_f32 v[94:95], v[38:39], v[38:39]
	v_pk_fma_f32 v[36:37], v[36:37], v[44:45], v[48:49]
	v_mul_f32_e32 v13, 0xbf38aa3b, v94
	v_pk_fma_f32 v[96:97], v[92:93], s[22:23], v[90:91] op_sel_hi:[1,0,0]
	v_exp_f32_e32 v94, v13
	v_pk_fma_f32 v[96:97], v[92:93], v[96:97], s[24:25] op_sel_hi:[1,1,0]
	v_mul_f32_e32 v13, 0xbf38aa3b, v95
	v_pk_fma_f32 v[96:97], v[92:93], v[96:97], s[34:35] op_sel_hi:[1,1,0]
	v_and_b32_e32 v41, 0x7fffffff, v39
	v_pk_fma_f32 v[96:97], v[92:93], v[96:97], s[40:41] op_sel_hi:[1,1,0]
	v_and_b32_e32 v40, 0x7fffffff, v38
	v_exp_f32_e32 v95, v13
	v_pk_mul_f32 v[92:93], v[92:93], v[96:97]
	v_fma_f32 v13, |v36|, s25, 1.0
	v_pk_mul_f32 v[40:41], v[40:41], v[92:93]
	v_rcp_f32_e32 v92, v13
	v_fma_f32 v13, |v37|, s25, 1.0
	v_rcp_f32_e32 v93, v13
	v_max_f32_e32 v38, 0, v38
	v_max_f32_e32 v39, 0, v39
	v_pk_fma_f32 v[38:39], v[94:95], v[40:41], v[38:39] neg_lo:[1,0,0] neg_hi:[1,0,0]
	v_pk_mul_f32 v[94:95], v[36:37], v[36:37]
	v_pk_fma_f32 v[96:97], v[92:93], s[22:23], v[90:91] op_sel_hi:[1,0,0]
	v_mul_f32_e32 v13, 0xbf38aa3b, v94
	v_exp_f32_e32 v94, v13
	v_pk_fma_f32 v[96:97], v[92:93], v[96:97], s[24:25] op_sel_hi:[1,1,0]
	v_mul_f32_e32 v13, 0xbf38aa3b, v95
	v_pk_fma_f32 v[96:97], v[92:93], v[96:97], s[34:35] op_sel_hi:[1,1,0]
	v_exp_f32_e32 v95, v13
	v_pk_fma_f32 v[96:97], v[92:93], v[96:97], s[40:41] op_sel_hi:[1,1,0]
	v_and_b32_e32 v41, 0x7fffffff, v37
	v_and_b32_e32 v40, 0x7fffffff, v36
	v_pk_mul_f32 v[92:93], v[92:93], v[96:97]
	v_readlane_b32 s0, v12, 2
	v_max_f32_e32 v36, 0, v36
	v_max_f32_e32 v37, 0, v37
	v_pk_mul_f32 v[40:41], v[40:41], v[92:93]
	v_pk_mul_f32 v[34:35], s[0:1], v[34:35] op_sel_hi:[0,1]
	v_pk_fma_f32 v[36:37], v[94:95], v[40:41], v[36:37] neg_lo:[1,0,0] neg_hi:[1,0,0]
	v_pk_fma_f32 v[34:35], v[34:35], v[42:43], v[46:47]
	v_cvt_pk_f16_f32 v38, v38, v39
	v_cvt_pk_f16_f32 v39, v36, v37
	v_fma_f32 v13, |v34|, s25, 1.0
	ds_write_b64 v139, v[38:39] offset:37376
	v_rcp_f32_e32 v38, v13
	v_fma_f32 v13, |v35|, s25, 1.0
	v_rcp_f32_e32 v39, v13
	v_pk_mul_f32 v[40:41], v[34:35], v[34:35]
	v_pk_mul_f32 v[32:33], s[0:1], v[32:33] op_sel_hi:[0,1]
	v_mul_f32_e32 v13, 0xbf38aa3b, v40
	v_pk_fma_f32 v[92:93], v[38:39], s[22:23], v[90:91] op_sel_hi:[1,0,0]
	v_exp_f32_e32 v40, v13
	v_pk_fma_f32 v[92:93], v[38:39], v[92:93], s[24:25] op_sel_hi:[1,1,0]
	v_mul_f32_e32 v13, 0xbf38aa3b, v41
	v_pk_fma_f32 v[92:93], v[38:39], v[92:93], s[34:35] op_sel_hi:[1,1,0]
	v_pk_fma_f32 v[32:33], v[32:33], v[44:45], v[48:49]
	v_pk_fma_f32 v[92:93], v[38:39], v[92:93], s[40:41] op_sel_hi:[1,1,0]
	v_and_b32_e32 v37, 0x7fffffff, v35
	v_and_b32_e32 v36, 0x7fffffff, v34
	v_exp_f32_e32 v41, v13
	v_pk_mul_f32 v[38:39], v[38:39], v[92:93]
	v_fma_f32 v13, |v32|, s25, 1.0
	v_pk_mul_f32 v[36:37], v[36:37], v[38:39]
	v_rcp_f32_e32 v38, v13
	v_fma_f32 v13, |v33|, s25, 1.0
	v_rcp_f32_e32 v39, v13
	v_max_f32_e32 v34, 0, v34
	v_max_f32_e32 v35, 0, v35
	v_pk_fma_f32 v[34:35], v[40:41], v[36:37], v[34:35] neg_lo:[1,0,0] neg_hi:[1,0,0]
	v_pk_mul_f32 v[40:41], v[32:33], v[32:33]
	v_pk_fma_f32 v[92:93], v[38:39], s[22:23], v[90:91] op_sel_hi:[1,0,0]
	v_mul_f32_e32 v13, 0xbf38aa3b, v40
	v_exp_f32_e32 v40, v13
	v_pk_fma_f32 v[92:93], v[38:39], v[92:93], s[24:25] op_sel_hi:[1,1,0]
	v_mul_f32_e32 v13, 0xbf38aa3b, v41
	v_pk_fma_f32 v[92:93], v[38:39], v[92:93], s[34:35] op_sel_hi:[1,1,0]
	v_exp_f32_e32 v41, v13
	v_pk_fma_f32 v[92:93], v[38:39], v[92:93], s[40:41] op_sel_hi:[1,1,0]
	v_and_b32_e32 v37, 0x7fffffff, v33
	v_and_b32_e32 v36, 0x7fffffff, v32
	v_pk_mul_f32 v[38:39], v[38:39], v[92:93]
	v_readlane_b32 s0, v12, 3
	v_max_f32_e32 v32, 0, v32
	v_max_f32_e32 v33, 0, v33
	v_pk_mul_f32 v[36:37], v[36:37], v[38:39]
	v_pk_mul_f32 v[30:31], s[0:1], v[30:31] op_sel_hi:[0,1]
	v_pk_fma_f32 v[32:33], v[40:41], v[36:37], v[32:33] neg_lo:[1,0,0] neg_hi:[1,0,0]
	v_pk_fma_f32 v[30:31], v[30:31], v[42:43], v[46:47]
	v_cvt_pk_f16_f32 v34, v34, v35
	v_cvt_pk_f16_f32 v35, v32, v33
	v_fma_f32 v13, |v30|, s25, 1.0
	ds_write_b64 v137, v[34:35] offset:37888
	v_rcp_f32_e32 v34, v13
	v_fma_f32 v13, |v31|, s25, 1.0
	v_rcp_f32_e32 v35, v13
	v_pk_mul_f32 v[36:37], v[30:31], v[30:31]
	v_pk_mul_f32 v[28:29], s[0:1], v[28:29] op_sel_hi:[0,1]
	v_mul_f32_e32 v13, 0xbf38aa3b, v36
	v_pk_fma_f32 v[38:39], v[34:35], s[22:23], v[90:91] op_sel_hi:[1,0,0]
	v_exp_f32_e32 v36, v13
	v_pk_fma_f32 v[38:39], v[34:35], v[38:39], s[24:25] op_sel_hi:[1,1,0]
	v_mul_f32_e32 v13, 0xbf38aa3b, v37
	v_pk_fma_f32 v[38:39], v[34:35], v[38:39], s[34:35] op_sel_hi:[1,1,0]
	v_pk_fma_f32 v[28:29], v[28:29], v[44:45], v[48:49]
	v_pk_fma_f32 v[38:39], v[34:35], v[38:39], s[40:41] op_sel_hi:[1,1,0]
	v_and_b32_e32 v33, 0x7fffffff, v31
	v_and_b32_e32 v32, 0x7fffffff, v30
	v_exp_f32_e32 v37, v13
	v_pk_mul_f32 v[34:35], v[34:35], v[38:39]
	v_fma_f32 v13, |v28|, s25, 1.0
	v_pk_mul_f32 v[32:33], v[32:33], v[34:35]
	v_rcp_f32_e32 v34, v13
	v_fma_f32 v13, |v29|, s25, 1.0
	v_rcp_f32_e32 v35, v13
	v_max_f32_e32 v30, 0, v30
	v_max_f32_e32 v31, 0, v31
	v_pk_fma_f32 v[30:31], v[36:37], v[32:33], v[30:31] neg_lo:[1,0,0] neg_hi:[1,0,0]
	v_pk_mul_f32 v[36:37], v[28:29], v[28:29]
	v_pk_fma_f32 v[38:39], v[34:35], s[22:23], v[90:91] op_sel_hi:[1,0,0]
	v_mul_f32_e32 v13, 0xbf38aa3b, v36
	v_exp_f32_e32 v36, v13
	v_pk_fma_f32 v[38:39], v[34:35], v[38:39], s[24:25] op_sel_hi:[1,1,0]
	v_mul_f32_e32 v13, 0xbf38aa3b, v37
	v_pk_fma_f32 v[38:39], v[34:35], v[38:39], s[34:35] op_sel_hi:[1,1,0]
	v_exp_f32_e32 v37, v13
	v_pk_fma_f32 v[38:39], v[34:35], v[38:39], s[40:41] op_sel_hi:[1,1,0]
	v_and_b32_e32 v33, 0x7fffffff, v29
	v_and_b32_e32 v32, 0x7fffffff, v28
	v_pk_mul_f32 v[34:35], v[34:35], v[38:39]
	v_readlane_b32 s0, v12, 4
	v_max_f32_e32 v28, 0, v28
	v_max_f32_e32 v29, 0, v29
	v_pk_mul_f32 v[32:33], v[32:33], v[34:35]
	v_pk_mul_f32 v[26:27], s[0:1], v[26:27] op_sel_hi:[0,1]
	v_pk_fma_f32 v[28:29], v[36:37], v[32:33], v[28:29] neg_lo:[1,0,0] neg_hi:[1,0,0]
	v_pk_fma_f32 v[26:27], v[26:27], v[42:43], v[46:47]
	v_cvt_pk_f16_f32 v30, v30, v31
	v_cvt_pk_f16_f32 v31, v28, v29
	v_fma_f32 v13, |v26|, s25, 1.0
	ds_write_b64 v136, v[30:31] offset:38400
	v_rcp_f32_e32 v30, v13
	v_fma_f32 v13, |v27|, s25, 1.0
	v_rcp_f32_e32 v31, v13
	v_pk_mul_f32 v[32:33], v[26:27], v[26:27]
	v_pk_mul_f32 v[24:25], s[0:1], v[24:25] op_sel_hi:[0,1]
	v_mul_f32_e32 v13, 0xbf38aa3b, v32
	v_pk_fma_f32 v[34:35], v[30:31], s[22:23], v[90:91] op_sel_hi:[1,0,0]
	v_exp_f32_e32 v32, v13
	v_pk_fma_f32 v[34:35], v[30:31], v[34:35], s[24:25] op_sel_hi:[1,1,0]
	v_mul_f32_e32 v13, 0xbf38aa3b, v33
	v_pk_fma_f32 v[34:35], v[30:31], v[34:35], s[34:35] op_sel_hi:[1,1,0]
	v_pk_fma_f32 v[24:25], v[24:25], v[44:45], v[48:49]
	v_pk_fma_f32 v[34:35], v[30:31], v[34:35], s[40:41] op_sel_hi:[1,1,0]
	v_and_b32_e32 v29, 0x7fffffff, v27
	v_and_b32_e32 v28, 0x7fffffff, v26
	v_exp_f32_e32 v33, v13
	v_pk_mul_f32 v[30:31], v[30:31], v[34:35]
	v_fma_f32 v13, |v24|, s25, 1.0
	v_pk_mul_f32 v[28:29], v[28:29], v[30:31]
	v_rcp_f32_e32 v30, v13
	v_fma_f32 v13, |v25|, s25, 1.0
	v_rcp_f32_e32 v31, v13
	v_max_f32_e32 v26, 0, v26
	v_max_f32_e32 v27, 0, v27
	v_pk_fma_f32 v[26:27], v[32:33], v[28:29], v[26:27] neg_lo:[1,0,0] neg_hi:[1,0,0]
	v_pk_mul_f32 v[32:33], v[24:25], v[24:25]
	v_pk_fma_f32 v[34:35], v[30:31], s[22:23], v[90:91] op_sel_hi:[1,0,0]
	v_mul_f32_e32 v13, 0xbf38aa3b, v32
	v_exp_f32_e32 v32, v13
	v_pk_fma_f32 v[34:35], v[30:31], v[34:35], s[24:25] op_sel_hi:[1,1,0]
	v_mul_f32_e32 v13, 0xbf38aa3b, v33
	v_pk_fma_f32 v[34:35], v[30:31], v[34:35], s[34:35] op_sel_hi:[1,1,0]
	v_exp_f32_e32 v33, v13
	v_pk_fma_f32 v[34:35], v[30:31], v[34:35], s[40:41] op_sel_hi:[1,1,0]
	v_and_b32_e32 v29, 0x7fffffff, v25
	v_and_b32_e32 v28, 0x7fffffff, v24
	v_pk_mul_f32 v[30:31], v[30:31], v[34:35]
	v_readlane_b32 s0, v12, 5
	v_max_f32_e32 v24, 0, v24
	v_max_f32_e32 v25, 0, v25
	v_pk_mul_f32 v[28:29], v[28:29], v[30:31]
	v_pk_mul_f32 v[22:23], s[0:1], v[22:23] op_sel_hi:[0,1]
	v_pk_fma_f32 v[24:25], v[32:33], v[28:29], v[24:25] neg_lo:[1,0,0] neg_hi:[1,0,0]
	v_pk_fma_f32 v[22:23], v[22:23], v[42:43], v[46:47]
	v_cvt_pk_f16_f32 v26, v26, v27
	v_cvt_pk_f16_f32 v27, v24, v25
	v_fma_f32 v13, |v22|, s25, 1.0
	ds_write_b64 v123, v[26:27] offset:38912
	v_rcp_f32_e32 v26, v13
	v_fma_f32 v13, |v23|, s25, 1.0
	v_rcp_f32_e32 v27, v13
	v_pk_mul_f32 v[28:29], v[22:23], v[22:23]
	v_pk_mul_f32 v[20:21], s[0:1], v[20:21] op_sel_hi:[0,1]
	v_mul_f32_e32 v13, 0xbf38aa3b, v28
	v_pk_fma_f32 v[30:31], v[26:27], s[22:23], v[90:91] op_sel_hi:[1,0,0]
	v_exp_f32_e32 v28, v13
	v_pk_fma_f32 v[30:31], v[26:27], v[30:31], s[24:25] op_sel_hi:[1,1,0]
	v_mul_f32_e32 v13, 0xbf38aa3b, v29
	v_pk_fma_f32 v[30:31], v[26:27], v[30:31], s[34:35] op_sel_hi:[1,1,0]
	v_pk_fma_f32 v[20:21], v[20:21], v[44:45], v[48:49]
	v_pk_fma_f32 v[30:31], v[26:27], v[30:31], s[40:41] op_sel_hi:[1,1,0]
	s_waitcnt vmcnt(7)
	v_add_f32_e32 v92, v78, v79
	v_add_f32_e32 v93, v80, v81
	v_and_b32_e32 v25, 0x7fffffff, v23
	v_and_b32_e32 v24, 0x7fffffff, v22
	v_exp_f32_e32 v29, v13
	v_pk_mul_f32 v[26:27], v[26:27], v[30:31]
	v_fma_f32 v13, |v20|, s25, 1.0
	v_add_f32_e32 v92, v92, v93
	s_waitcnt vmcnt(6)
	v_add_f32_e32 v93, v74, v75
	v_add_f32_e32 v94, v76, v77
	v_pk_mul_f32 v[24:25], v[24:25], v[26:27]
	v_rcp_f32_e32 v26, v13
	v_fma_f32 v13, |v21|, s25, 1.0
	v_add_f32_e32 v93, v93, v94
	s_waitcnt vmcnt(5)
	v_add_f32_e32 v94, v70, v71
	v_add_f32_e32 v95, v72, v73
	v_rcp_f32_e32 v27, v13
	v_add_f32_e32 v94, v94, v95
	s_waitcnt vmcnt(4)
	v_add_f32_e32 v95, v66, v67
	v_add_f32_e32 v96, v68, v69
	v_add_f32_e32 v95, v95, v96
	s_waitcnt vmcnt(3)
	v_add_f32_e32 v96, v62, v63
	v_add_f32_e32 v97, v64, v65
	v_max_f32_e32 v22, 0, v22
	v_max_f32_e32 v23, 0, v23
	v_add_f32_e32 v96, v96, v97
	s_waitcnt vmcnt(2)
	v_add_f32_e32 v97, v58, v59
	v_add_f32_e32 v98, v60, v61
	v_pk_fma_f32 v[22:23], v[28:29], v[24:25], v[22:23] neg_lo:[1,0,0] neg_hi:[1,0,0]
	v_pk_mul_f32 v[28:29], v[20:21], v[20:21]
	v_add_f32_e32 v97, v97, v98
	s_waitcnt vmcnt(1)
	v_add_f32_e32 v98, v54, v55
	v_add_f32_e32 v99, v56, v57
	v_mul_f32_e32 v13, 0xbf38aa3b, v28
	v_pk_fma_f32 v[30:31], v[26:27], s[22:23], v[90:91] op_sel_hi:[1,0,0]
	v_add_f32_e32 v98, v98, v99
	s_waitcnt vmcnt(0)
	v_add_f32_e32 v99, v50, v51
	v_add_f32_e32 v100, v52, v53
	v_exp_f32_e32 v28, v13
	v_pk_fma_f32 v[30:31], v[26:27], v[30:31], s[24:25] op_sel_hi:[1,1,0]
	v_mul_f32_e32 v13, 0xbf38aa3b, v29
	v_add_f32_e32 v99, v99, v100
	v_cndmask_b32_e64 v100, v93, v92, s[4:5]
	v_cndmask_b32_e64 v92, v92, v93, s[4:5]
	v_cndmask_b32_e64 v93, v95, v94, s[4:5]
	v_cndmask_b32_e64 v94, v94, v95, s[4:5]
	v_pk_fma_f32 v[30:31], v[26:27], v[30:31], s[34:35] op_sel_hi:[1,1,0]
	v_exp_f32_e32 v29, v13
	v_add_f32_dpp v93, v93, v94 quad_perm:[1,0,3,2] row_mask:0xf bank_mask:0xf bound_ctrl:1
	v_cndmask_b32_e64 v94, v97, v96, s[4:5]
	v_cndmask_b32_e64 v95, v96, v97, s[4:5]
	v_pk_fma_f32 v[30:31], v[26:27], v[30:31], s[40:41] op_sel_hi:[1,1,0]
	v_cndmask_b32_e64 v96, v98, v99, s[4:5]
	v_add_f32_dpp v94, v94, v95 quad_perm:[1,0,3,2] row_mask:0xf bank_mask:0xf bound_ctrl:1
	v_cndmask_b32_e64 v95, v99, v98, s[4:5]
	v_and_b32_e32 v25, 0x7fffffff, v21
	v_and_b32_e32 v24, 0x7fffffff, v20
	v_pk_mul_f32 v[26:27], v[26:27], v[30:31]
	v_readlane_b32 s0, v12, 6
	v_add_f32_dpp v92, v100, v92 quad_perm:[1,0,3,2] row_mask:0xf bank_mask:0xf bound_ctrl:1
	v_add_f32_dpp v95, v95, v96 quad_perm:[1,0,3,2] row_mask:0xf bank_mask:0xf bound_ctrl:1
	v_max_f32_e32 v20, 0, v20
	v_max_f32_e32 v21, 0, v21
	v_pk_mul_f32 v[24:25], v[24:25], v[26:27]
	v_pk_mul_f32 v[18:19], s[0:1], v[18:19] op_sel_hi:[0,1]
	v_cndmask_b32_e64 v96, v92, v93, s[6:7]
	v_cndmask_b32_e64 v92, v93, v92, s[6:7]
	v_cndmask_b32_e64 v93, v94, v95, s[6:7]
	v_cndmask_b32_e64 v94, v95, v94, s[6:7]
	v_pk_fma_f32 v[20:21], v[28:29], v[24:25], v[20:21] neg_lo:[1,0,0] neg_hi:[1,0,0]
	v_pk_fma_f32 v[18:19], v[18:19], v[42:43], v[46:47]
	v_add_f32_dpp v92, v96, v92 quad_perm:[2,3,0,1] row_mask:0xf bank_mask:0xf bound_ctrl:1
	v_add_f32_dpp v93, v93, v94 quad_perm:[2,3,0,1] row_mask:0xf bank_mask:0xf bound_ctrl:1
	v_cvt_pk_f16_f32 v22, v22, v23
	v_cvt_pk_f16_f32 v23, v20, v21
	v_fma_f32 v13, |v18|, s25, 1.0
	v_cndmask_b32_e64 v94, v92, v93, s[8:9]
	ds_write_b64 v133, v[22:23] offset:39424
	v_rcp_f32_e32 v22, v13
	v_fma_f32 v13, |v19|, s25, 1.0
	v_cndmask_b32_e64 v92, v93, v92, s[8:9]
	v_mov_b32_e32 v93, v94
	v_rcp_f32_e32 v23, v13
	v_pk_mul_f32 v[24:25], v[18:19], v[18:19]
	v_mov_b32_dpp v93, v93 row_shl:4 row_mask:0xf bank_mask:0x5
	v_mul_f32_e32 v13, 0xbf38aa3b, v24
	v_pk_fma_f32 v[26:27], v[22:23], s[22:23], v[90:91] op_sel_hi:[1,0,0]
	v_mov_b32_dpp v93, v94 row_shr:4 row_mask:0xf bank_mask:0xa
	v_add_f32_e32 v92, v92, v93
	v_pk_fma_f32 v[26:27], v[22:23], v[26:27], s[24:25] op_sel_hi:[1,1,0]
	v_pk_mul_f32 v[16:17], s[0:1], v[16:17] op_sel_hi:[0,1]
	v_add_f32_dpp v92, v92, v92 row_ror:8 row_mask:0xf bank_mask:0xf bound_ctrl:1
	v_mov_b32_e32 v93, v92
	s_nop 1
	v_permlane16_swap_b32_e32 v92, v93
	v_pk_fma_f32 v[26:27], v[22:23], v[26:27], s[34:35] op_sel_hi:[1,1,0]
	v_add_f32_e32 v92, v92, v93
	v_exp_f32_e32 v24, v13
	v_pk_fma_f32 v[26:27], v[22:23], v[26:27], s[40:41] op_sel_hi:[1,1,0]
	v_mul_f32_e32 v13, 0xbf38aa3b, v25
	v_pk_fma_f32 v[16:17], v[16:17], v[44:45], v[48:49]
	v_mov_b32_e32 v93, v92
	v_and_b32_e32 v21, 0x7fffffff, v19
	v_and_b32_e32 v20, 0x7fffffff, v18
	v_exp_f32_e32 v25, v13
	v_pk_mul_f32 v[22:23], v[22:23], v[26:27]
	v_fma_f32 v13, |v16|, s25, 1.0
	v_permlane32_swap_b32_e32 v92, v93
	v_pk_mul_f32 v[20:21], v[20:21], v[22:23]
	v_rcp_f32_e32 v22, v13
	v_fma_f32 v13, |v17|, s25, 1.0
	v_add_f32_e32 v92, v92, v93
	v_rcp_f32_e32 v23, v13
	v_mul_f32_e32 v92, 0x3b800000, v92
	v_max_f32_e32 v18, 0, v18
	v_max_f32_e32 v19, 0, v19
	v_readlane_b32 s42, v92, 0
	v_readlane_b32 s44, v92, 1
	v_readlane_b32 s46, v92, 2
	v_readlane_b32 s48, v92, 3
	v_pk_fma_f32 v[18:19], v[24:25], v[20:21], v[18:19] neg_lo:[1,0,0] neg_hi:[1,0,0]
	v_pk_mul_f32 v[24:25], v[16:17], v[16:17]
	v_pk_add_f32 v[160:161], v[80:81], s[42:43] op_sel_hi:[1,0] neg_lo:[0,1] neg_hi:[0,1]
	v_pk_add_f32 v[110:111], v[76:77], s[44:45] op_sel_hi:[1,0] neg_lo:[0,1] neg_hi:[0,1]
	v_pk_add_f32 v[104:105], v[72:73], s[46:47] op_sel_hi:[1,0] neg_lo:[0,1] neg_hi:[0,1]
	v_pk_add_f32 v[100:101], v[68:69], s[48:49] op_sel_hi:[1,0] neg_lo:[0,1] neg_hi:[0,1]
	v_mul_f32_e32 v13, 0xbf38aa3b, v24
	v_pk_add_f32 v[158:159], v[78:79], s[42:43] op_sel_hi:[1,0] neg_lo:[0,1] neg_hi:[0,1]
	v_mul_f32_e32 v78, v161, v161
	v_pk_add_f32 v[162:163], v[74:75], s[44:45] op_sel_hi:[1,0] neg_lo:[0,1] neg_hi:[0,1]
	v_mul_f32_e32 v74, v111, v111
	v_pk_add_f32 v[108:109], v[70:71], s[46:47] op_sel_hi:[1,0] neg_lo:[0,1] neg_hi:[0,1]
	v_mul_f32_e32 v70, v105, v105
	v_pk_add_f32 v[102:103], v[66:67], s[48:49] op_sel_hi:[1,0] neg_lo:[0,1] neg_hi:[0,1]
	v_mul_f32_e32 v66, v101, v101
	v_exp_f32_e32 v24, v13
	v_pk_fma_f32 v[26:27], v[22:23], s[22:23], v[90:91] op_sel_hi:[1,0,0]
	v_mul_f32_e32 v13, 0xbf38aa3b, v25
	v_readlane_b32 s0, v12, 7
	v_fmac_f32_e32 v78, v160, v160
	v_fmac_f32_e32 v74, v110, v110
	v_fmac_f32_e32 v70, v104, v104
	v_fmac_f32_e32 v66, v100, v100
	v_pk_fma_f32 v[26:27], v[22:23], v[26:27], s[24:25] op_sel_hi:[1,1,0]
	v_exp_f32_e32 v25, v13
	v_pk_mul_f32 v[12:13], s[0:1], v[14:15] op_sel_hi:[0,1]
	v_pk_mul_f32 v[10:11], s[0:1], v[10:11] op_sel_hi:[0,1]
	s_movk_i32 s0, 0x6000
	v_fmac_f32_e32 v78, v159, v159
	v_fmac_f32_e32 v74, v163, v163
	v_fmac_f32_e32 v70, v109, v109
	v_fmac_f32_e32 v66, v103, v103
	v_pk_fma_f32 v[26:27], v[22:23], v[26:27], s[34:35] op_sel_hi:[1,1,0]
	v_add_co_u32_e32 v154, vcc, s0, v82
	v_fmac_f32_e32 v78, v158, v158
	v_fmac_f32_e32 v74, v162, v162
	v_fmac_f32_e32 v70, v108, v108
	v_fmac_f32_e32 v66, v102, v102
	v_pk_fma_f32 v[26:27], v[22:23], v[26:27], s[40:41] op_sel_hi:[1,1,0]
	v_addc_co_u32_e32 v155, vcc, 0, v83, vcc
	s_movk_i32 s0, 0x7000
	v_cndmask_b32_e64 v75, v74, v78, s[4:5]
	v_cndmask_b32_e64 v74, v78, v74, s[4:5]
	v_cndmask_b32_e64 v67, v66, v70, s[4:5]
	v_cndmask_b32_e64 v66, v70, v66, s[4:5]
	v_and_b32_e32 v21, 0x7fffffff, v17
	v_and_b32_e32 v20, 0x7fffffff, v16
	v_pk_mul_f32 v[22:23], v[22:23], v[26:27]
	v_add_co_u32_e32 v156, vcc, s0, v82
	v_readlane_b32 s50, v92, 4
	v_readlane_b32 s52, v92, 5
	v_readlane_b32 s54, v92, 6
	v_readlane_b32 s0, v92, 7
	v_add_f32_dpp v74, v75, v74 quad_perm:[1,0,3,2] row_mask:0xf bank_mask:0xf bound_ctrl:1
	v_add_f32_dpp v66, v67, v66 quad_perm:[1,0,3,2] row_mask:0xf bank_mask:0xf bound_ctrl:1
	v_max_f32_e32 v16, 0, v16
	v_max_f32_e32 v17, 0, v17
	v_pk_mul_f32 v[20:21], v[20:21], v[22:23]
	v_cndmask_b32_e64 v67, v74, v66, s[6:7]
	v_cndmask_b32_e64 v66, v66, v74, s[6:7]
	v_pk_add_f32 v[96:97], v[64:65], s[50:51] op_sel_hi:[1,0] neg_lo:[0,1] neg_hi:[0,1]
	v_pk_add_f32 v[92:93], v[60:61], s[52:53] op_sel_hi:[1,0] neg_lo:[0,1] neg_hi:[0,1]
	v_pk_add_f32 v[78:79], v[56:57], s[54:55] op_sel_hi:[1,0] neg_lo:[0,1] neg_hi:[0,1]
	v_pk_add_f32 v[74:75], v[52:53], s[0:1] op_sel_hi:[1,0] neg_lo:[0,1] neg_hi:[0,1]
	v_pk_fma_f32 v[16:17], v[24:25], v[20:21], v[16:17] neg_lo:[1,0,0] neg_hi:[1,0,0]
	v_pk_fma_f32 v[12:13], v[12:13], v[42:43], v[46:47]
	v_pk_add_f32 v[98:99], v[62:63], s[50:51] op_sel_hi:[1,0] neg_lo:[0,1] neg_hi:[0,1]
	v_mul_f32_e32 v62, v97, v97
	v_pk_add_f32 v[94:95], v[58:59], s[52:53] op_sel_hi:[1,0] neg_lo:[0,1] neg_hi:[0,1]
	v_mul_f32_e32 v58, v93, v93
	v_pk_add_f32 v[80:81], v[54:55], s[54:55] op_sel_hi:[1,0] neg_lo:[0,1] neg_hi:[0,1]
	v_mul_f32_e32 v54, v79, v79
	v_pk_add_f32 v[76:77], v[50:51], s[0:1] op_sel_hi:[1,0] neg_lo:[0,1] neg_hi:[0,1]
	v_mul_f32_e32 v50, v75, v75
	v_cvt_pk_f16_f32 v18, v18, v19
	v_cvt_pk_f16_f32 v19, v16, v17
	v_fma_f32 v16, |v12|, s25, 1.0
	v_fma_f32 v17, |v13|, s25, 1.0
	v_fmac_f32_e32 v62, v96, v96
	v_fmac_f32_e32 v58, v92, v92
	v_fmac_f32_e32 v54, v78, v78
	v_fmac_f32_e32 v50, v74, v74
	v_rcp_f32_e32 v16, v16
	v_rcp_f32_e32 v17, v17
	v_fmac_f32_e32 v62, v99, v99
	v_fmac_f32_e32 v58, v95, v95
	v_fmac_f32_e32 v54, v81, v81
	v_fmac_f32_e32 v50, v77, v77
	v_fmac_f32_e32 v62, v98, v98
	v_fmac_f32_e32 v58, v94, v94
	v_fmac_f32_e32 v54, v80, v80
	v_fmac_f32_e32 v50, v76, v76
	v_cndmask_b32_e64 v59, v58, v62, s[4:5]
	v_cndmask_b32_e64 v58, v62, v58, s[4:5]
	v_cndmask_b32_e64 v51, v50, v54, s[4:5]
	v_cndmask_b32_e64 v50, v54, v50, s[4:5]
	v_add_f32_dpp v58, v59, v58 quad_perm:[1,0,3,2] row_mask:0xf bank_mask:0xf bound_ctrl:1
	ds_write_b64 v119, v[18:19] offset:39936
	v_add_f32_dpp v50, v51, v50 quad_perm:[1,0,3,2] row_mask:0xf bank_mask:0xf bound_ctrl:1
	v_pk_mul_f32 v[18:19], v[12:13], v[12:13]
	v_pk_fma_f32 v[20:21], v[16:17], s[22:23], v[90:91] op_sel_hi:[1,0,0]
	v_cndmask_b32_e64 v51, v58, v50, s[6:7]
	v_cndmask_b32_e64 v50, v50, v58, s[6:7]
	v_mul_f32_e32 v18, 0xbf38aa3b, v18
	v_pk_fma_f32 v[20:21], v[16:17], v[20:21], s[24:25] op_sel_hi:[1,1,0]
	v_mul_f32_e32 v19, 0xbf38aa3b, v19
	v_add_f32_dpp v66, v67, v66 quad_perm:[2,3,0,1] row_mask:0xf bank_mask:0xf bound_ctrl:1
	v_add_f32_dpp v50, v51, v50 quad_perm:[2,3,0,1] row_mask:0xf bank_mask:0xf bound_ctrl:1
	v_exp_f32_e32 v18, v18
	v_pk_fma_f32 v[20:21], v[16:17], v[20:21], s[34:35] op_sel_hi:[1,1,0]
	v_exp_f32_e32 v19, v19
	v_cndmask_b32_e64 v51, v66, v50, s[8:9]
	v_pk_fma_f32 v[20:21], v[16:17], v[20:21], s[40:41] op_sel_hi:[1,1,0]
	v_mov_b32_e32 v52, v51
	v_and_b32_e32 v15, 0x7fffffff, v13
	v_and_b32_e32 v14, 0x7fffffff, v12
	v_pk_mul_f32 v[16:17], v[16:17], v[20:21]
	v_mov_b32_dpp v52, v52 row_shl:4 row_mask:0xf bank_mask:0x5
	v_max_f32_e32 v12, 0, v12
	v_max_f32_e32 v13, 0, v13
	v_pk_mul_f32 v[14:15], v[14:15], v[16:17]
	v_cndmask_b32_e64 v50, v50, v66, s[8:9]
	v_mov_b32_dpp v52, v51 row_shr:4 row_mask:0xf bank_mask:0xa
	v_pk_fma_f32 v[12:13], v[18:19], v[14:15], v[12:13] neg_lo:[1,0,0] neg_hi:[1,0,0]
	v_pk_fma_f32 v[10:11], v[10:11], v[44:45], v[48:49]
	v_add_f32_e32 v50, v50, v52
	v_cvt_pk_f16_f32 v12, v12, v13
	v_fma_f32 v13, |v10|, s25, 1.0
	v_add_f32_dpp v50, v50, v50 row_ror:8 row_mask:0xf bank_mask:0xf bound_ctrl:1
	v_rcp_f32_e32 v16, v13
	v_fma_f32 v13, |v11|, s25, 1.0
	v_mov_b32_e32 v51, v50
	v_rcp_f32_e32 v17, v13
	s_nop 0
	v_permlane16_swap_b32_e32 v50, v51
	v_add_f32_e32 v50, v50, v51
	v_mov_b32_e32 v51, v50
	v_pk_mul_f32 v[18:19], v[10:11], v[10:11]
	s_nop 0
	v_permlane32_swap_b32_e32 v50, v51
	v_mul_f32_e32 v13, 0xbf38aa3b, v18
	v_pk_fma_f32 v[20:21], v[16:17], s[22:23], v[90:91] op_sel_hi:[1,0,0]
	v_add_f32_e32 v50, v50, v51
	v_exp_f32_e32 v18, v13
	v_pk_fma_f32 v[20:21], v[16:17], v[20:21], s[24:25] op_sel_hi:[1,1,0]
	v_mul_f32_e32 v13, 0xbf38aa3b, v19
	v_addc_co_u32_e32 v157, vcc, 0, v83, vcc
	v_fmamk_f32 v50, v50, 0x3b800000, v116
	v_pk_fma_f32 v[20:21], v[16:17], v[20:21], s[34:35] op_sel_hi:[1,1,0]
	v_exp_f32_e32 v19, v13
	v_mul_f32_e32 v51, 0x4f800000, v50
	v_cmp_gt_f32_e32 vcc, s35, v50
	v_pk_fma_f32 v[20:21], v[16:17], v[20:21], s[40:41] op_sel_hi:[1,1,0]
	v_and_b32_e32 v15, 0x7fffffff, v11
	v_cndmask_b32_e32 v50, v50, v51, vcc
	v_and_b32_e32 v14, 0x7fffffff, v10
	v_pk_mul_f32 v[16:17], v[16:17], v[20:21]
	v_sqrt_f32_e32 v51, v50
	v_max_f32_e32 v10, 0, v10
	v_max_f32_e32 v11, 0, v11
	v_pk_mul_f32 v[14:15], v[14:15], v[16:17]
	v_add_u32_e32 v52, -1, v51
	v_pk_fma_f32 v[10:11], v[18:19], v[14:15], v[10:11] neg_lo:[1,0,0] neg_hi:[1,0,0]
	v_fma_f32 v53, -v52, v51, v50
	v_cvt_pk_f16_f32 v13, v10, v11
	v_bitop3_b32 v10, v86, s41, v88 bitop3:0x6c
	v_or3_b32 v146, v85, v10, v87
	v_lshlrev_b32_e32 v10, 4, v141
	v_and_or_b32 v147, v10, s41, v84
	v_lshlrev_b32_e32 v10, 4, v142
	v_and_or_b32 v148, v10, s41, v84
	v_lshlrev_b32_e32 v10, 4, v143
	v_cmp_ge_f32_e64 s[0:1], 0, v53
	v_add_u32_e32 v53, 1, v51
	v_and_or_b32 v149, v10, s41, v84
	v_bitop3_b32 v10, v125, v0, 15 bitop3:0x78
	v_cndmask_b32_e64 v52, v51, v52, s[0:1]
	v_fma_f32 v51, -v53, v51, v50
	v_lshl_or_b32 v150, v10, 4, v84
	v_bitop3_b32 v10, v125, v107, 4 bitop3:0x36
	v_cmp_lt_f32_e64 s[0:1], 0, v51
	v_lshl_or_b32 v151, v10, 4, v84
	v_bitop3_b32 v10, v125, v107, 8 bitop3:0x36
	v_cndmask_b32_e64 v51, v52, v53, s[0:1]
	v_lshl_or_b32 v152, v10, 4, v84
	v_bitop3_b32 v10, v125, v107, 12 bitop3:0x36
	v_mul_f32_e32 v52, 0x37800000, v51
	ds_write_b64 v146, v[12:13] offset:40448
	v_lshl_or_b32 v153, v10, 4, v84
	v_cndmask_b32_e32 v51, v51, v52, vcc
	v_cmp_class_f32_e32 vcc, v50, v117
	ds_read_b128 v[38:41], v115 offset:32768
	ds_read_b128 v[34:37], v147 offset:32768
	ds_read_b128 v[30:33], v148 offset:32768
	ds_read_b128 v[26:29], v149 offset:32768
	ds_read_b128 v[22:25], v150 offset:33024
	ds_read_b128 v[18:21], v151 offset:33024
	ds_read_b128 v[14:17], v152 offset:33024
	ds_read_b128 v[10:13], v153 offset:33024
	global_load_dwordx4 v[86:89], v[154:155], off offset:1024 nt
	global_load_dwordx4 v[82:85], v[154:155], off offset:2048 nt
	global_load_dwordx4 v[66:69], v[154:155], off offset:3072 nt
	global_load_dwordx4 v[70:73], v[156:157], off offset:-4096 nt
	global_load_dwordx4 v[58:61], v[156:157], off nt
	v_cndmask_b32_e32 v154, v51, v50, vcc
	v_div_scale_f32 v155, s[0:1], v154, v154, 1.0
	v_rcp_f32_e32 v164, v155
	global_load_dwordx4 v[62:65], v[156:157], off offset:1024 nt
	global_load_dwordx4 v[54:57], v[156:157], off offset:2048 nt
	global_load_dwordx4 v[50:53], v[156:157], off offset:3072 nt
	v_fma_f32 v156, -v155, v164, 1.0
	v_fmac_f32_e32 v164, v156, v164
	v_div_scale_f32 v156, vcc, 1.0, v154, 1.0
	v_mul_f32_e32 v157, v156, v164
	v_fma_f32 v165, -v155, v157, v156
	v_fmac_f32_e32 v157, v165, v164
	v_fma_f32 v155, -v155, v157, v156
	v_div_fmas_f32 v155, v155, v164, v157
	v_div_fixup_f32 v154, v155, v154, 1.0
	s_nop 0
	v_readlane_b32 s0, v154, 0
	s_nop 1
	v_pk_mul_f32 v[156:157], s[0:1], v[158:159] op_sel_hi:[0,1]
	v_pk_fma_f32 v[156:157], v[156:157], v[42:43], v[46:47]
	s_nop 0
	v_fma_f32 v155, |v156|, s25, 1.0
	v_rcp_f32_e32 v164, v155
	v_fma_f32 v155, |v157|, s25, 1.0
	v_rcp_f32_e32 v165, v155
	v_pk_mul_f32 v[166:167], v[156:157], v[156:157]
	v_and_b32_e32 v159, 0x7fffffff, v157
	v_mul_f32_e32 v155, 0xbf38aa3b, v166
	v_pk_fma_f32 v[168:169], v[164:165], s[22:23], v[90:91] op_sel_hi:[1,0,0]
	v_exp_f32_e32 v166, v155
	v_pk_fma_f32 v[168:169], v[164:165], v[168:169], s[24:25] op_sel_hi:[1,1,0]
	v_mul_f32_e32 v155, 0xbf38aa3b, v167
	v_pk_fma_f32 v[168:169], v[164:165], v[168:169], s[34:35] op_sel_hi:[1,1,0]
	v_exp_f32_e32 v167, v155
	v_pk_fma_f32 v[168:169], v[164:165], v[168:169], s[40:41] op_sel_hi:[1,1,0]
	v_and_b32_e32 v158, 0x7fffffff, v156
	v_pk_mul_f32 v[164:165], v[164:165], v[168:169]
	v_max_f32_e32 v156, 0, v156
	v_max_f32_e32 v157, 0, v157
	v_pk_mul_f32 v[158:159], v[158:159], v[164:165]
	s_nop 0
	v_pk_fma_f32 v[156:157], v[166:167], v[158:159], v[156:157] neg_lo:[1,0,0] neg_hi:[1,0,0]
	v_pk_mul_f32 v[158:159], s[0:1], v[160:161] op_sel_hi:[0,1]
	v_pk_fma_f32 v[158:159], v[158:159], v[44:45], v[48:49]
	v_cvt_pk_f16_f32 v156, v156, v157
	v_fma_f32 v155, |v158|, s25, 1.0
	v_rcp_f32_e32 v164, v155
	v_fma_f32 v155, |v159|, s25, 1.0
	v_rcp_f32_e32 v165, v155
	v_pk_mul_f32 v[166:167], v[158:159], v[158:159]
	v_and_b32_e32 v161, 0x7fffffff, v159
	v_mul_f32_e32 v155, 0xbf38aa3b, v166
	v_pk_fma_f32 v[168:169], v[164:165], s[22:23], v[90:91] op_sel_hi:[1,0,0]
	v_exp_f32_e32 v166, v155
	v_pk_fma_f32 v[168:169], v[164:165], v[168:169], s[24:25] op_sel_hi:[1,1,0]
	v_mul_f32_e32 v155, 0xbf38aa3b, v167
	v_pk_fma_f32 v[168:169], v[164:165], v[168:169], s[34:35] op_sel_hi:[1,1,0]
	v_exp_f32_e32 v167, v155
	v_pk_fma_f32 v[168:169], v[164:165], v[168:169], s[40:41] op_sel_hi:[1,1,0]
	v_and_b32_e32 v160, 0x7fffffff, v158
	v_pk_mul_f32 v[164:165], v[164:165], v[168:169]
	v_max_f32_e32 v158, 0, v158
	v_max_f32_e32 v159, 0, v159
	v_pk_mul_f32 v[160:161], v[160:161], v[164:165]
	v_readlane_b32 s0, v154, 1
	v_pk_fma_f32 v[158:159], v[166:167], v[160:161], v[158:159] neg_lo:[1,0,0] neg_hi:[1,0,0]
	s_nop 0
	v_cvt_pk_f16_f32 v157, v158, v159
	ds_write_b64 v140, v[156:157] offset:32768
	v_pk_mul_f32 v[156:157], s[0:1], v[162:163] op_sel_hi:[0,1]
	v_pk_fma_f32 v[156:157], v[156:157], v[42:43], v[46:47]
	v_pk_mul_f32 v[110:111], s[0:1], v[110:111] op_sel_hi:[0,1]
	v_fma_f32 v140, |v156|, s25, 1.0
	v_rcp_f32_e32 v160, v140
	v_fma_f32 v140, |v157|, s25, 1.0
	v_rcp_f32_e32 v161, v140
	v_pk_mul_f32 v[162:163], v[156:157], v[156:157]
	v_pk_fma_f32 v[110:111], v[110:111], v[44:45], v[48:49]
	v_mul_f32_e32 v140, 0xbf38aa3b, v162
	v_pk_fma_f32 v[164:165], v[160:161], s[22:23], v[90:91] op_sel_hi:[1,0,0]
	v_exp_f32_e32 v162, v140
	v_pk_fma_f32 v[164:165], v[160:161], v[164:165], s[24:25] op_sel_hi:[1,1,0]
	v_mul_f32_e32 v140, 0xbf38aa3b, v163
	v_pk_fma_f32 v[164:165], v[160:161], v[164:165], s[34:35] op_sel_hi:[1,1,0]
	v_and_b32_e32 v159, 0x7fffffff, v157
	v_pk_fma_f32 v[164:165], v[160:161], v[164:165], s[40:41] op_sel_hi:[1,1,0]
	v_and_b32_e32 v158, 0x7fffffff, v156
	v_exp_f32_e32 v163, v140
	v_pk_mul_f32 v[160:161], v[160:161], v[164:165]
	v_fma_f32 v140, |v110|, s25, 1.0
	v_pk_mul_f32 v[158:159], v[158:159], v[160:161]
	v_rcp_f32_e32 v160, v140
	v_fma_f32 v140, |v111|, s25, 1.0
	v_rcp_f32_e32 v161, v140
	v_max_f32_e32 v156, 0, v156
	v_max_f32_e32 v157, 0, v157
	v_pk_fma_f32 v[156:157], v[162:163], v[158:159], v[156:157] neg_lo:[1,0,0] neg_hi:[1,0,0]
	v_pk_mul_f32 v[162:163], v[110:111], v[110:111]
	v_pk_fma_f32 v[164:165], v[160:161], s[22:23], v[90:91] op_sel_hi:[1,0,0]
	v_mul_f32_e32 v140, 0xbf38aa3b, v162
	v_exp_f32_e32 v162, v140
	v_pk_fma_f32 v[164:165], v[160:161], v[164:165], s[24:25] op_sel_hi:[1,1,0]
	v_mul_f32_e32 v140, 0xbf38aa3b, v163
	v_pk_fma_f32 v[164:165], v[160:161], v[164:165], s[34:35] op_sel_hi:[1,1,0]
	v_exp_f32_e32 v163, v140
	v_pk_fma_f32 v[164:165], v[160:161], v[164:165], s[40:41] op_sel_hi:[1,1,0]
	v_and_b32_e32 v159, 0x7fffffff, v111
	v_and_b32_e32 v158, 0x7fffffff, v110
	v_pk_mul_f32 v[160:161], v[160:161], v[164:165]
	v_max_f32_e32 v110, 0, v110
	v_max_f32_e32 v111, 0, v111
	v_pk_mul_f32 v[158:159], v[158:159], v[160:161]
	v_readlane_b32 s0, v154, 2
	v_pk_fma_f32 v[110:111], v[162:163], v[158:159], v[110:111] neg_lo:[1,0,0] neg_hi:[1,0,0]
	v_cvt_pk_f16_f32 v156, v156, v157
	v_pk_mul_f32 v[108:109], s[0:1], v[108:109] op_sel_hi:[0,1]
	v_cvt_pk_f16_f32 v157, v110, v111
	v_pk_fma_f32 v[108:109], v[108:109], v[42:43], v[46:47]
	ds_write_b64 v138, v[156:157] offset:33280
	v_fma_f32 v138, |v108|, s25, 1.0
	v_rcp_f32_e32 v156, v138
	v_fma_f32 v138, |v109|, s25, 1.0
	v_rcp_f32_e32 v157, v138
	v_pk_mul_f32 v[158:159], v[108:109], v[108:109]
	v_and_b32_e32 v111, 0x7fffffff, v109
	v_mul_f32_e32 v138, 0xbf38aa3b, v158
	v_pk_fma_f32 v[160:161], v[156:157], s[22:23], v[90:91] op_sel_hi:[1,0,0]
	v_exp_f32_e32 v158, v138
	v_pk_fma_f32 v[160:161], v[156:157], v[160:161], s[24:25] op_sel_hi:[1,1,0]
	v_mul_f32_e32 v138, 0xbf38aa3b, v159
	v_pk_fma_f32 v[160:161], v[156:157], v[160:161], s[34:35] op_sel_hi:[1,1,0]
	v_exp_f32_e32 v159, v138
	v_pk_fma_f32 v[160:161], v[156:157], v[160:161], s[40:41] op_sel_hi:[1,1,0]
	v_and_b32_e32 v110, 0x7fffffff, v108
	v_pk_mul_f32 v[156:157], v[156:157], v[160:161]
	v_max_f32_e32 v108, 0, v108
	v_max_f32_e32 v109, 0, v109
	v_pk_mul_f32 v[110:111], v[110:111], v[156:157]
	v_pk_mul_f32 v[104:105], s[0:1], v[104:105] op_sel_hi:[0,1]
	v_pk_fma_f32 v[108:109], v[158:159], v[110:111], v[108:109] neg_lo:[1,0,0] neg_hi:[1,0,0]
	v_pk_fma_f32 v[104:105], v[104:105], v[44:45], v[48:49]
	v_cvt_pk_f16_f32 v108, v108, v109
	v_fma_f32 v109, |v104|, s25, 1.0
	v_rcp_f32_e32 v156, v109
	v_fma_f32 v109, |v105|, s25, 1.0
	v_rcp_f32_e32 v157, v109
	v_pk_mul_f32 v[158:159], v[104:105], v[104:105]
	v_and_b32_e32 v111, 0x7fffffff, v105
	v_mul_f32_e32 v109, 0xbf38aa3b, v158
	v_pk_fma_f32 v[160:161], v[156:157], s[22:23], v[90:91] op_sel_hi:[1,0,0]
	v_exp_f32_e32 v158, v109
	v_pk_fma_f32 v[160:161], v[156:157], v[160:161], s[24:25] op_sel_hi:[1,1,0]
	v_mul_f32_e32 v109, 0xbf38aa3b, v159
	v_pk_fma_f32 v[160:161], v[156:157], v[160:161], s[34:35] op_sel_hi:[1,1,0]
	v_exp_f32_e32 v159, v109
	v_pk_fma_f32 v[160:161], v[156:157], v[160:161], s[40:41] op_sel_hi:[1,1,0]
	v_and_b32_e32 v110, 0x7fffffff, v104
	v_pk_mul_f32 v[156:157], v[156:157], v[160:161]
	v_max_f32_e32 v104, 0, v104
	v_max_f32_e32 v105, 0, v105
	v_pk_mul_f32 v[110:111], v[110:111], v[156:157]
	v_readlane_b32 s0, v154, 3
	v_pk_fma_f32 v[104:105], v[158:159], v[110:111], v[104:105] neg_lo:[1,0,0] neg_hi:[1,0,0]
	s_nop 0
	v_pk_mul_f32 v[102:103], s[0:1], v[102:103] op_sel_hi:[0,1]
	v_cvt_pk_f16_f32 v109, v104, v105
	v_pk_fma_f32 v[102:103], v[102:103], v[42:43], v[46:47]
	ds_write_b64 v135, v[108:109] offset:33792
	v_fma_f32 v108, |v102|, s25, 1.0
	v_fma_f32 v109, |v103|, s25, 1.0
	v_rcp_f32_e32 v108, v108
	v_rcp_f32_e32 v109, v109
	v_pk_mul_f32 v[110:111], v[102:103], v[102:103]
	v_and_b32_e32 v105, 0x7fffffff, v103
	v_mul_f32_e32 v110, 0xbf38aa3b, v110
	v_pk_fma_f32 v[156:157], v[108:109], s[22:23], v[90:91] op_sel_hi:[1,0,0]
	v_mul_f32_e32 v111, 0xbf38aa3b, v111
	v_pk_fma_f32 v[156:157], v[108:109], v[156:157], s[24:25] op_sel_hi:[1,1,0]
	v_exp_f32_e32 v110, v110
	v_pk_fma_f32 v[156:157], v[108:109], v[156:157], s[34:35] op_sel_hi:[1,1,0]
	v_exp_f32_e32 v111, v111
	v_pk_fma_f32 v[156:157], v[108:109], v[156:157], s[40:41] op_sel_hi:[1,1,0]
	v_and_b32_e32 v104, 0x7fffffff, v102
	v_pk_mul_f32 v[108:109], v[108:109], v[156:157]
	v_max_f32_e32 v102, 0, v102
	v_max_f32_e32 v103, 0, v103
	v_pk_mul_f32 v[104:105], v[104:105], v[108:109]
	v_pk_mul_f32 v[100:101], s[0:1], v[100:101] op_sel_hi:[0,1]
	v_pk_fma_f32 v[102:103], v[110:111], v[104:105], v[102:103] neg_lo:[1,0,0] neg_hi:[1,0,0]
	v_pk_fma_f32 v[100:101], v[100:101], v[44:45], v[48:49]
	v_cvt_pk_f16_f32 v102, v102, v103
	v_fma_f32 v103, |v100|, s25, 1.0
	v_rcp_f32_e32 v108, v103
	v_fma_f32 v103, |v101|, s25, 1.0
	v_rcp_f32_e32 v109, v103
	v_pk_mul_f32 v[110:111], v[100:101], v[100:101]
	v_and_b32_e32 v105, 0x7fffffff, v101
	v_mul_f32_e32 v103, 0xbf38aa3b, v110
	v_pk_fma_f32 v[156:157], v[108:109], s[22:23], v[90:91] op_sel_hi:[1,0,0]
	v_exp_f32_e32 v110, v103
	v_pk_fma_f32 v[156:157], v[108:109], v[156:157], s[24:25] op_sel_hi:[1,1,0]
	v_mul_f32_e32 v103, 0xbf38aa3b, v111
	v_pk_fma_f32 v[156:157], v[108:109], v[156:157], s[34:35] op_sel_hi:[1,1,0]
	v_exp_f32_e32 v111, v103
	v_pk_fma_f32 v[156:157], v[108:109], v[156:157], s[40:41] op_sel_hi:[1,1,0]
	v_and_b32_e32 v104, 0x7fffffff, v100
	v_pk_mul_f32 v[108:109], v[108:109], v[156:157]
	v_max_f32_e32 v100, 0, v100
	v_max_f32_e32 v101, 0, v101
	v_pk_mul_f32 v[104:105], v[104:105], v[108:109]
	v_readlane_b32 s0, v154, 4
	v_pk_fma_f32 v[100:101], v[110:111], v[104:105], v[100:101] neg_lo:[1,0,0] neg_hi:[1,0,0]
	s_nop 0
	v_pk_mul_f32 v[98:99], s[0:1], v[98:99] op_sel_hi:[0,1]
	v_cvt_pk_f16_f32 v103, v100, v101
	v_pk_fma_f32 v[98:99], v[98:99], v[42:43], v[46:47]
	ds_write_b64 v134, v[102:103] offset:34304
	v_fma_f32 v102, |v98|, s25, 1.0
	v_fma_f32 v103, |v99|, s25, 1.0
	v_rcp_f32_e32 v102, v102
	v_rcp_f32_e32 v103, v103
	v_pk_mul_f32 v[104:105], v[98:99], v[98:99]
	v_and_b32_e32 v101, 0x7fffffff, v99
	v_mul_f32_e32 v104, 0xbf38aa3b, v104
	v_pk_fma_f32 v[108:109], v[102:103], s[22:23], v[90:91] op_sel_hi:[1,0,0]
	v_mul_f32_e32 v105, 0xbf38aa3b, v105
	v_pk_fma_f32 v[108:109], v[102:103], v[108:109], s[24:25] op_sel_hi:[1,1,0]
	v_exp_f32_e32 v104, v104
	v_pk_fma_f32 v[108:109], v[102:103], v[108:109], s[34:35] op_sel_hi:[1,1,0]
	v_exp_f32_e32 v105, v105
	v_pk_fma_f32 v[108:109], v[102:103], v[108:109], s[40:41] op_sel_hi:[1,1,0]
	v_and_b32_e32 v100, 0x7fffffff, v98
	v_pk_mul_f32 v[102:103], v[102:103], v[108:109]
	v_max_f32_e32 v98, 0, v98
	v_max_f32_e32 v99, 0, v99
	v_pk_mul_f32 v[100:101], v[100:101], v[102:103]
	v_pk_mul_f32 v[96:97], s[0:1], v[96:97] op_sel_hi:[0,1]
	v_pk_fma_f32 v[98:99], v[104:105], v[100:101], v[98:99] neg_lo:[1,0,0] neg_hi:[1,0,0]
	v_pk_fma_f32 v[96:97], v[96:97], v[44:45], v[48:49]
	v_cvt_pk_f16_f32 v98, v98, v99
	v_fma_f32 v99, |v96|, s25, 1.0
	v_rcp_f32_e32 v102, v99
	v_fma_f32 v99, |v97|, s25, 1.0
	v_rcp_f32_e32 v103, v99
	v_pk_mul_f32 v[104:105], v[96:97], v[96:97]
	v_and_b32_e32 v101, 0x7fffffff, v97
	v_mul_f32_e32 v99, 0xbf38aa3b, v104
	v_pk_fma_f32 v[108:109], v[102:103], s[22:23], v[90:91] op_sel_hi:[1,0,0]
	v_exp_f32_e32 v104, v99
	v_pk_fma_f32 v[108:109], v[102:103], v[108:109], s[24:25] op_sel_hi:[1,1,0]
	v_mul_f32_e32 v99, 0xbf38aa3b, v105
	v_pk_fma_f32 v[108:109], v[102:103], v[108:109], s[34:35] op_sel_hi:[1,1,0]
	v_exp_f32_e32 v105, v99
	v_pk_fma_f32 v[108:109], v[102:103], v[108:109], s[40:41] op_sel_hi:[1,1,0]
	v_and_b32_e32 v100, 0x7fffffff, v96
	v_pk_mul_f32 v[102:103], v[102:103], v[108:109]
	v_max_f32_e32 v96, 0, v96
	v_max_f32_e32 v97, 0, v97
	v_pk_mul_f32 v[100:101], v[100:101], v[102:103]
	v_readlane_b32 s0, v154, 5
	v_pk_fma_f32 v[96:97], v[104:105], v[100:101], v[96:97] neg_lo:[1,0,0] neg_hi:[1,0,0]
	v_mov_b32_e32 v104, 0
	v_pk_mul_f32 v[94:95], s[0:1], v[94:95] op_sel_hi:[0,1]
	v_cvt_pk_f16_f32 v99, v96, v97
	v_pk_fma_f32 v[94:95], v[94:95], v[42:43], v[46:47]
	ds_write_b64 v120, v[98:99] offset:34816
	v_fma_f32 v98, |v94|, s25, 1.0
	v_fma_f32 v99, |v95|, s25, 1.0
	v_rcp_f32_e32 v98, v98
	v_rcp_f32_e32 v99, v99
	v_pk_mul_f32 v[100:101], v[94:95], v[94:95]
	v_and_b32_e32 v97, 0x7fffffff, v95
	v_mul_f32_e32 v100, 0xbf38aa3b, v100
	v_pk_fma_f32 v[102:103], v[98:99], s[22:23], v[90:91] op_sel_hi:[1,0,0]
	v_mul_f32_e32 v101, 0xbf38aa3b, v101
	v_pk_fma_f32 v[102:103], v[98:99], v[102:103], s[24:25] op_sel_hi:[1,1,0]
	v_exp_f32_e32 v100, v100
	v_pk_fma_f32 v[102:103], v[98:99], v[102:103], s[34:35] op_sel_hi:[1,1,0]
	v_exp_f32_e32 v101, v101
	v_pk_fma_f32 v[102:103], v[98:99], v[102:103], s[40:41] op_sel_hi:[1,1,0]
	v_and_b32_e32 v96, 0x7fffffff, v94
	v_pk_mul_f32 v[98:99], v[98:99], v[102:103]
	v_max_f32_e32 v94, 0, v94
	v_max_f32_e32 v95, 0, v95
	v_pk_mul_f32 v[96:97], v[96:97], v[98:99]
	v_pk_mul_f32 v[92:93], s[0:1], v[92:93] op_sel_hi:[0,1]
	v_pk_fma_f32 v[94:95], v[100:101], v[96:97], v[94:95] neg_lo:[1,0,0] neg_hi:[1,0,0]
	v_pk_fma_f32 v[92:93], v[92:93], v[44:45], v[48:49]
	v_cvt_pk_f16_f32 v94, v94, v95
	v_fma_f32 v95, |v92|, s25, 1.0
	v_rcp_f32_e32 v98, v95
	v_fma_f32 v95, |v93|, s25, 1.0
	v_rcp_f32_e32 v99, v95
	v_pk_mul_f32 v[100:101], v[92:93], v[92:93]
	v_and_b32_e32 v97, 0x7fffffff, v93
	v_mul_f32_e32 v95, 0xbf38aa3b, v100
	v_pk_fma_f32 v[102:103], v[98:99], s[22:23], v[90:91] op_sel_hi:[1,0,0]
	v_exp_f32_e32 v100, v95
	v_pk_fma_f32 v[102:103], v[98:99], v[102:103], s[24:25] op_sel_hi:[1,1,0]
	v_mul_f32_e32 v95, 0xbf38aa3b, v101
	v_pk_fma_f32 v[102:103], v[98:99], v[102:103], s[34:35] op_sel_hi:[1,1,0]
	v_exp_f32_e32 v101, v95
	v_pk_fma_f32 v[102:103], v[98:99], v[102:103], s[40:41] op_sel_hi:[1,1,0]
	v_and_b32_e32 v96, 0x7fffffff, v92
	v_pk_mul_f32 v[98:99], v[98:99], v[102:103]
	v_max_f32_e32 v92, 0, v92
	v_max_f32_e32 v93, 0, v93
	v_pk_mul_f32 v[96:97], v[96:97], v[98:99]
	v_readlane_b32 s0, v154, 6
	v_pk_fma_f32 v[92:93], v[100:101], v[96:97], v[92:93] neg_lo:[1,0,0] neg_hi:[1,0,0]
	s_waitcnt vmcnt(1)
	v_add_f32_e32 v100, v56, v57
	v_pk_mul_f32 v[80:81], s[0:1], v[80:81] op_sel_hi:[0,1]
	v_cvt_pk_f16_f32 v95, v92, v93
	v_pk_fma_f32 v[80:81], v[80:81], v[42:43], v[46:47]
	ds_write_b64 v121, v[94:95] offset:35328
	v_fma_f32 v94, |v80|, s25, 1.0
	v_fma_f32 v95, |v81|, s25, 1.0
	v_rcp_f32_e32 v94, v94
	v_rcp_f32_e32 v95, v95
	v_pk_mul_f32 v[96:97], v[80:81], v[80:81]
	v_and_b32_e32 v93, 0x7fffffff, v81
	v_mul_f32_e32 v96, 0xbf38aa3b, v96
	v_pk_fma_f32 v[98:99], v[94:95], s[22:23], v[90:91] op_sel_hi:[1,0,0]
	v_mul_f32_e32 v97, 0xbf38aa3b, v97
	v_pk_fma_f32 v[98:99], v[94:95], v[98:99], s[24:25] op_sel_hi:[1,1,0]
	v_exp_f32_e32 v96, v96
	v_pk_fma_f32 v[98:99], v[94:95], v[98:99], s[34:35] op_sel_hi:[1,1,0]
	v_exp_f32_e32 v97, v97
	v_pk_fma_f32 v[98:99], v[94:95], v[98:99], s[40:41] op_sel_hi:[1,1,0]
	v_and_b32_e32 v92, 0x7fffffff, v80
	v_pk_mul_f32 v[94:95], v[94:95], v[98:99]
	v_max_f32_e32 v80, 0, v80
	v_max_f32_e32 v81, 0, v81
	v_pk_mul_f32 v[92:93], v[92:93], v[94:95]
	v_pk_mul_f32 v[78:79], s[0:1], v[78:79] op_sel_hi:[0,1]
	v_pk_fma_f32 v[80:81], v[96:97], v[92:93], v[80:81] neg_lo:[1,0,0] neg_hi:[1,0,0]
	v_pk_fma_f32 v[78:79], v[78:79], v[44:45], v[48:49]
	v_cvt_pk_f16_f32 v80, v80, v81
	v_fma_f32 v81, |v78|, s25, 1.0
	v_rcp_f32_e32 v94, v81
	v_fma_f32 v81, |v79|, s25, 1.0
	v_rcp_f32_e32 v95, v81
	v_pk_mul_f32 v[96:97], v[78:79], v[78:79]
	v_and_b32_e32 v93, 0x7fffffff, v79
	v_mul_f32_e32 v81, 0xbf38aa3b, v96
	v_pk_fma_f32 v[98:99], v[94:95], s[22:23], v[90:91] op_sel_hi:[1,0,0]
	v_exp_f32_e32 v96, v81
	v_pk_fma_f32 v[98:99], v[94:95], v[98:99], s[24:25] op_sel_hi:[1,1,0]
	v_mul_f32_e32 v81, 0xbf38aa3b, v97
	v_pk_fma_f32 v[98:99], v[94:95], v[98:99], s[34:35] op_sel_hi:[1,1,0]
	v_exp_f32_e32 v97, v81
	v_pk_fma_f32 v[98:99], v[94:95], v[98:99], s[40:41] op_sel_hi:[1,1,0]
	v_and_b32_e32 v92, 0x7fffffff, v78
	v_pk_mul_f32 v[94:95], v[94:95], v[98:99]
	v_max_f32_e32 v78, 0, v78
	v_max_f32_e32 v79, 0, v79
	v_pk_mul_f32 v[92:93], v[92:93], v[94:95]
	v_readlane_b32 s0, v154, 7
	v_pk_fma_f32 v[78:79], v[96:97], v[92:93], v[78:79] neg_lo:[1,0,0] neg_hi:[1,0,0]
	v_add_f32_e32 v97, v64, v65
	v_pk_mul_f32 v[76:77], s[0:1], v[76:77] op_sel_hi:[0,1]
	v_cvt_pk_f16_f32 v81, v78, v79
	v_pk_fma_f32 v[76:77], v[76:77], v[42:43], v[46:47]
	ds_write_b64 v118, v[80:81] offset:35840
	v_fma_f32 v80, |v76|, s25, 1.0
	v_fma_f32 v81, |v77|, s25, 1.0
	v_rcp_f32_e32 v80, v80
	v_rcp_f32_e32 v81, v81
	v_pk_mul_f32 v[92:93], v[76:77], v[76:77]
	v_and_b32_e32 v79, 0x7fffffff, v77
	v_mul_f32_e32 v92, 0xbf38aa3b, v92
	v_pk_fma_f32 v[94:95], v[80:81], s[22:23], v[90:91] op_sel_hi:[1,0,0]
	v_mul_f32_e32 v93, 0xbf38aa3b, v93
	v_pk_fma_f32 v[94:95], v[80:81], v[94:95], s[24:25] op_sel_hi:[1,1,0]
	v_exp_f32_e32 v92, v92
	v_pk_fma_f32 v[94:95], v[80:81], v[94:95], s[34:35] op_sel_hi:[1,1,0]
	v_exp_f32_e32 v93, v93
	v_pk_fma_f32 v[94:95], v[80:81], v[94:95], s[40:41] op_sel_hi:[1,1,0]
	v_and_b32_e32 v78, 0x7fffffff, v76
	v_pk_mul_f32 v[80:81], v[80:81], v[94:95]
	v_max_f32_e32 v76, 0, v76
	v_max_f32_e32 v77, 0, v77
	v_pk_mul_f32 v[78:79], v[78:79], v[80:81]
	v_pk_mul_f32 v[74:75], s[0:1], v[74:75] op_sel_hi:[0,1]
	v_pk_fma_f32 v[76:77], v[92:93], v[78:79], v[76:77] neg_lo:[1,0,0] neg_hi:[1,0,0]
	v_pk_fma_f32 v[92:93], v[74:75], v[44:45], v[48:49]
	v_cvt_pk_f16_f32 v80, v76, v77
	v_fma_f32 v74, |v92|, s25, 1.0
	v_fma_f32 v75, |v93|, s25, 1.0
	v_rcp_f32_e32 v74, v74
	v_rcp_f32_e32 v75, v75
	v_pk_mul_f32 v[76:77], v[92:93], v[92:93]
	s_waitcnt vmcnt(0)
	v_add_f32_e32 v101, v52, v53
	v_mul_f32_e32 v76, 0xbf38aa3b, v76
	v_pk_fma_f32 v[78:79], v[74:75], s[22:23], v[90:91] op_sel_hi:[1,0,0]
	v_exp_f32_e32 v96, v76
	v_pk_fma_f32 v[78:79], v[74:75], v[78:79], s[24:25] op_sel_hi:[1,1,0]
	v_add_f32_e32 v76, v88, v89
	v_pk_fma_f32 v[78:79], v[74:75], v[78:79], s[34:35] op_sel_hi:[1,1,0]
	v_mul_f32_e32 v81, 0xbf38aa3b, v77
	v_pk_fma_f32 v[78:79], v[74:75], v[78:79], s[40:41] op_sel_hi:[1,1,0]
	v_add_f32_e32 v77, v84, v85
	v_pk_mul_f32 v[98:99], v[74:75], v[78:79]
	v_add_f32_e32 v74, v70, v71
	v_add_f32_e32 v75, v72, v73
	v_add_f32_e32 v74, v74, v75
	v_add_f32_e32 v75, v86, v87
	v_add_f32_e32 v75, v75, v76
	v_add_f32_e32 v76, v82, v83
	v_add_f32_e32 v76, v76, v77
	v_add_f32_e32 v77, v66, v67
	v_add_f32_e32 v78, v68, v69
	v_add_f32_e32 v77, v77, v78
	v_add_f32_e32 v78, v58, v59
	v_add_f32_e32 v79, v60, v61
	v_add_f32_e32 v78, v78, v79
	v_add_f32_e32 v79, v62, v63
	v_add_f32_e32 v79, v79, v97
	v_add_f32_e32 v97, v54, v55
	v_add_f32_e32 v97, v97, v100
	v_add_f32_e32 v100, v50, v51
	v_add_f32_e32 v100, v100, v101
	v_cndmask_b32_e64 v101, v75, v74, s[4:5]
	v_cndmask_b32_e64 v74, v74, v75, s[4:5]
	v_cndmask_b32_e64 v75, v77, v76, s[4:5]
	v_cndmask_b32_e64 v76, v76, v77, s[4:5]
	v_cndmask_b32_e64 v77, v78, v79, s[4:5]
	v_add_f32_dpp v74, v101, v74 quad_perm:[1,0,3,2] row_mask:0xf bank_mask:0xf bound_ctrl:1
	v_add_f32_dpp v75, v75, v76 quad_perm:[1,0,3,2] row_mask:0xf bank_mask:0xf bound_ctrl:1
	v_cndmask_b32_e64 v76, v79, v78, s[4:5]
	v_cndmask_b32_e64 v78, v97, v100, s[4:5]
	v_and_b32_e32 v95, 0x7fffffff, v93
	v_add_f32_dpp v76, v76, v77 quad_perm:[1,0,3,2] row_mask:0xf bank_mask:0xf bound_ctrl:1
	v_cndmask_b32_e64 v77, v100, v97, s[4:5]
	v_exp_f32_e32 v97, v81
	v_and_b32_e32 v94, 0x7fffffff, v92
	v_add_f32_dpp v77, v77, v78 quad_perm:[1,0,3,2] row_mask:0xf bank_mask:0xf bound_ctrl:1
	v_cndmask_b32_e64 v78, v74, v75, s[6:7]
	v_cndmask_b32_e64 v74, v75, v74, s[6:7]
	v_cndmask_b32_e64 v75, v76, v77, s[6:7]
	v_cndmask_b32_e64 v76, v77, v76, s[6:7]
	v_add_f32_dpp v74, v78, v74 quad_perm:[2,3,0,1] row_mask:0xf bank_mask:0xf bound_ctrl:1
	v_max_f32_e32 v92, 0, v92
	v_add_f32_dpp v75, v75, v76 quad_perm:[2,3,0,1] row_mask:0xf bank_mask:0xf bound_ctrl:1
	v_cndmask_b32_e64 v76, v74, v75, s[8:9]
	v_cndmask_b32_e64 v74, v75, v74, s[8:9]
	v_mov_b32_e32 v75, v76
	v_max_f32_e32 v93, 0, v93
	s_waitcnt lgkmcnt(14)
	v_dot2c_f32_f16_e32 v104, v38, v38
	v_mov_b32_dpp v75, v75 row_shl:4 row_mask:0xf bank_mask:0x5
	v_mov_b32_e32 v105, 0
	v_dot2c_f32_f16_e32 v104, v39, v39
	v_mov_b32_dpp v75, v76 row_shr:4 row_mask:0xf bank_mask:0xa
	v_add_f32_e32 v74, v74, v75
	v_dot2c_f32_f16_e32 v104, v40, v40
	v_dot2c_f32_f16_e32 v104, v41, v41
	v_add_f32_dpp v74, v74, v74 row_ror:8 row_mask:0xf bank_mask:0xf bound_ctrl:1
	v_mov_b32_e32 v75, v74
	s_nop 1
	v_permlane16_swap_b32_e32 v74, v75
	v_add_f32_e32 v74, v74, v75
	v_mov_b32_e32 v75, v74
	s_nop 1
	v_permlane32_swap_b32_e32 v74, v75
	v_add_f32_e32 v74, v74, v75
	v_mul_f32_e32 v74, 0x3b800000, v74
	s_waitcnt lgkmcnt(13)
	v_dot2c_f32_f16_e32 v104, v34, v34
	v_readlane_b32 s42, v74, 0
	v_readlane_b32 s44, v74, 1
	v_readlane_b32 s46, v74, 2
	v_pk_add_f32 v[102:103], v[72:73], s[42:43] op_sel_hi:[1,0] neg_lo:[0,1] neg_hi:[0,1]
	v_pk_add_f32 v[78:79], v[88:89], s[44:45] op_sel_hi:[1,0] neg_lo:[0,1] neg_hi:[0,1]
	v_pk_add_f32 v[100:101], v[70:71], s[42:43] op_sel_hi:[1,0] neg_lo:[0,1] neg_hi:[0,1]
	v_mul_f32_e32 v70, v103, v103
	v_mul_f32_e32 v71, v79, v79
	v_fmac_f32_e32 v70, v102, v102
	v_pk_add_f32 v[86:87], v[86:87], s[44:45] op_sel_hi:[1,0] neg_lo:[0,1] neg_hi:[0,1]
	v_fmac_f32_e32 v71, v78, v78
	v_fmac_f32_e32 v70, v101, v101
	v_fmac_f32_e32 v71, v87, v87
	v_fmac_f32_e32 v70, v100, v100
	v_fmac_f32_e32 v71, v86, v86
	v_readlane_b32 s48, v74, 3
	v_cndmask_b32_e64 v72, v71, v70, s[4:5]
	v_cndmask_b32_e64 v70, v70, v71, s[4:5]
	v_readlane_b32 s50, v74, 4
	v_readlane_b32 s52, v74, 5
	v_readlane_b32 s54, v74, 6
	v_readlane_b32 s0, v74, 7
	v_add_f32_dpp v88, v72, v70 quad_perm:[1,0,3,2] row_mask:0xf bank_mask:0xf bound_ctrl:1
	v_pk_add_f32 v[74:75], v[84:85], s[46:47] op_sel_hi:[1,0] neg_lo:[0,1] neg_hi:[0,1]
	v_pk_add_f32 v[70:71], v[68:69], s[48:49] op_sel_hi:[1,0] neg_lo:[0,1] neg_hi:[0,1]
	v_pk_add_f32 v[76:77], v[82:83], s[46:47] op_sel_hi:[1,0] neg_lo:[0,1] neg_hi:[0,1]
	v_mul_f32_e32 v82, v75, v75
	v_pk_add_f32 v[72:73], v[66:67], s[48:49] op_sel_hi:[1,0] neg_lo:[0,1] neg_hi:[0,1]
	v_mul_f32_e32 v66, v71, v71
	v_fmac_f32_e32 v82, v74, v74
	v_fmac_f32_e32 v66, v70, v70
	v_fmac_f32_e32 v82, v77, v77
	v_fmac_f32_e32 v66, v73, v73
	v_fmac_f32_e32 v82, v76, v76
	v_fmac_f32_e32 v66, v72, v72
	v_cndmask_b32_e64 v67, v66, v82, s[4:5]
	v_cndmask_b32_e64 v66, v82, v66, s[4:5]
	v_pk_add_f32 v[68:69], v[58:59], s[50:51] op_sel_hi:[1,0] neg_lo:[0,1] neg_hi:[0,1]
	v_pk_add_f32 v[62:63], v[62:63], s[52:53] op_sel_hi:[1,0] neg_lo:[0,1] neg_hi:[0,1]
	v_add_f32_dpp v66, v67, v66 quad_perm:[1,0,3,2] row_mask:0xf bank_mask:0xf bound_ctrl:1
	v_cndmask_b32_e64 v67, v88, v66, s[6:7]
	v_cndmask_b32_e64 v66, v66, v88, s[6:7]
	v_pk_add_f32 v[56:57], v[56:57], s[54:55] op_sel_hi:[1,0] neg_lo:[0,1] neg_hi:[0,1]
	v_dot2c_f32_f16_e32 v104, v35, v35
	v_add_f32_dpp v82, v67, v66 quad_perm:[2,3,0,1] row_mask:0xf bank_mask:0xf bound_ctrl:1
	v_pk_add_f32 v[66:67], v[60:61], s[50:51] op_sel_hi:[1,0] neg_lo:[0,1] neg_hi:[0,1]
	v_pk_add_f32 v[60:61], v[64:65], s[52:53] op_sel_hi:[1,0] neg_lo:[0,1] neg_hi:[0,1]
	v_mul_f32_e32 v58, v67, v67
	v_mul_f32_e32 v59, v61, v61
	v_fmac_f32_e32 v58, v66, v66
	v_fmac_f32_e32 v59, v60, v60
	v_fmac_f32_e32 v58, v69, v69
	v_fmac_f32_e32 v59, v63, v63
	v_fmac_f32_e32 v58, v68, v68
	v_fmac_f32_e32 v59, v62, v62
	v_cndmask_b32_e64 v64, v59, v58, s[4:5]
	v_cndmask_b32_e64 v58, v58, v59, s[4:5]
	v_mul_f32_e32 v65, v57, v57
	v_fmac_f32_e32 v65, v56, v56
	v_add_f32_dpp v64, v64, v58 quad_perm:[1,0,3,2] row_mask:0xf bank_mask:0xf bound_ctrl:1
	v_pk_add_f32 v[58:59], v[54:55], s[54:55] op_sel_hi:[1,0] neg_lo:[0,1] neg_hi:[0,1]
	v_pk_add_f32 v[54:55], v[50:51], s[0:1] op_sel_hi:[1,0] neg_lo:[0,1] neg_hi:[0,1]
	v_pk_add_f32 v[50:51], v[52:53], s[0:1] op_sel_hi:[1,0] neg_lo:[0,1] neg_hi:[0,1]
	v_fmac_f32_e32 v65, v59, v59
	v_mul_f32_e32 v52, v51, v51
	v_fmac_f32_e32 v52, v50, v50
	v_fmac_f32_e32 v52, v55, v55
	v_fmac_f32_e32 v65, v58, v58
	v_fmac_f32_e32 v52, v54, v54
	v_cndmask_b32_e64 v53, v52, v65, s[4:5]
	v_cndmask_b32_e64 v52, v65, v52, s[4:5]
	v_dot2c_f32_f16_e32 v104, v36, v36
	v_dot2c_f32_f16_e32 v104, v37, v37
	v_add_f32_dpp v52, v53, v52 quad_perm:[1,0,3,2] row_mask:0xf bank_mask:0xf bound_ctrl:1
	v_cndmask_b32_e64 v53, v64, v52, s[6:7]
	v_cndmask_b32_e64 v52, v52, v64, s[6:7]
	s_waitcnt lgkmcnt(12)
	v_dot2c_f32_f16_e32 v104, v30, v30
	v_dot2c_f32_f16_e32 v104, v31, v31
	v_add_f32_dpp v52, v53, v52 quad_perm:[2,3,0,1] row_mask:0xf bank_mask:0xf bound_ctrl:1
	v_cndmask_b32_e64 v53, v82, v52, s[8:9]
	v_mov_b32_e32 v64, v53
	v_cndmask_b32_e64 v52, v52, v82, s[8:9]
	v_dot2c_f32_f16_e32 v104, v32, v32
	v_mov_b32_dpp v64, v64 row_shl:4 row_mask:0xf bank_mask:0x5
	v_dot2c_f32_f16_e32 v104, v33, v33
	s_waitcnt lgkmcnt(11)
	v_dot2c_f32_f16_e32 v104, v26, v26
	v_mov_b32_dpp v64, v53 row_shr:4 row_mask:0xf bank_mask:0xa
	v_add_f32_e32 v52, v52, v64
	v_dot2c_f32_f16_e32 v104, v27, v27
	v_dot2c_f32_f16_e32 v104, v28, v28
	v_add_f32_dpp v52, v52, v52 row_ror:8 row_mask:0xf bank_mask:0xf bound_ctrl:1
	v_mov_b32_e32 v53, v52
	s_nop 1
	v_permlane16_swap_b32_e32 v52, v53
	v_add_f32_e32 v52, v52, v53
	v_mov_b32_e32 v53, v52
	s_nop 1
	v_permlane32_swap_b32_e32 v52, v53
	v_add_f32_e32 v52, v52, v53
	v_fmac_f32_e32 v116, 0x3b800000, v52
	v_mul_f32_e32 v52, 0x4f800000, v116
	v_cmp_gt_f32_e32 vcc, s35, v116
	v_dot2c_f32_f16_e32 v104, v29, v29
	s_waitcnt lgkmcnt(10)
	v_dot2c_f32_f16_e32 v104, v22, v22
	v_cndmask_b32_e32 v64, v116, v52, vcc
	v_sqrt_f32_e32 v65, v64
	v_pk_mul_f32 v[52:53], v[94:95], v[98:99]
	v_and_b32_e32 v94, 48, v0
	v_pk_fma_f32 v[52:53], v[96:97], v[52:53], v[92:93] neg_lo:[1,0,0] neg_hi:[1,0,0]
	v_add_u32_e32 v81, -1, v65
	v_fma_f32 v82, -v81, v65, v64
	v_cmp_ge_f32_e64 s[0:1], 0, v82
	v_add_u32_e32 v82, 1, v65
	v_add_u32_e32 v95, 0x19860, v94
	v_cndmask_b32_e64 v81, v65, v81, s[0:1]
	v_fma_f32 v65, -v82, v65, v64
	v_cmp_lt_f32_e64 s[0:1], 0, v65
	v_dot2c_f32_f16_e32 v104, v23, v23
	v_dot2c_f32_f16_e32 v104, v24, v24
	v_cndmask_b32_e64 v65, v81, v82, s[0:1]
	v_mul_f32_e32 v81, 0x37800000, v65
	v_cndmask_b32_e32 v65, v65, v81, vcc
	v_cmp_class_f32_e32 vcc, v64, v117
	v_cvt_pk_f16_f32 v81, v52, v53
	ds_write_b64 v144, v[80:81] offset:36352
	v_cndmask_b32_e32 v64, v65, v64, vcc
	v_div_scale_f32 v65, s[0:1], v64, v64, 1.0
	v_rcp_f32_e32 v82, v65
	v_dot2c_f32_f16_e32 v104, v25, v25
	s_waitcnt lgkmcnt(10)
	v_dot2c_f32_f16_e32 v104, v18, v18
	v_dot2c_f32_f16_e32 v104, v19, v19
	v_fma_f32 v52, -v65, v82, 1.0
	v_fmac_f32_e32 v82, v52, v82
	v_div_scale_f32 v52, vcc, 1.0, v64, 1.0
	v_mul_f32_e32 v53, v52, v82
	v_fma_f32 v80, -v65, v53, v52
	v_fmac_f32_e32 v53, v80, v82
	v_fma_f32 v52, -v65, v53, v52
	v_div_fmas_f32 v52, v52, v82, v53
	v_div_fixup_f32 v52, v52, v64, 1.0
	v_dot2c_f32_f16_e32 v104, v20, v20
	v_readlane_b32 s0, v52, 0
	v_dot2c_f32_f16_e32 v104, v21, v21
	s_waitcnt lgkmcnt(9)
	v_dot2c_f32_f16_e32 v104, v14, v14
	v_pk_mul_f32 v[64:65], s[0:1], v[100:101] op_sel_hi:[0,1]
	v_pk_fma_f32 v[64:65], v[64:65], v[42:43], v[46:47]
	v_dot2c_f32_f16_e32 v104, v15, v15
	v_fma_f32 v53, |v64|, s25, 1.0
	v_rcp_f32_e32 v82, v53
	v_fma_f32 v53, |v65|, s25, 1.0
	v_rcp_f32_e32 v83, v53
	v_pk_mul_f32 v[84:85], v[64:65], v[64:65]
	v_and_b32_e32 v81, 0x7fffffff, v65
	v_mul_f32_e32 v53, 0xbf38aa3b, v84
	v_pk_fma_f32 v[88:89], v[82:83], s[22:23], v[90:91] op_sel_hi:[1,0,0]
	v_exp_f32_e32 v84, v53
	v_pk_fma_f32 v[88:89], v[82:83], v[88:89], s[24:25] op_sel_hi:[1,1,0]
	v_mul_f32_e32 v53, 0xbf38aa3b, v85
	v_pk_fma_f32 v[88:89], v[82:83], v[88:89], s[34:35] op_sel_hi:[1,1,0]
	v_exp_f32_e32 v85, v53
	v_pk_fma_f32 v[88:89], v[82:83], v[88:89], s[40:41] op_sel_hi:[1,1,0]
	v_and_b32_e32 v80, 0x7fffffff, v64
	v_pk_mul_f32 v[82:83], v[82:83], v[88:89]
	v_max_f32_e32 v64, 0, v64
	v_max_f32_e32 v65, 0, v65
	v_pk_mul_f32 v[80:81], v[80:81], v[82:83]
	v_dot2c_f32_f16_e32 v104, v16, v16
	v_pk_fma_f32 v[64:65], v[84:85], v[80:81], v[64:65] neg_lo:[1,0,0] neg_hi:[1,0,0]
	v_pk_mul_f32 v[80:81], s[0:1], v[102:103] op_sel_hi:[0,1]
	v_pk_fma_f32 v[80:81], v[80:81], v[44:45], v[48:49]
	v_cvt_pk_f16_f32 v64, v64, v65
	v_fma_f32 v53, |v80|, s25, 1.0
	v_rcp_f32_e32 v84, v53
	v_fma_f32 v53, |v81|, s25, 1.0
	v_rcp_f32_e32 v85, v53
	v_pk_mul_f32 v[88:89], v[80:81], v[80:81]
	v_and_b32_e32 v83, 0x7fffffff, v81
	v_mul_f32_e32 v53, 0xbf38aa3b, v88
	v_pk_fma_f32 v[92:93], v[84:85], s[22:23], v[90:91] op_sel_hi:[1,0,0]
	v_exp_f32_e32 v88, v53
	v_pk_fma_f32 v[92:93], v[84:85], v[92:93], s[24:25] op_sel_hi:[1,1,0]
	v_mul_f32_e32 v53, 0xbf38aa3b, v89
	v_pk_fma_f32 v[92:93], v[84:85], v[92:93], s[34:35] op_sel_hi:[1,1,0]
	v_exp_f32_e32 v89, v53
	v_pk_fma_f32 v[92:93], v[84:85], v[92:93], s[40:41] op_sel_hi:[1,1,0]
	v_and_b32_e32 v82, 0x7fffffff, v80
	v_pk_mul_f32 v[84:85], v[84:85], v[92:93]
	v_max_f32_e32 v80, 0, v80
	v_max_f32_e32 v81, 0, v81
	v_pk_mul_f32 v[82:83], v[82:83], v[84:85]
	v_readlane_b32 s0, v52, 1
	v_pk_fma_f32 v[80:81], v[88:89], v[82:83], v[80:81] neg_lo:[1,0,0] neg_hi:[1,0,0]
	v_dot2c_f32_f16_e32 v104, v17, v17
	v_cvt_pk_f16_f32 v65, v80, v81
	ds_write_b64 v145, v[64:65] offset:36864
	v_pk_mul_f32 v[64:65], s[0:1], v[86:87] op_sel_hi:[0,1]
	v_pk_fma_f32 v[64:65], v[64:65], v[42:43], v[46:47]
	v_pk_mul_f32 v[78:79], s[0:1], v[78:79] op_sel_hi:[0,1]
	v_fma_f32 v53, |v64|, s25, 1.0
	v_rcp_f32_e32 v82, v53
	v_fma_f32 v53, |v65|, s25, 1.0
	v_rcp_f32_e32 v83, v53
	v_pk_mul_f32 v[84:85], v[64:65], v[64:65]
	v_pk_fma_f32 v[78:79], v[78:79], v[44:45], v[48:49]
	v_mul_f32_e32 v53, 0xbf38aa3b, v84
	v_pk_fma_f32 v[86:87], v[82:83], s[22:23], v[90:91] op_sel_hi:[1,0,0]
	v_exp_f32_e32 v84, v53
	v_pk_fma_f32 v[86:87], v[82:83], v[86:87], s[24:25] op_sel_hi:[1,1,0]
	v_mul_f32_e32 v53, 0xbf38aa3b, v85
	v_pk_fma_f32 v[86:87], v[82:83], v[86:87], s[34:35] op_sel_hi:[1,1,0]
	v_and_b32_e32 v81, 0x7fffffff, v65
	v_pk_fma_f32 v[86:87], v[82:83], v[86:87], s[40:41] op_sel_hi:[1,1,0]
	v_and_b32_e32 v80, 0x7fffffff, v64
	v_exp_f32_e32 v85, v53
	v_pk_mul_f32 v[82:83], v[82:83], v[86:87]
	v_fma_f32 v53, |v78|, s25, 1.0
	v_pk_mul_f32 v[80:81], v[80:81], v[82:83]
	v_rcp_f32_e32 v82, v53
	v_fma_f32 v53, |v79|, s25, 1.0
	v_rcp_f32_e32 v83, v53
	v_max_f32_e32 v64, 0, v64
	v_max_f32_e32 v65, 0, v65
	v_pk_fma_f32 v[64:65], v[84:85], v[80:81], v[64:65] neg_lo:[1,0,0] neg_hi:[1,0,0]
	v_pk_mul_f32 v[84:85], v[78:79], v[78:79]
	v_pk_fma_f32 v[86:87], v[82:83], s[22:23], v[90:91] op_sel_hi:[1,0,0]
	v_mul_f32_e32 v53, 0xbf38aa3b, v84
	v_exp_f32_e32 v84, v53
	v_pk_fma_f32 v[86:87], v[82:83], v[86:87], s[24:25] op_sel_hi:[1,1,0]
	v_mul_f32_e32 v53, 0xbf38aa3b, v85
	v_pk_fma_f32 v[86:87], v[82:83], v[86:87], s[34:35] op_sel_hi:[1,1,0]
	v_exp_f32_e32 v85, v53
	v_pk_fma_f32 v[86:87], v[82:83], v[86:87], s[40:41] op_sel_hi:[1,1,0]
	v_and_b32_e32 v81, 0x7fffffff, v79
	v_and_b32_e32 v80, 0x7fffffff, v78
	v_pk_mul_f32 v[82:83], v[82:83], v[86:87]
	v_max_f32_e32 v78, 0, v78
	v_max_f32_e32 v79, 0, v79
	v_pk_mul_f32 v[80:81], v[80:81], v[82:83]
	v_cvt_pk_f16_f32 v64, v64, v65
	v_pk_fma_f32 v[78:79], v[84:85], v[80:81], v[78:79] neg_lo:[1,0,0] neg_hi:[1,0,0]
	v_readlane_b32 s0, v52, 2
	v_cvt_pk_f16_f32 v65, v78, v79
	ds_write_b64 v139, v[64:65] offset:37376
	v_pk_mul_f32 v[64:65], s[0:1], v[76:77] op_sel_hi:[0,1]
	v_pk_fma_f32 v[64:65], v[64:65], v[42:43], v[46:47]
	v_pk_mul_f32 v[74:75], s[0:1], v[74:75] op_sel_hi:[0,1]
	v_fma_f32 v53, |v64|, s25, 1.0
	v_rcp_f32_e32 v78, v53
	v_fma_f32 v53, |v65|, s25, 1.0
	v_rcp_f32_e32 v79, v53
	v_pk_mul_f32 v[80:81], v[64:65], v[64:65]
	v_pk_fma_f32 v[74:75], v[74:75], v[44:45], v[48:49]
	v_mul_f32_e32 v53, 0xbf38aa3b, v80
	v_pk_fma_f32 v[82:83], v[78:79], s[22:23], v[90:91] op_sel_hi:[1,0,0]
	v_exp_f32_e32 v80, v53
	v_pk_fma_f32 v[82:83], v[78:79], v[82:83], s[24:25] op_sel_hi:[1,1,0]
	v_mul_f32_e32 v53, 0xbf38aa3b, v81
	v_pk_fma_f32 v[82:83], v[78:79], v[82:83], s[34:35] op_sel_hi:[1,1,0]
	v_and_b32_e32 v77, 0x7fffffff, v65
	v_pk_fma_f32 v[82:83], v[78:79], v[82:83], s[40:41] op_sel_hi:[1,1,0]
	v_and_b32_e32 v76, 0x7fffffff, v64
	v_exp_f32_e32 v81, v53
	v_pk_mul_f32 v[78:79], v[78:79], v[82:83]
	v_fma_f32 v53, |v74|, s25, 1.0
	v_pk_mul_f32 v[76:77], v[76:77], v[78:79]
	v_rcp_f32_e32 v78, v53
	v_fma_f32 v53, |v75|, s25, 1.0
	v_rcp_f32_e32 v79, v53
	v_max_f32_e32 v64, 0, v64
	v_max_f32_e32 v65, 0, v65
	v_pk_fma_f32 v[64:65], v[80:81], v[76:77], v[64:65] neg_lo:[1,0,0] neg_hi:[1,0,0]
	v_pk_mul_f32 v[80:81], v[74:75], v[74:75]
	v_pk_fma_f32 v[82:83], v[78:79], s[22:23], v[90:91] op_sel_hi:[1,0,0]
	v_mul_f32_e32 v53, 0xbf38aa3b, v80
	v_exp_f32_e32 v80, v53
	v_pk_fma_f32 v[82:83], v[78:79], v[82:83], s[24:25] op_sel_hi:[1,1,0]
	v_mul_f32_e32 v53, 0xbf38aa3b, v81
	v_pk_fma_f32 v[82:83], v[78:79], v[82:83], s[34:35] op_sel_hi:[1,1,0]
	v_exp_f32_e32 v81, v53
	v_pk_fma_f32 v[82:83], v[78:79], v[82:83], s[40:41] op_sel_hi:[1,1,0]
	v_and_b32_e32 v77, 0x7fffffff, v75
	v_and_b32_e32 v76, 0x7fffffff, v74
	v_pk_mul_f32 v[78:79], v[78:79], v[82:83]
	v_max_f32_e32 v74, 0, v74
	v_max_f32_e32 v75, 0, v75
	v_pk_mul_f32 v[76:77], v[76:77], v[78:79]
	v_cvt_pk_f16_f32 v64, v64, v65
	v_pk_fma_f32 v[74:75], v[80:81], v[76:77], v[74:75] neg_lo:[1,0,0] neg_hi:[1,0,0]
	v_readlane_b32 s0, v52, 3
	v_cvt_pk_f16_f32 v65, v74, v75
	ds_write_b64 v137, v[64:65] offset:37888
	v_pk_mul_f32 v[64:65], s[0:1], v[72:73] op_sel_hi:[0,1]
	v_pk_fma_f32 v[64:65], v[64:65], v[42:43], v[46:47]
	v_pk_mul_f32 v[70:71], s[0:1], v[70:71] op_sel_hi:[0,1]
	v_fma_f32 v53, |v64|, s25, 1.0
	v_rcp_f32_e32 v74, v53
	v_fma_f32 v53, |v65|, s25, 1.0
	v_rcp_f32_e32 v75, v53
	v_pk_mul_f32 v[76:77], v[64:65], v[64:65]
	v_pk_fma_f32 v[70:71], v[70:71], v[44:45], v[48:49]
	v_mul_f32_e32 v53, 0xbf38aa3b, v76
	v_pk_fma_f32 v[78:79], v[74:75], s[22:23], v[90:91] op_sel_hi:[1,0,0]
	v_exp_f32_e32 v76, v53
	v_pk_fma_f32 v[78:79], v[74:75], v[78:79], s[24:25] op_sel_hi:[1,1,0]
	v_mul_f32_e32 v53, 0xbf38aa3b, v77
	v_pk_fma_f32 v[78:79], v[74:75], v[78:79], s[34:35] op_sel_hi:[1,1,0]
	v_and_b32_e32 v73, 0x7fffffff, v65
	v_pk_fma_f32 v[78:79], v[74:75], v[78:79], s[40:41] op_sel_hi:[1,1,0]
	v_and_b32_e32 v72, 0x7fffffff, v64
	v_exp_f32_e32 v77, v53
	v_pk_mul_f32 v[74:75], v[74:75], v[78:79]
	v_fma_f32 v53, |v70|, s25, 1.0
	v_pk_mul_f32 v[72:73], v[72:73], v[74:75]
	v_rcp_f32_e32 v74, v53
	v_fma_f32 v53, |v71|, s25, 1.0
	v_rcp_f32_e32 v75, v53
	v_max_f32_e32 v64, 0, v64
	v_max_f32_e32 v65, 0, v65
	v_pk_fma_f32 v[64:65], v[76:77], v[72:73], v[64:65] neg_lo:[1,0,0] neg_hi:[1,0,0]
	v_pk_mul_f32 v[76:77], v[70:71], v[70:71]
	v_pk_fma_f32 v[78:79], v[74:75], s[22:23], v[90:91] op_sel_hi:[1,0,0]
	v_mul_f32_e32 v53, 0xbf38aa3b, v76
	v_exp_f32_e32 v76, v53
	v_pk_fma_f32 v[78:79], v[74:75], v[78:79], s[24:25] op_sel_hi:[1,1,0]
	v_mul_f32_e32 v53, 0xbf38aa3b, v77
	v_pk_fma_f32 v[78:79], v[74:75], v[78:79], s[34:35] op_sel_hi:[1,1,0]
	v_exp_f32_e32 v77, v53
	v_pk_fma_f32 v[78:79], v[74:75], v[78:79], s[40:41] op_sel_hi:[1,1,0]
	v_and_b32_e32 v73, 0x7fffffff, v71
	v_and_b32_e32 v72, 0x7fffffff, v70
	v_pk_mul_f32 v[74:75], v[74:75], v[78:79]
	v_max_f32_e32 v70, 0, v70
	v_max_f32_e32 v71, 0, v71
	v_pk_mul_f32 v[72:73], v[72:73], v[74:75]
	v_cvt_pk_f16_f32 v64, v64, v65
	v_pk_fma_f32 v[70:71], v[76:77], v[72:73], v[70:71] neg_lo:[1,0,0] neg_hi:[1,0,0]
	v_readlane_b32 s0, v52, 4
	v_cvt_pk_f16_f32 v65, v70, v71
	ds_write_b64 v136, v[64:65] offset:38400
	v_pk_mul_f32 v[64:65], s[0:1], v[68:69] op_sel_hi:[0,1]
	v_pk_fma_f32 v[64:65], v[64:65], v[42:43], v[46:47]
	v_pk_mul_f32 v[66:67], s[0:1], v[66:67] op_sel_hi:[0,1]
	v_fma_f32 v53, |v64|, s25, 1.0
	v_rcp_f32_e32 v70, v53
	v_fma_f32 v53, |v65|, s25, 1.0
	v_rcp_f32_e32 v71, v53
	v_pk_mul_f32 v[72:73], v[64:65], v[64:65]
	v_pk_fma_f32 v[66:67], v[66:67], v[44:45], v[48:49]
	v_mul_f32_e32 v53, 0xbf38aa3b, v72
	v_pk_fma_f32 v[74:75], v[70:71], s[22:23], v[90:91] op_sel_hi:[1,0,0]
	v_exp_f32_e32 v72, v53
	v_pk_fma_f32 v[74:75], v[70:71], v[74:75], s[24:25] op_sel_hi:[1,1,0]
	v_mul_f32_e32 v53, 0xbf38aa3b, v73
	v_pk_fma_f32 v[74:75], v[70:71], v[74:75], s[34:35] op_sel_hi:[1,1,0]
	v_and_b32_e32 v69, 0x7fffffff, v65
	v_pk_fma_f32 v[74:75], v[70:71], v[74:75], s[40:41] op_sel_hi:[1,1,0]
	v_and_b32_e32 v68, 0x7fffffff, v64
	v_exp_f32_e32 v73, v53
	v_pk_mul_f32 v[70:71], v[70:71], v[74:75]
	v_fma_f32 v53, |v66|, s25, 1.0
	v_pk_mul_f32 v[68:69], v[68:69], v[70:71]
	v_rcp_f32_e32 v70, v53
	v_fma_f32 v53, |v67|, s25, 1.0
	v_rcp_f32_e32 v71, v53
	v_max_f32_e32 v64, 0, v64
	v_max_f32_e32 v65, 0, v65
	v_pk_fma_f32 v[64:65], v[72:73], v[68:69], v[64:65] neg_lo:[1,0,0] neg_hi:[1,0,0]
	v_pk_mul_f32 v[72:73], v[66:67], v[66:67]
	v_pk_fma_f32 v[74:75], v[70:71], s[22:23], v[90:91] op_sel_hi:[1,0,0]
	v_mul_f32_e32 v53, 0xbf38aa3b, v72
	v_exp_f32_e32 v72, v53
	v_pk_fma_f32 v[74:75], v[70:71], v[74:75], s[24:25] op_sel_hi:[1,1,0]
	v_mul_f32_e32 v53, 0xbf38aa3b, v73
	v_pk_fma_f32 v[74:75], v[70:71], v[74:75], s[34:35] op_sel_hi:[1,1,0]
	v_exp_f32_e32 v73, v53
	v_pk_fma_f32 v[74:75], v[70:71], v[74:75], s[40:41] op_sel_hi:[1,1,0]
	v_readlane_b32 s0, v52, 5
	v_and_b32_e32 v69, 0x7fffffff, v67
	v_and_b32_e32 v68, 0x7fffffff, v66
	v_pk_mul_f32 v[70:71], v[70:71], v[74:75]
	v_pk_mul_f32 v[62:63], s[0:1], v[62:63] op_sel_hi:[0,1]
	v_max_f32_e32 v66, 0, v66
	v_max_f32_e32 v67, 0, v67
	v_pk_mul_f32 v[68:69], v[68:69], v[70:71]
	v_pk_fma_f32 v[62:63], v[62:63], v[42:43], v[46:47]
	v_pk_fma_f32 v[66:67], v[72:73], v[68:69], v[66:67] neg_lo:[1,0,0] neg_hi:[1,0,0]
	v_fma_f32 v53, |v62|, s25, 1.0
	v_cvt_pk_f16_f32 v64, v64, v65
	v_cvt_pk_f16_f32 v65, v66, v67
	v_rcp_f32_e32 v66, v53
	v_fma_f32 v53, |v63|, s25, 1.0
	v_rcp_f32_e32 v67, v53
	v_pk_mul_f32 v[68:69], v[62:63], v[62:63]
	v_pk_mul_f32 v[60:61], s[0:1], v[60:61] op_sel_hi:[0,1]
	v_mul_f32_e32 v53, 0xbf38aa3b, v68
	v_pk_fma_f32 v[70:71], v[66:67], s[22:23], v[90:91] op_sel_hi:[1,0,0]
	v_exp_f32_e32 v68, v53
	v_pk_fma_f32 v[70:71], v[66:67], v[70:71], s[24:25] op_sel_hi:[1,1,0]
	v_mul_f32_e32 v53, 0xbf38aa3b, v69
	v_pk_fma_f32 v[70:71], v[66:67], v[70:71], s[34:35] op_sel_hi:[1,1,0]
	v_pk_fma_f32 v[60:61], v[60:61], v[44:45], v[48:49]
	v_pk_fma_f32 v[70:71], v[66:67], v[70:71], s[40:41] op_sel_hi:[1,1,0]
	ds_write_b64 v123, v[64:65] offset:38912
	v_and_b32_e32 v65, 0x7fffffff, v63
	v_and_b32_e32 v64, 0x7fffffff, v62
	v_exp_f32_e32 v69, v53
	v_pk_mul_f32 v[66:67], v[66:67], v[70:71]
	v_fma_f32 v53, |v60|, s25, 1.0
	v_pk_mul_f32 v[64:65], v[64:65], v[66:67]
	v_rcp_f32_e32 v66, v53
	v_fma_f32 v53, |v61|, s25, 1.0
	v_rcp_f32_e32 v67, v53
	v_max_f32_e32 v62, 0, v62
	v_max_f32_e32 v63, 0, v63
	v_pk_fma_f32 v[62:63], v[68:69], v[64:65], v[62:63] neg_lo:[1,0,0] neg_hi:[1,0,0]
	v_pk_mul_f32 v[68:69], v[60:61], v[60:61]
	v_pk_fma_f32 v[70:71], v[66:67], s[22:23], v[90:91] op_sel_hi:[1,0,0]
	v_mul_f32_e32 v53, 0xbf38aa3b, v68
	v_exp_f32_e32 v68, v53
	v_pk_fma_f32 v[70:71], v[66:67], v[70:71], s[24:25] op_sel_hi:[1,1,0]
	v_mul_f32_e32 v53, 0xbf38aa3b, v69
	v_pk_fma_f32 v[70:71], v[66:67], v[70:71], s[34:35] op_sel_hi:[1,1,0]
	v_exp_f32_e32 v69, v53
	v_pk_fma_f32 v[70:71], v[66:67], v[70:71], s[40:41] op_sel_hi:[1,1,0]
	v_and_b32_e32 v65, 0x7fffffff, v61
	v_and_b32_e32 v64, 0x7fffffff, v60
	v_pk_mul_f32 v[66:67], v[66:67], v[70:71]
	v_readlane_b32 s0, v52, 6
	v_max_f32_e32 v60, 0, v60
	v_max_f32_e32 v61, 0, v61
	v_pk_mul_f32 v[64:65], v[64:65], v[66:67]
	v_pk_mul_f32 v[58:59], s[0:1], v[58:59] op_sel_hi:[0,1]
	v_pk_fma_f32 v[60:61], v[68:69], v[64:65], v[60:61] neg_lo:[1,0,0] neg_hi:[1,0,0]
	v_pk_fma_f32 v[58:59], v[58:59], v[42:43], v[46:47]
	v_cvt_pk_f16_f32 v62, v62, v63
	v_cvt_pk_f16_f32 v63, v60, v61
	v_fma_f32 v53, |v58|, s25, 1.0
	ds_write_b64 v133, v[62:63] offset:39424
	v_rcp_f32_e32 v62, v53
	v_fma_f32 v53, |v59|, s25, 1.0
	v_rcp_f32_e32 v63, v53
	v_pk_mul_f32 v[64:65], v[58:59], v[58:59]
	v_pk_mul_f32 v[56:57], s[0:1], v[56:57] op_sel_hi:[0,1]
	v_mul_f32_e32 v53, 0xbf38aa3b, v64
	v_pk_fma_f32 v[66:67], v[62:63], s[22:23], v[90:91] op_sel_hi:[1,0,0]
	v_exp_f32_e32 v64, v53
	v_pk_fma_f32 v[66:67], v[62:63], v[66:67], s[24:25] op_sel_hi:[1,1,0]
	v_mul_f32_e32 v53, 0xbf38aa3b, v65
	v_pk_fma_f32 v[66:67], v[62:63], v[66:67], s[34:35] op_sel_hi:[1,1,0]
	v_exp_f32_e32 v65, v53
	v_pk_fma_f32 v[66:67], v[62:63], v[66:67], s[40:41] op_sel_hi:[1,1,0]
	v_pk_fma_f32 v[56:57], v[56:57], v[44:45], v[48:49]
	v_and_b32_e32 v61, 0x7fffffff, v59
	v_and_b32_e32 v60, 0x7fffffff, v58
	v_pk_mul_f32 v[62:63], v[62:63], v[66:67]
	v_fma_f32 v53, |v56|, s25, 1.0
	v_pk_mul_f32 v[60:61], v[60:61], v[62:63]
	v_rcp_f32_e32 v62, v53
	v_fma_f32 v53, |v57|, s25, 1.0
	v_max_f32_e32 v58, 0, v58
	v_max_f32_e32 v59, 0, v59
	v_rcp_f32_e32 v63, v53
	v_pk_fma_f32 v[58:59], v[64:65], v[60:61], v[58:59] neg_lo:[1,0,0] neg_hi:[1,0,0]
	v_pk_mul_f32 v[64:65], v[56:57], v[56:57]
	v_readlane_b32 s0, v52, 7
	v_mul_f32_e32 v53, 0xbf38aa3b, v64
	v_exp_f32_e32 v64, v53
	v_mul_f32_e32 v53, 0xbf38aa3b, v65
	v_pk_fma_f32 v[66:67], v[62:63], s[22:23], v[90:91] op_sel_hi:[1,0,0]
	v_exp_f32_e32 v65, v53
	v_pk_mul_f32 v[52:53], s[0:1], v[54:55] op_sel_hi:[0,1]
	v_pk_fma_f32 v[66:67], v[62:63], v[66:67], s[24:25] op_sel_hi:[1,1,0]
	v_pk_fma_f32 v[42:43], v[52:53], v[42:43], v[46:47]
	v_pk_fma_f32 v[66:67], v[62:63], v[66:67], s[34:35] op_sel_hi:[1,1,0]
	v_fma_f32 v52, |v42|, s25, 1.0
	v_fma_f32 v53, |v43|, s25, 1.0
	v_pk_fma_f32 v[66:67], v[62:63], v[66:67], s[40:41] op_sel_hi:[1,1,0]
	v_rcp_f32_e32 v52, v52
	v_rcp_f32_e32 v53, v53
	v_and_b32_e32 v61, 0x7fffffff, v57
	v_and_b32_e32 v60, 0x7fffffff, v56
	v_pk_mul_f32 v[62:63], v[62:63], v[66:67]
	v_max_f32_e32 v56, 0, v56
	v_max_f32_e32 v57, 0, v57
	v_pk_mul_f32 v[60:61], v[60:61], v[62:63]
	v_cvt_pk_f16_f32 v58, v58, v59
	v_pk_fma_f32 v[56:57], v[64:65], v[60:61], v[56:57] neg_lo:[1,0,0] neg_hi:[1,0,0]
	v_pk_mul_f32 v[54:55], v[42:43], v[42:43]
	v_cvt_pk_f16_f32 v59, v56, v57
	v_pk_fma_f32 v[56:57], v[52:53], s[22:23], v[90:91] op_sel_hi:[1,0,0]
	v_mul_f32_e32 v54, 0xbf38aa3b, v54
	v_pk_fma_f32 v[56:57], v[52:53], v[56:57], s[24:25] op_sel_hi:[1,1,0]
	v_mul_f32_e32 v55, 0xbf38aa3b, v55
	v_exp_f32_e32 v54, v54
	v_pk_fma_f32 v[56:57], v[52:53], v[56:57], s[34:35] op_sel_hi:[1,1,0]
	v_exp_f32_e32 v55, v55
	v_pk_fma_f32 v[56:57], v[52:53], v[56:57], s[40:41] op_sel_hi:[1,1,0]
	v_and_b32_e32 v47, 0x7fffffff, v43
	v_and_b32_e32 v46, 0x7fffffff, v42
	v_pk_mul_f32 v[52:53], v[52:53], v[56:57]
	v_max_f32_e32 v42, 0, v42
	v_max_f32_e32 v43, 0, v43
	v_pk_mul_f32 v[46:47], v[46:47], v[52:53]
	ds_write_b64 v119, v[58:59] offset:39936
	v_pk_fma_f32 v[42:43], v[54:55], v[46:47], v[42:43] neg_lo:[1,0,0] neg_hi:[1,0,0]
	v_pk_mul_f32 v[46:47], s[0:1], v[50:51] op_sel_hi:[0,1]
	v_pk_fma_f32 v[44:45], v[46:47], v[44:45], v[48:49]
	v_cvt_pk_f16_f32 v42, v42, v43
	v_fma_f32 v43, |v44|, s25, 1.0
	v_rcp_f32_e32 v48, v43
	v_fma_f32 v43, |v45|, s25, 1.0
	v_rcp_f32_e32 v49, v43
	v_pk_mul_f32 v[50:51], v[44:45], v[44:45]
	v_and_b32_e32 v47, 0x7fffffff, v45
	v_mul_f32_e32 v43, 0xbf38aa3b, v50
	v_pk_fma_f32 v[52:53], v[48:49], s[22:23], v[90:91] op_sel_hi:[1,0,0]
	v_exp_f32_e32 v50, v43
	v_pk_fma_f32 v[52:53], v[48:49], v[52:53], s[24:25] op_sel_hi:[1,1,0]
	v_mul_f32_e32 v43, 0xbf38aa3b, v51
	v_pk_fma_f32 v[52:53], v[48:49], v[52:53], s[34:35] op_sel_hi:[1,1,0]
	v_exp_f32_e32 v51, v43
	v_pk_fma_f32 v[52:53], v[48:49], v[52:53], s[40:41] op_sel_hi:[1,1,0]
	v_and_b32_e32 v46, 0x7fffffff, v44
	v_pk_mul_f32 v[48:49], v[48:49], v[52:53]
	v_max_f32_e32 v44, 0, v44
	v_max_f32_e32 v45, 0, v45
	v_pk_mul_f32 v[46:47], v[46:47], v[48:49]
	s_waitcnt lgkmcnt(14)
	v_dot2c_f32_f16_e32 v104, v10, v10
	v_pk_fma_f32 v[44:45], v[50:51], v[46:47], v[44:45] neg_lo:[1,0,0] neg_hi:[1,0,0]
	v_dot2c_f32_f16_e32 v104, v11, v11
	v_cvt_pk_f16_f32 v43, v44, v45
	ds_write_b64 v146, v[42:43] offset:40448
	ds_read_b128 v[70:73], v115 offset:32768
	ds_read_b128 v[66:69], v147 offset:32768
	ds_read_b128 v[62:65], v148 offset:32768
	ds_read_b128 v[58:61], v149 offset:32768
	ds_read_b128 v[54:57], v150 offset:33024
	ds_read_b128 v[50:53], v151 offset:33024
	ds_read_b128 v[46:49], v152 offset:33024
	ds_read_b128 v[42:45], v153 offset:33024
	ds_read_b128 v[74:77], v95
	ds_read_b128 v[78:81], v95 offset:64
	ds_read_b128 v[82:85], v95 offset:128
	ds_read_b128 v[86:89], v95 offset:192
	ds_read_b128 v[90:93], v95 offset:256
	ds_read_b128 v[96:99], v95 offset:320
	s_waitcnt lgkmcnt(5)
	v_dot2c_f32_f16_e32 v105, v38, v74
	v_dot2c_f32_f16_e32 v105, v39, v75
	ds_read_b128 v[100:103], v95 offset:384
	ds_read_b128 v[108:111], v95 offset:448
	v_mov_b32_e32 v95, 0
	v_dot2c_f32_f16_e32 v105, v40, v76
	v_dot2c_f32_f16_e32 v95, v70, v70
	v_dot2c_f32_f16_e32 v105, v41, v77
	v_mov_b32_e32 v115, 0
	v_dot2c_f32_f16_e32 v95, v71, v71
	s_waitcnt lgkmcnt(6)
	v_dot2c_f32_f16_e32 v105, v34, v78
	v_dot2c_f32_f16_e32 v115, v70, v74
	v_dot2c_f32_f16_e32 v95, v72, v72
	v_dot2c_f32_f16_e32 v105, v35, v79
	v_dot2c_f32_f16_e32 v115, v71, v75
	v_dot2c_f32_f16_e32 v95, v73, v73
	v_dot2c_f32_f16_e32 v105, v36, v80
	v_dot2c_f32_f16_e32 v115, v72, v76
	v_dot2c_f32_f16_e32 v95, v66, v66
	v_dot2c_f32_f16_e32 v105, v37, v81
	v_dot2c_f32_f16_e32 v115, v73, v77
	v_dot2c_f32_f16_e32 v95, v67, v67
	s_waitcnt lgkmcnt(5)
	v_dot2c_f32_f16_e32 v105, v30, v82
	v_dot2c_f32_f16_e32 v115, v66, v78
	v_dot2c_f32_f16_e32 v95, v68, v68
	v_dot2c_f32_f16_e32 v105, v31, v83
	v_dot2c_f32_f16_e32 v115, v67, v79
	v_dot2c_f32_f16_e32 v95, v69, v69
	v_dot2c_f32_f16_e32 v105, v32, v84
	v_dot2c_f32_f16_e32 v115, v68, v80
	v_dot2c_f32_f16_e32 v95, v62, v62
	v_dot2c_f32_f16_e32 v105, v33, v85
	v_dot2c_f32_f16_e32 v115, v69, v81
	v_dot2c_f32_f16_e32 v95, v63, v63
	s_waitcnt lgkmcnt(4)
	v_dot2c_f32_f16_e32 v105, v26, v86
	v_dot2c_f32_f16_e32 v115, v62, v82
	v_dot2c_f32_f16_e32 v95, v64, v64
	v_dot2c_f32_f16_e32 v105, v27, v87
	v_dot2c_f32_f16_e32 v115, v63, v83
	v_dot2c_f32_f16_e32 v95, v65, v65
	v_dot2c_f32_f16_e32 v105, v28, v88
	v_dot2c_f32_f16_e32 v115, v64, v84
	v_dot2c_f32_f16_e32 v95, v58, v58
	v_dot2c_f32_f16_e32 v105, v29, v89
	v_dot2c_f32_f16_e32 v115, v65, v85
	v_dot2c_f32_f16_e32 v95, v59, v59
	s_waitcnt lgkmcnt(3)
	v_dot2c_f32_f16_e32 v105, v22, v90
	v_dot2c_f32_f16_e32 v115, v58, v86
	v_dot2c_f32_f16_e32 v95, v60, v60
	v_dot2c_f32_f16_e32 v105, v23, v91
	v_dot2c_f32_f16_e32 v115, v59, v87
	v_dot2c_f32_f16_e32 v95, v61, v61
	v_dot2c_f32_f16_e32 v105, v24, v92
	v_dot2c_f32_f16_e32 v115, v60, v88
	v_dot2c_f32_f16_e32 v95, v54, v54
	v_dot2c_f32_f16_e32 v105, v25, v93
	v_dot2c_f32_f16_e32 v115, v61, v89
	v_dot2c_f32_f16_e32 v95, v55, v55
	s_waitcnt lgkmcnt(2)
	v_dot2c_f32_f16_e32 v105, v18, v96
	v_dot2c_f32_f16_e32 v115, v54, v90
	v_dot2c_f32_f16_e32 v95, v56, v56
	v_dot2c_f32_f16_e32 v105, v19, v97
	v_dot2c_f32_f16_e32 v115, v55, v91
	v_dot2c_f32_f16_e32 v95, v57, v57
	v_dot2c_f32_f16_e32 v105, v20, v98
	v_dot2c_f32_f16_e32 v115, v56, v92
	v_dot2c_f32_f16_e32 v95, v50, v50
	v_dot2c_f32_f16_e32 v105, v21, v99
	v_dot2c_f32_f16_e32 v115, v57, v93
	v_dot2c_f32_f16_e32 v95, v51, v51
	s_waitcnt lgkmcnt(1)
	v_dot2c_f32_f16_e32 v105, v14, v100
	v_dot2c_f32_f16_e32 v115, v50, v96
	v_dot2c_f32_f16_e32 v95, v52, v52
	v_dot2c_f32_f16_e32 v105, v15, v101
	v_dot2c_f32_f16_e32 v115, v51, v97
	v_dot2c_f32_f16_e32 v95, v53, v53
	v_dot2c_f32_f16_e32 v105, v16, v102
	v_dot2c_f32_f16_e32 v115, v52, v98
	v_dot2c_f32_f16_e32 v95, v46, v46
	v_dot2c_f32_f16_e32 v105, v17, v103
	v_dot2c_f32_f16_e32 v115, v53, v99
	v_dot2c_f32_f16_e32 v95, v47, v47
	s_waitcnt lgkmcnt(0)
	v_dot2c_f32_f16_e32 v105, v10, v108
	v_dot2c_f32_f16_e32 v104, v12, v12
	v_dot2c_f32_f16_e32 v115, v46, v100
	v_dot2c_f32_f16_e32 v95, v48, v48
	v_dot2c_f32_f16_e32 v105, v11, v109
	v_dot2c_f32_f16_e32 v104, v13, v13
	v_dot2c_f32_f16_e32 v115, v47, v101
	v_dot2c_f32_f16_e32 v95, v49, v49
	v_dot2c_f32_f16_e32 v105, v12, v110
	v_dot2c_f32_f16_e32 v115, v48, v102
	v_dot2c_f32_f16_e32 v95, v42, v42
	v_mov_b32_e32 v74, v104
	v_dot2c_f32_f16_e32 v105, v13, v111
	v_dot2c_f32_f16_e32 v115, v49, v103
	v_dot2c_f32_f16_e32 v95, v43, v43
	v_permlane16_swap_b32_e32 v104, v74
	v_dot2c_f32_f16_e32 v115, v42, v108
	v_dot2c_f32_f16_e32 v95, v44, v44
	v_add_f32_e32 v133, v104, v74
	v_mov_b32_e32 v74, v105
	v_dot2c_f32_f16_e32 v115, v43, v109
	v_dot2c_f32_f16_e32 v95, v45, v45
	v_permlane16_swap_b32_e32 v105, v74
	v_dot2c_f32_f16_e32 v115, v44, v110
	v_add_f32_e32 v137, v105, v74
	v_mov_b32_e32 v74, v95
	v_dot2c_f32_f16_e32 v115, v45, v111
	s_nop 0
	v_permlane16_swap_b32_e32 v95, v74
	v_add_f32_e32 v135, v95, v74
	v_mov_b32_e32 v74, v115
	s_nop 1
	v_permlane16_swap_b32_e32 v115, v74
	v_add_f32_e32 v139, v115, v74
	v_lshlrev_b32_e32 v74, 8, v107
	v_lshlrev_b32_e32 v75, 3, v114
	s_movk_i32 s0, 0x78
	v_and_or_b32 v76, v75, s0, v74
	v_lshlrev_b32_e32 v75, 3, v141
	v_and_or_b32 v77, v75, s0, v74
	v_lshlrev_b32_e32 v75, 3, v142
	v_and_or_b32 v78, v75, s0, v74
	v_lshlrev_b32_e32 v75, 3, v143
	v_and_or_b32 v79, v75, s0, v74
	s_add_u32 s0, s26, 0x8000
	v_or_b32_e32 v108, 0x8000, v112
	v_mov_b32_e32 v123, 0
	s_addc_u32 s1, s27, 0
	v_readfirstlane_b32 s4, v108
	s_waitcnt vmcnt(0)
	s_barrier
	v_lshl_add_u64 v[74:75], s[0:1], 0, v[122:123]
	s_mov_b32 m0, s4
	s_nop 0
	global_load_lds_dwordx4 v[74:75], off
	s_addk_i32 s4, 0x400
	v_mov_b32_e32 v107, v123
	v_lshl_add_u64 v[74:75], s[0:1], 0, v[106:107]
	s_add_u32 s0, s26, 0xc000
	s_mov_b32 m0, s4
	s_nop 0
	global_load_lds_dwordx4 v[74:75], off
	s_addc_u32 s1, s27, 0
	v_or_b32_e32 v109, 0xc000, v112
	v_lshl_add_u64 v[74:75], s[0:1], 0, v[122:123]
	v_readfirstlane_b32 s4, v109
	s_mov_b32 m0, s4
	s_nop 0
	global_load_lds_dwordx4 v[74:75], off
	s_addk_i32 s4, 0x400
	v_lshl_add_u64 v[74:75], s[0:1], 0, v[106:107]
	s_mov_b32 m0, s4
	s_nop 0
	global_load_lds_dwordx4 v[74:75], off
	v_mov_b32_e32 v134, v133
	v_mov_b32_e32 v138, v137
	v_mov_b32_e32 v136, v135
	v_mov_b32_e32 v140, v139
	v_lshlrev_b32_e32 v144, 1, v76
	v_lshlrev_b32_e32 v143, 1, v77
	v_lshlrev_b32_e32 v142, 1, v78
	v_lshlrev_b32_e32 v141, 1, v79
	s_add_u32 s0, s26, 0x14000
	v_mov_b32_e32 v74, 0x7f61b1e6
	v_permlane32_swap_b32_e32 v133, v134
	v_permlane32_swap_b32_e32 v137, v138
	v_permlane32_swap_b32_e32 v135, v136
	v_permlane32_swap_b32_e32 v139, v140
	v_or_b32_e32 v160, 0x10000, v144
	v_or_b32_e32 v158, 0x10000, v143
	v_or_b32_e32 v156, 0x10000, v142
	v_or_b32_e32 v154, 0x10000, v141
	v_or_b32_e32 v159, 0x12000, v144
	v_or_b32_e32 v157, 0x12000, v143
	v_or_b32_e32 v155, 0x12000, v142
	v_or_b32_e32 v153, 0x12000, v141
	v_or_b32_e32 v152, 0x14000, v144
	v_or_b32_e32 v150, 0x14000, v143
	v_or_b32_e32 v148, 0x14000, v142
	v_or_b32_e32 v146, 0x14000, v141
	v_or_b32_e32 v151, 0x16000, v144
	v_or_b32_e32 v149, 0x16000, v143
	v_or_b32_e32 v147, 0x16000, v142
	v_or_b32_e32 v145, 0x16000, v141
	s_addc_u32 s1, s27, 0
	v_mov_b32_e32 v98, 0x7f800000
	s_mov_b32 s22, 0
	v_mov_b32_e32 v100, 0x7f800000
	v_mov_b32_e32 v99, 0x7f800000
	v_mov_b32_e32 v111, 0x7f800000
	v_mov_b32_e32 v101, 0x7f800000
	v_mov_b32_e32 v110, 0x7f800000
	v_mov_b32_e32 v75, v74
	v_mov_b32_e32 v76, v74
	v_mov_b32_e32 v77, v74
	v_mov_b32_e32 v78, v74
	v_mov_b32_e32 v79, v74
	v_mov_b32_e32 v80, v74
	v_mov_b32_e32 v81, v74
	v_mov_b32_e32 v82, v74
	v_mov_b32_e32 v83, v74
	v_mov_b32_e32 v84, v74
	v_mov_b32_e32 v85, v74
	v_mov_b32_e32 v86, v74
	v_mov_b32_e32 v87, v74
	v_mov_b32_e32 v88, v74
	v_mov_b32_e32 v89, v74
	v_mov_b32_e32 v247, 0xfffffc00
.LBB1_7:
	s_add_u32 s4, s0, 0xffffc000
	v_readfirstlane_b32 s8, v112
	s_addc_u32 s5, s1, -1
	s_add_i32 s35, s8, 0x10000
	v_lshl_add_u64 v[96:97], s[4:5], 0, v[122:123]
	s_mov_b32 m0, s35
	s_nop 0
	global_load_lds_dwordx4 v[96:97], off
	s_add_i32 s34, s8, 0x10400
	v_lshl_add_u64 v[102:103], s[4:5], 0, v[106:107]
	s_mov_b32 m0, s34
	s_nop 0
	global_load_lds_dwordx4 v[102:103], off
	v_lshl_add_u64 v[90:91], s[0:1], 0, v[122:123]
	s_add_i32 s6, s8, 0x14000
	s_mov_b32 m0, s6
	s_nop 0
	global_load_lds_dwordx4 v[90:91], off
	v_lshl_add_u64 v[92:93], s[0:1], 0, v[106:107]
	s_add_i32 s7, s8, 0x14400
	s_mov_b32 m0, s7
	s_nop 0
	global_load_lds_dwordx4 v[92:93], off
	ds_read_b128 v[90:93], v144
	ds_read_b128 v[118:121], v144 offset:8192
	v_add_u32_e32 v95, s3, v94
	v_add_u32_e32 v96, 0x18060, v95
	v_add_u32_e32 v97, 0x180a0, v95
	ds_read_b128 v[102:105], v96
	ds_read_b128 v[162:165], v97
	s_lshl_b32 s24, s22, 5
	s_or_b32 s70, s24, 1
	s_or_b32 s71, s24, 2
	s_or_b32 s72, s24, 3
	s_or_b32 s73, s24, 17
	s_or_b32 s74, s24, 18
	s_or_b32 s75, s24, 19
	v_and_or_b32 v86, v86, v247, s24
	v_med3_f32 v111, v101, v111, v86
	v_med3_f32 v101, v110, v101, v86
	v_min_f32 v110, v110, v86
	s_waitcnt lgkmcnt(1)
	v_mfma_f32_16x16x32_f16 v[114:117], v[90:93], v[38:41], v[102:105]
	s_or_b32 s41, s24, 16
	ds_read_b128 v[166:169], v143 offset:8448
	ds_read_b128 v[170:173], v142 offset:8448
	v_mfma_f32_16x16x32_f16 v[90:93], v[90:93], v[70:73], v[102:105]
	v_and_or_b32 v96, v89, v247, s72
	ds_read_b128 v[102:105], v143
	v_and_or_b32 v97, v87, v247, s70
	v_and_or_b32 v161, v88, v247, s71
	s_waitcnt lgkmcnt(3)
	v_mfma_f32_16x16x32_f16 v[86:89], v[118:121], v[38:41], v[162:165]
	ds_read_b128 v[174:177], v141 offset:8448
	v_med3_f32 v111, v101, v111, v97
	v_med3_f32 v101, v110, v101, v97
	v_mfma_f32_16x16x32_f16 v[118:121], v[118:121], v[70:73], v[162:165]
	ds_read_b128 v[162:165], v143 offset:8192
	v_and_or_b32 v230, v82, v247, s24
	v_and_or_b32 v231, v83, v247, s70
	s_waitcnt lgkmcnt(2)
	v_mfma_f32_16x16x32_f16 v[114:117], v[102:105], v[34:37], v[114:117]
	v_min_f32 v97, v110, v97
	ds_read_b128 v[202:205], v144 offset:24576
	v_med3_f32 v110, v101, v111, v161
	v_mfma_f32_16x16x32_f16 v[90:93], v[102:105], v[66:69], v[90:93]
	v_and_or_b32 v232, v84, v247, s71
	v_and_or_b32 v233, v85, v247, s72
	s_waitcnt lgkmcnt(1)
	v_mfma_f32_16x16x32_f16 v[82:85], v[162:165], v[34:37], v[86:89]
	v_med3_f32 v101, v97, v101, v161
	v_min_f32 v97, v97, v161
	v_med3_f32 v98, v100, v98, v230
	v_mfma_f32_16x16x32_f16 v[102:105], v[162:165], v[66:69], v[118:121]
	v_and_or_b32 v234, v78, v247, s41
	s_nop 0
	ds_read_b128 v[86:89], v142
	ds_read_b128 v[118:121], v142 offset:8192
	v_and_or_b32 v235, v79, v247, s73
	v_and_or_b32 v236, v80, v247, s74
	s_waitcnt lgkmcnt(1)
	v_mfma_f32_16x16x32_f16 v[114:117], v[86:89], v[30:33], v[114:117]
	ds_read_b128 v[162:165], v144 offset:8448
	v_med3_f32 v100, v99, v100, v230
	ds_read_b128 v[178:181], v143 offset:16384
	v_mfma_f32_16x16x32_f16 v[86:89], v[86:89], v[62:65], v[90:93]
	v_and_or_b32 v237, v81, v247, s75
	v_and_or_b32 v238, v74, v247, s41
	s_waitcnt lgkmcnt(2)
	v_mfma_f32_16x16x32_f16 v[78:81], v[118:121], v[30:33], v[82:85]
	ds_read_b128 v[206:209], v143 offset:24576
	s_add_i32 s9, s23, 0xffffff70
	s_or_b32 s76, s9, 1
	s_or_b32 s77, s9, 2
	s_or_b32 s78, s9, 3
	s_or_b32 s79, s9, 17
	s_or_b32 s80, s9, 18
	s_or_b32 s81, s9, 19
	ds_read_b128 v[182:185], v142 offset:16384
	ds_read_b128 v[82:85], v141
	v_mfma_f32_16x16x32_f16 v[90:93], v[118:121], v[62:65], v[102:105]
	v_and_or_b32 v239, v75, v247, s73
	v_and_or_b32 v240, v76, v247, s74
	v_and_or_b32 v241, v77, v247, s75
	s_waitcnt lgkmcnt(0)
	v_mfma_f32_16x16x32_f16 v[74:77], v[82:85], v[26:29], v[114:117]
	ds_read_b128 v[102:105], v144 offset:256
	s_nop 1
	ds_read_b128 v[114:117], v143 offset:256
	ds_read_b128 v[118:121], v141 offset:256
	v_mfma_f32_16x16x32_f16 v[82:85], v[82:85], v[58:61], v[86:89]
	ds_read_b128 v[210:213], v142 offset:24576
	s_add_i32 s25, s23, 0xffffff80
	ds_read_b128 v[186:189], v141 offset:16384
	ds_read_b128 v[86:89], v141 offset:8192
	s_waitcnt lgkmcnt(0)
	v_mfma_f32_16x16x32_f16 v[78:81], v[86:89], v[26:29], v[78:81]
	ds_read_b128 v[214:217], v141 offset:24576
	ds_read_b128 v[190:193], v144 offset:16640
	s_add_u32 s4, s0, 0x4000
	v_mfma_f32_16x16x32_f16 v[86:89], v[86:89], v[58:61], v[90:93]
	s_addc_u32 s5, s1, 0
	s_add_i32 s40, s8, 0x400
	s_add_u32 s6, s0, 0x8000
	ds_read_b128 v[90:93], v142 offset:256
	v_mfma_f32_16x16x32_f16 v[74:77], v[102:105], v[22:25], v[74:77]
	s_addc_u32 s7, s1, 0
	ds_read_b128 v[194:197], v143 offset:16640
	ds_read_b128 v[218:221], v143 offset:24832
	v_mfma_f32_16x16x32_f16 v[82:85], v[102:105], v[54:57], v[82:85]
	ds_read_b128 v[102:105], v144 offset:16384
	ds_read_b128 v[222:225], v142 offset:24832
	ds_read_b128 v[198:201], v141 offset:16640
	v_mfma_f32_16x16x32_f16 v[78:81], v[162:165], v[22:25], v[78:81]
	ds_read_b128 v[226:229], v141 offset:24832
	s_add_i32 s35, s23, 0xffffff90
	s_or_b32 s82, s35, 1
	s_or_b32 s83, s35, 2
	s_or_b32 s84, s35, 3
	s_or_b32 s85, s35, 17
	s_or_b32 s86, s35, 18
	s_or_b32 s87, s35, 19
	s_add_i32 s41, s23, 0xffffffa0
	v_mfma_f32_16x16x32_f16 v[86:89], v[162:165], v[54:57], v[86:89]
	ds_read_b128 v[162:165], v142 offset:16640
	s_add_i32 s24, s23, 0xffffffb0
	s_or_b32 s70, s24, 1
	s_or_b32 s71, s24, 2
	s_or_b32 s72, s24, 3
	s_or_b32 s73, s24, 17
	s_or_b32 s74, s24, 18
	s_or_b32 s75, s24, 19
	s_sub_i32 s34, s23, 64
	v_mfma_f32_16x16x32_f16 v[74:77], v[114:117], v[18:21], v[74:77]
	s_mov_b32 s22, s33
	v_mfma_f32_16x16x32_f16 v[82:85], v[114:117], v[50:53], v[82:85]
	ds_read_b128 v[114:117], v144 offset:24832
	v_mfma_f32_16x16x32_f16 v[78:81], v[166:169], v[18:21], v[78:81]
	v_mfma_f32_16x16x32_f16 v[86:89], v[166:169], v[50:53], v[86:89]
	s_waitcnt lgkmcnt(8)
	v_mfma_f32_16x16x32_f16 v[74:77], v[90:93], v[14:17], v[74:77]
	v_mfma_f32_16x16x32_f16 v[82:85], v[90:93], v[46:49], v[82:85]
	v_min_f32 v90, v99, v230
	v_med3_f32 v91, v101, v110, v96
	v_med3_f32 v92, v97, v101, v96
	v_min_f32 v93, v97, v96
	v_med3_f32 v96, v100, v98, v231
	v_add_u32_e32 v99, 0x18120, v95
	v_med3_f32 v97, v90, v100, v231
	v_min_f32 v90, v90, v231
	v_med3_f32 v110, v92, v91, v234
	v_med3_f32 v111, v93, v92, v234
	s_nop 0
	v_med3_f32 v96, v97, v96, v232
	v_med3_f32 v97, v90, v97, v232
	v_min_f32 v98, v90, v232
	v_add_u32_e32 v90, 0x180e0, v95
	v_mfma_f32_16x16x32_f16 v[78:81], v[170:173], v[14:17], v[78:81]
	v_med3_f32 v167, v98, v97, v233
	v_min_f32 v168, v98, v233
	v_mfma_f32_16x16x32_f16 v[86:89], v[170:173], v[46:49], v[86:89]
	v_mfma_f32_16x16x32_f16 v[74:77], v[118:121], v[10:13], v[74:77]
	v_mfma_f32_16x16x32_f16 v[82:85], v[118:121], v[42:45], v[82:85]
	v_min_f32 v119, v93, v234
	ds_read_b128 v[90:93], v90
	v_med3_f32 v120, v97, v96, v233
	ds_read_b128 v[96:99], v99
	s_nop 4
	v_and_or_b32 v118, v74, v247, s9
	v_and_or_b32 v121, v75, v247, s76
	v_mfma_f32_16x16x32_f16 v[78:81], v[174:177], v[10:13], v[78:81]
	s_waitcnt vmcnt(4)
	s_waitcnt lgkmcnt(0)
	s_barrier
	v_mfma_f32_16x16x32_f16 v[86:89], v[174:177], v[42:45], v[86:89]
	v_and_or_b32 v161, v76, v247, s77
	v_and_or_b32 v166, v77, v247, s78
	s_waitcnt lgkmcnt(1)
	v_mfma_f32_16x16x32_f16 v[74:77], v[102:105], v[38:41], v[90:93]
	v_mfma_f32_16x16x32_f16 v[90:93], v[102:105], v[70:73], v[90:93]
	v_and_or_b32 v104, v82, v247, s9
	v_and_or_b32 v105, v83, v247, s76
	v_med3_f32 v82, v111, v110, v235
	v_med3_f32 v83, v119, v111, v235
	v_and_or_b32 v111, v84, v247, s77
	s_waitcnt lgkmcnt(0)
	v_mfma_f32_16x16x32_f16 v[100:103], v[202:205], v[38:41], v[96:99]
	v_min_f32 v110, v119, v235
	v_med3_f32 v170, v83, v82, v236
	v_mfma_f32_16x16x32_f16 v[96:99], v[202:205], v[70:73], v[96:99]
	v_and_or_b32 v169, v78, v247, s25
	v_and_or_b32 v119, v85, v247, s78
	v_mfma_f32_16x16x32_f16 v[74:77], v[178:181], v[34:37], v[74:77]
	v_med3_f32 v171, v110, v83, v236
	v_min_f32 v110, v110, v236
	v_mfma_f32_16x16x32_f16 v[82:85], v[178:181], v[66:69], v[90:93]
	v_and_b32_e32 v172, 0xfffffc00, v81
	v_and_or_b32 v173, v79, v247, s79
	v_and_or_b32 v174, v80, v247, s80
	v_mfma_f32_16x16x32_f16 v[90:93], v[206:209], v[66:69], v[96:99]
	v_min_f32 v99, v168, v238
	v_mfma_f32_16x16x32_f16 v[78:81], v[206:209], v[34:37], v[100:103]
	s_nop 0
	v_and_or_b32 v97, v86, v247, s25
	v_and_or_b32 v98, v87, v247, s79
	v_med3_f32 v86, v167, v120, v238
	v_med3_f32 v87, v168, v167, v238
	v_med3_f32 v100, v171, v170, v237
	v_med3_f32 v101, v110, v171, v237
	v_min_f32 v102, v110, v237
	v_or3_b32 v96, s9, v172, 19
	v_mfma_f32_16x16x32_f16 v[74:77], v[182:185], v[30:33], v[74:77]
	v_med3_f32 v120, v87, v86, v239
	v_med3_f32 v167, v99, v87, v239
	v_min_f32 v99, v99, v239
	v_mfma_f32_16x16x32_f16 v[82:85], v[182:185], v[62:65], v[82:85]
	v_and_or_b32 v103, v88, v247, s80
	v_and_or_b32 v110, v89, v247, s81
	v_mfma_f32_16x16x32_f16 v[86:89], v[210:213], v[62:65], v[90:93]
	v_med3_f32 v90, v167, v120, v240
	v_med3_f32 v91, v99, v167, v240
	v_min_f32 v92, v99, v240
	v_med3_f32 v93, v101, v100, v118
	v_med3_f32 v99, v102, v101, v118
	v_min_f32 v100, v102, v118
	v_mfma_f32_16x16x32_f16 v[78:81], v[210:213], v[30:33], v[78:81]
	v_med3_f32 v90, v91, v90, v241
	v_med3_f32 v91, v92, v91, v241
	v_min_f32 v92, v92, v241
	v_med3_f32 v93, v99, v93, v121
	v_med3_f32 v99, v100, v99, v121
	v_min_f32 v100, v100, v121
	v_mfma_f32_16x16x32_f16 v[74:77], v[186:189], v[26:29], v[74:77]
	v_med3_f32 v90, v91, v90, v104
	v_med3_f32 v91, v92, v91, v104
	v_min_f32 v92, v92, v104
	v_med3_f32 v93, v99, v93, v161
	v_med3_f32 v99, v100, v99, v161
	v_min_f32 v100, v100, v161
	v_mfma_f32_16x16x32_f16 v[82:85], v[186:189], v[58:61], v[82:85]
	v_med3_f32 v90, v91, v90, v105
	v_med3_f32 v91, v92, v91, v105
	v_min_f32 v92, v92, v105
	v_med3_f32 v93, v99, v93, v166
	v_med3_f32 v99, v100, v99, v166
	v_min_f32 v100, v100, v166
	s_nop 0
	v_med3_f32 v90, v91, v90, v111
	v_med3_f32 v91, v92, v91, v111
	v_min_f32 v92, v92, v111
	v_med3_f32 v93, v99, v93, v169
	v_med3_f32 v99, v100, v99, v169
	v_min_f32 v100, v100, v169
	s_nop 0
	v_med3_f32 v90, v91, v90, v119
	v_med3_f32 v91, v92, v91, v119
	v_min_f32 v92, v92, v119
	v_med3_f32 v93, v99, v93, v173
	v_med3_f32 v99, v100, v99, v173
	v_min_f32 v100, v100, v173
	s_nop 0
	v_med3_f32 v90, v91, v90, v97
	v_med3_f32 v91, v92, v91, v97
	v_min_f32 v92, v92, v97
	v_med3_f32 v93, v99, v93, v174
	v_med3_f32 v99, v100, v99, v174
	v_min_f32 v100, v100, v174
	s_nop 0
	v_med3_f32 v90, v91, v90, v98
	v_med3_f32 v91, v92, v91, v98
	v_min_f32 v92, v92, v98
	v_med3_f32 v104, v99, v93, v96
	v_med3_f32 v105, v100, v99, v96
	v_min_f32 v111, v100, v96
	v_lshl_add_u64 v[96:97], s[6:7], 0, v[122:123]
	v_med3_f32 v100, v91, v90, v103
	v_med3_f32 v101, v92, v91, v103
	v_min_f32 v102, v92, v103
	v_lshl_add_u64 v[90:91], s[4:5], 0, v[122:123]
	v_lshl_add_u64 v[92:93], s[4:5], 0, v[106:107]
	v_readfirstlane_b32 s5, v113
	v_lshl_add_u64 v[98:99], s[6:7], 0, v[106:107]
	v_mfma_f32_16x16x32_f16 v[78:81], v[214:217], v[26:29], v[78:81]
	s_mov_b32 m0, s8
	s_nop 0
	global_load_lds_dwordx4 v[90:91], off
	s_add_i32 s6, s5, 0x400
	s_mov_b32 m0, s40
	s_nop 0
	global_load_lds_dwordx4 v[92:93], off
	v_mfma_f32_16x16x32_f16 v[86:89], v[214:217], v[58:61], v[86:89]
	s_mov_b32 m0, s5
	s_nop 0
	global_load_lds_dwordx4 v[96:97], off
	v_med3_f32 v161, v101, v100, v110
	v_med3_f32 v230, v102, v101, v110
	v_mfma_f32_16x16x32_f16 v[74:77], v[190:193], v[22:25], v[74:77]
	s_mov_b32 m0, s6
	s_nop 0
	global_load_lds_dwordx4 v[98:99], off
	ds_read_b128 v[90:93], v144 offset:32768
	v_min_f32 v110, v102, v110
	v_mfma_f32_16x16x32_f16 v[82:85], v[190:193], v[54:57], v[82:85]
	ds_read_b128 v[166:169], v143 offset:41216
	ds_read_b128 v[170:173], v142 offset:41216
	ds_read_b128 v[174:177], v141 offset:41216
	v_mfma_f32_16x16x32_f16 v[78:81], v[114:117], v[22:25], v[78:81]
	ds_read_b128 v[202:205], v144 offset:57344
	ds_read_b128 v[178:181], v143 offset:49152
	ds_read_b128 v[182:185], v142 offset:49152
	v_mfma_f32_16x16x32_f16 v[86:89], v[114:117], v[54:57], v[86:89]
	ds_read_b128 v[114:117], v144 offset:40960
	ds_read_b128 v[206:209], v143 offset:57344
	ds_read_b128 v[186:189], v141 offset:49152
	v_mfma_f32_16x16x32_f16 v[74:77], v[194:197], v[18:21], v[74:77]
	ds_read_b128 v[210:213], v142 offset:57344
	ds_read_b128 v[190:193], v144 offset:49408
	ds_read_b128 v[214:217], v141 offset:57344
	v_mfma_f32_16x16x32_f16 v[82:85], v[194:197], v[50:53], v[82:85]
	ds_read_b128 v[194:197], v143 offset:49408
	s_add_u32 s4, s0, 0xc000
	s_addc_u32 s5, s1, 0
	v_mfma_f32_16x16x32_f16 v[78:81], v[218:221], v[18:21], v[78:81]
	v_mfma_f32_16x16x32_f16 v[86:89], v[218:221], v[50:53], v[86:89]
	ds_read_b128 v[218:221], v143 offset:57600
	v_mfma_f32_16x16x32_f16 v[74:77], v[162:165], v[14:17], v[74:77]
	v_mfma_f32_16x16x32_f16 v[82:85], v[162:165], v[46:49], v[82:85]
	ds_read_b128 v[162:165], v144 offset:41216
	v_mfma_f32_16x16x32_f16 v[78:81], v[222:225], v[14:17], v[78:81]
	v_mfma_f32_16x16x32_f16 v[86:89], v[222:225], v[46:49], v[86:89]
	ds_read_b128 v[222:225], v142 offset:57600
	v_mfma_f32_16x16x32_f16 v[74:77], v[198:201], v[10:13], v[74:77]
	v_mfma_f32_16x16x32_f16 v[82:85], v[198:201], v[42:45], v[82:85]
	ds_read_b128 v[198:201], v141 offset:49408
	v_mfma_f32_16x16x32_f16 v[78:81], v[226:229], v[10:13], v[78:81]
	v_mfma_f32_16x16x32_f16 v[86:89], v[226:229], v[42:45], v[86:89]
	v_add_u32_e32 v100, 0x18160, v95
	ds_read_b128 v[96:99], v100
	s_nop 1
	v_add_u32_e32 v118, 0x181a0, v95
	v_and_or_b32 v231, v74, v247, s35
	s_waitcnt lgkmcnt(0)
	v_mfma_f32_16x16x32_f16 v[100:103], v[90:93], v[38:41], v[96:99]
	ds_read_b128 v[118:121], v118
	v_med3_f32 v104, v105, v104, v231
	v_med3_f32 v105, v111, v105, v231
	v_mfma_f32_16x16x32_f16 v[90:93], v[90:93], v[70:73], v[96:99]
	v_and_or_b32 v232, v75, v247, s82
	ds_read_b128 v[96:99], v143 offset:32768
	v_and_or_b32 v233, v76, v247, s83
	v_and_or_b32 v234, v77, v247, s84
	s_waitcnt lgkmcnt(1)
	v_mfma_f32_16x16x32_f16 v[74:77], v[114:117], v[38:41], v[118:121]
	v_min_f32 v111, v111, v231
	v_med3_f32 v104, v105, v104, v232
	ds_read_b128 v[226:229], v141 offset:57600
	v_mfma_f32_16x16x32_f16 v[114:117], v[114:117], v[70:73], v[118:121]
	v_and_or_b32 v235, v82, v247, s35
	v_and_or_b32 v236, v83, v247, s82
	s_waitcnt lgkmcnt(1)
	v_mfma_f32_16x16x32_f16 v[100:103], v[96:99], v[34:37], v[100:103]
	ds_read_b128 v[118:121], v143 offset:40960
	v_med3_f32 v105, v111, v105, v232
	v_min_f32 v111, v111, v232
	v_mfma_f32_16x16x32_f16 v[90:93], v[96:99], v[66:69], v[90:93]
	v_and_or_b32 v237, v84, v247, s83
	v_and_or_b32 v238, v85, v247, s84
	ds_read_b128 v[82:85], v142 offset:32768
	v_and_or_b32 v239, v78, v247, s41
	s_waitcnt lgkmcnt(1)
	v_mfma_f32_16x16x32_f16 v[74:77], v[118:121], v[34:37], v[74:77]
	v_med3_f32 v104, v105, v104, v233
	v_med3_f32 v105, v111, v105, v233
	v_min_f32 v111, v111, v233
	v_mfma_f32_16x16x32_f16 v[96:99], v[118:121], v[66:69], v[114:117]
	v_and_or_b32 v240, v79, v247, s85
	v_and_or_b32 v242, v81, v247, s87
	v_and_or_b32 v241, v80, v247, s86
	s_waitcnt lgkmcnt(0)
	v_mfma_f32_16x16x32_f16 v[78:81], v[82:85], v[30:33], v[100:103]
	ds_read_b128 v[118:121], v141 offset:33024
	v_med3_f32 v104, v105, v104, v234
	v_med3_f32 v105, v111, v105, v234
	v_mfma_f32_16x16x32_f16 v[82:85], v[82:85], v[62:65], v[90:93]
	ds_read_b128 v[100:103], v142 offset:40960
	ds_read_b128 v[90:93], v141 offset:32768
	v_and_or_b32 v243, v86, v247, s41
	v_and_or_b32 v244, v87, v247, s85
	s_waitcnt lgkmcnt(1)
	v_mfma_f32_16x16x32_f16 v[74:77], v[100:103], v[30:33], v[74:77]
	ds_read_b128 v[114:117], v143 offset:33024
	v_min_f32 v111, v111, v234
	v_mfma_f32_16x16x32_f16 v[96:99], v[100:103], v[62:65], v[96:99]
	v_and_or_b32 v245, v88, v247, s86
	v_and_or_b32 v246, v89, v247, s87
	ds_read_b128 v[86:89], v141 offset:40960
	ds_read_b128 v[100:103], v144 offset:33024
	s_waitcnt lgkmcnt(3)
	v_mfma_f32_16x16x32_f16 v[78:81], v[90:93], v[26:29], v[78:81]
	v_mfma_f32_16x16x32_f16 v[82:85], v[90:93], v[58:61], v[82:85]
	ds_read_b128 v[90:93], v142 offset:33024
	s_waitcnt lgkmcnt(2)
	v_mfma_f32_16x16x32_f16 v[74:77], v[86:89], v[26:29], v[74:77]
	v_mfma_f32_16x16x32_f16 v[86:89], v[86:89], v[58:61], v[96:99]
	s_waitcnt lgkmcnt(1)
	v_mfma_f32_16x16x32_f16 v[78:81], v[100:103], v[22:25], v[78:81]
	s_nop 0
	ds_read_b128 v[96:99], v144 offset:49152
	v_mfma_f32_16x16x32_f16 v[82:85], v[100:103], v[54:57], v[82:85]
	ds_read_b128 v[100:103], v142 offset:49408
	v_mfma_f32_16x16x32_f16 v[74:77], v[162:165], v[22:25], v[74:77]
	v_mfma_f32_16x16x32_f16 v[86:89], v[162:165], v[54:57], v[86:89]
	ds_read_b128 v[162:165], v144 offset:57600
	v_mfma_f32_16x16x32_f16 v[78:81], v[114:117], v[18:21], v[78:81]
	v_mfma_f32_16x16x32_f16 v[82:85], v[114:117], v[50:53], v[82:85]
	v_med3_f32 v114, v230, v161, v235
	v_med3_f32 v115, v110, v230, v235
	v_mfma_f32_16x16x32_f16 v[74:77], v[166:169], v[18:21], v[74:77]
	v_mfma_f32_16x16x32_f16 v[86:89], v[166:169], v[50:53], v[86:89]
	s_waitcnt lgkmcnt(3)
	v_mfma_f32_16x16x32_f16 v[78:81], v[90:93], v[14:17], v[78:81]
	v_mfma_f32_16x16x32_f16 v[82:85], v[90:93], v[46:49], v[82:85]
	v_min_f32 v90, v110, v235
	v_med3_f32 v91, v115, v114, v236
	s_nop 0
	v_med3_f32 v92, v90, v115, v236
	v_min_f32 v90, v90, v236
	s_nop 0
	v_med3_f32 v91, v92, v91, v237
	v_med3_f32 v92, v90, v92, v237
	v_min_f32 v90, v90, v237
	s_nop 0
	v_med3_f32 v110, v92, v91, v238
	v_med3_f32 v161, v90, v92, v238
	v_min_f32 v166, v90, v238
	v_med3_f32 v90, v105, v104, v239
	v_med3_f32 v104, v111, v105, v239
	v_add_u32_e32 v91, 0x181e0, v95
	v_add_u32_e32 v105, 0x18220, v95
	v_mfma_f32_16x16x32_f16 v[74:77], v[170:173], v[14:17], v[74:77]
	ds_read_b128 v[114:117], v105
	v_min_f32 v111, v111, v239
	v_mfma_f32_16x16x32_f16 v[86:89], v[170:173], v[46:49], v[86:89]
	v_mfma_f32_16x16x32_f16 v[78:81], v[118:121], v[10:13], v[78:81]
	v_mfma_f32_16x16x32_f16 v[82:85], v[118:121], v[42:45], v[82:85]
	v_med3_f32 v119, v104, v90, v240
	ds_read_b128 v[90:93], v91
	s_nop 5
	v_and_or_b32 v118, v78, v247, s24
	v_and_or_b32 v120, v79, v247, s70
	v_mfma_f32_16x16x32_f16 v[74:77], v[174:177], v[10:13], v[74:77]
	v_med3_f32 v104, v111, v104, v240
	v_min_f32 v111, v111, v240
	s_waitcnt vmcnt(4)
	v_mfma_f32_16x16x32_f16 v[86:89], v[174:177], v[42:45], v[86:89]
	v_and_or_b32 v121, v80, v247, s71
	v_and_or_b32 v167, v81, v247, s72
	s_waitcnt lgkmcnt(0)
	v_mfma_f32_16x16x32_f16 v[78:81], v[96:99], v[38:41], v[90:93]
	s_waitcnt lgkmcnt(0)
	s_barrier
	v_mfma_f32_16x16x32_f16 v[90:93], v[96:99], v[70:73], v[90:93]
	v_and_or_b32 v105, v82, v247, s24
	v_and_or_b32 v168, v83, v247, s70
	v_med3_f32 v82, v104, v119, v241
	v_med3_f32 v83, v111, v104, v241
	v_min_f32 v104, v111, v241
	v_and_or_b32 v111, v84, v247, s71
	v_mfma_f32_16x16x32_f16 v[96:99], v[202:205], v[38:41], v[114:117]
	v_med3_f32 v170, v83, v82, v242
	v_med3_f32 v171, v104, v83, v242
	v_min_f32 v104, v104, v242
	v_mfma_f32_16x16x32_f16 v[114:117], v[202:205], v[70:73], v[114:117]
	v_and_or_b32 v119, v85, v247, s72
	v_and_or_b32 v169, v74, v247, s34
	v_mfma_f32_16x16x32_f16 v[78:81], v[178:181], v[34:37], v[78:81]
	v_mfma_f32_16x16x32_f16 v[82:85], v[178:181], v[66:69], v[90:93]
	v_and_b32_e32 v172, 0xfffffc00, v77
	v_and_or_b32 v173, v75, v247, s73
	v_and_or_b32 v174, v76, v247, s74
	v_mfma_f32_16x16x32_f16 v[74:77], v[206:209], v[34:37], v[96:99]
	v_med3_f32 v96, v161, v110, v243
	v_med3_f32 v97, v166, v161, v243
	v_min_f32 v98, v166, v243
	v_mfma_f32_16x16x32_f16 v[90:93], v[206:209], v[66:69], v[114:117]
	v_and_or_b32 v110, v86, v247, s34
	s_nop 0
	v_or3_b32 v99, s24, v172, 19
	v_and_or_b32 v114, v87, v247, s73
	v_mfma_f32_16x16x32_f16 v[78:81], v[182:185], v[30:33], v[78:81]
	v_med3_f32 v86, v97, v96, v244
	v_med3_f32 v87, v98, v97, v244
	v_min_f32 v96, v98, v244
	v_mfma_f32_16x16x32_f16 v[82:85], v[182:185], v[62:65], v[82:85]
	v_and_or_b32 v97, v88, v247, s74
	v_and_or_b32 v98, v89, v247, s75
	v_med3_f32 v115, v87, v86, v245
	v_mfma_f32_16x16x32_f16 v[74:77], v[210:213], v[30:33], v[74:77]
	v_med3_f32 v116, v96, v87, v245
	v_min_f32 v96, v96, v245
	v_mfma_f32_16x16x32_f16 v[86:89], v[210:213], v[62:65], v[90:93]
	v_med3_f32 v90, v116, v115, v246
	v_med3_f32 v91, v96, v116, v246
	v_min_f32 v92, v96, v246
	v_mfma_f32_16x16x32_f16 v[78:81], v[186:189], v[26:29], v[78:81]
	v_med3_f32 v93, v171, v170, v118
	v_med3_f32 v90, v91, v90, v105
	v_med3_f32 v91, v92, v91, v105
	v_mfma_f32_16x16x32_f16 v[82:85], v[186:189], v[58:61], v[82:85]
	v_min_f32 v92, v92, v105
	v_med3_f32 v96, v104, v171, v118
	v_med3_f32 v90, v91, v90, v168
	v_mfma_f32_16x16x32_f16 v[74:77], v[214:217], v[26:29], v[74:77]
	v_med3_f32 v93, v96, v93, v120
	v_med3_f32 v91, v92, v91, v168
	v_min_f32 v92, v92, v168
	v_mfma_f32_16x16x32_f16 v[86:89], v[214:217], v[58:61], v[86:89]
	v_min_f32 v104, v104, v118
	v_med3_f32 v90, v91, v90, v111
	v_med3_f32 v91, v92, v91, v111
	v_mfma_f32_16x16x32_f16 v[78:81], v[190:193], v[22:25], v[78:81]
	v_med3_f32 v96, v104, v96, v120
	v_min_f32 v92, v92, v111
	v_min_f32 v104, v104, v120
	v_mfma_f32_16x16x32_f16 v[82:85], v[190:193], v[54:57], v[82:85]
	v_med3_f32 v93, v96, v93, v121
	v_med3_f32 v96, v104, v96, v121
	v_med3_f32 v90, v91, v90, v119
	v_mfma_f32_16x16x32_f16 v[74:77], v[162:165], v[22:25], v[74:77]
	v_med3_f32 v93, v96, v93, v167
	v_med3_f32 v91, v92, v91, v119
	v_min_f32 v92, v92, v119
	v_mfma_f32_16x16x32_f16 v[86:89], v[162:165], v[54:57], v[86:89]
	v_min_f32 v104, v104, v121
	v_med3_f32 v90, v91, v90, v110
	v_med3_f32 v91, v92, v91, v110
	v_mfma_f32_16x16x32_f16 v[78:81], v[194:197], v[18:21], v[78:81]
	v_med3_f32 v96, v104, v96, v167
	v_min_f32 v92, v92, v110
	v_min_f32 v104, v104, v167
	v_mfma_f32_16x16x32_f16 v[82:85], v[194:197], v[50:53], v[82:85]
	v_med3_f32 v93, v96, v93, v169
	v_med3_f32 v96, v104, v96, v169
	v_med3_f32 v90, v91, v90, v114
	v_mfma_f32_16x16x32_f16 v[74:77], v[218:221], v[18:21], v[74:77]
	v_med3_f32 v93, v96, v93, v173
	v_med3_f32 v91, v92, v91, v114
	v_min_f32 v92, v92, v114
	v_mfma_f32_16x16x32_f16 v[86:89], v[218:221], v[50:53], v[86:89]
	v_min_f32 v104, v104, v169
	v_med3_f32 v90, v91, v90, v97
	v_med3_f32 v91, v92, v91, v97
	v_mfma_f32_16x16x32_f16 v[78:81], v[100:103], v[14:17], v[78:81]
	v_med3_f32 v96, v104, v96, v173
	v_min_f32 v92, v92, v97
	v_min_f32 v104, v104, v173
	v_mfma_f32_16x16x32_f16 v[82:85], v[100:103], v[46:49], v[82:85]
	v_med3_f32 v93, v96, v93, v174
	v_med3_f32 v96, v104, v96, v174
	v_med3_f32 v111, v91, v90, v98
	v_mfma_f32_16x16x32_f16 v[74:77], v[222:225], v[14:17], v[74:77]
	v_med3_f32 v105, v96, v93, v99
	v_med3_f32 v161, v92, v91, v98
	v_min_f32 v230, v92, v98
	v_mfma_f32_16x16x32_f16 v[86:89], v[222:225], v[46:49], v[86:89]
	v_min_f32 v104, v104, v174
	v_mfma_f32_16x16x32_f16 v[78:81], v[198:201], v[10:13], v[78:81]
	v_med3_f32 v110, v104, v96, v99
	v_min_f32 v104, v104, v99
	v_mfma_f32_16x16x32_f16 v[82:85], v[198:201], v[42:45], v[82:85]
	v_readfirstlane_b32 s6, v108
	v_lshl_add_u64 v[90:91], s[4:5], 0, v[122:123]
	v_lshl_add_u64 v[92:93], s[4:5], 0, v[106:107]
	s_add_i32 s4, s6, 0x400
	s_mov_b32 m0, s6
	s_nop 0
	global_load_lds_dwordx4 v[90:91], off
	s_add_u32 s6, s0, 0x10000
	s_mov_b32 m0, s4
	s_nop 0
	global_load_lds_dwordx4 v[92:93], off
	s_addc_u32 s7, s1, 0
	v_readfirstlane_b32 s5, v109
	v_lshl_add_u64 v[90:91], s[6:7], 0, v[122:123]
	s_mov_b32 m0, s5
	s_nop 0
	global_load_lds_dwordx4 v[90:91], off
	s_add_i32 s8, s5, 0x400
	v_mfma_f32_16x16x32_f16 v[74:77], v[226:229], v[10:13], v[74:77]
	s_sub_i32 s9, s23, 48
	s_or_b32 s76, s9, 1
	s_or_b32 s77, s9, 2
	s_or_b32 s78, s9, 3
	s_or_b32 s79, s9, 17
	s_or_b32 s80, s9, 18
	s_or_b32 s81, s9, 19
	s_sub_i32 s24, s23, 32
	s_or_b32 s70, s24, 1
	s_or_b32 s71, s24, 2
	s_or_b32 s72, s24, 3
	s_or_b32 s73, s24, 17
	s_or_b32 s74, s24, 18
	s_or_b32 s75, s24, 19
	s_add_i32 s4, s23, -16
	s_or_b32 s88, s4, 1
	s_or_b32 s89, s4, 2
	s_or_b32 s90, s4, 3
	s_or_b32 s91, s4, 17
	s_or_b32 s92, s4, 18
	s_or_b32 s93, s4, 19
	v_mfma_f32_16x16x32_f16 v[86:89], v[226:229], v[42:45], v[86:89]
	v_lshl_add_u64 v[92:93], s[6:7], 0, v[106:107]
	s_mov_b32 m0, s8
	s_nop 0
	global_load_lds_dwordx4 v[92:93], off
	ds_read_b128 v[90:93], v160
	ds_read_b128 v[114:117], v159
	v_add_u32_e32 v96, 0x18260, v95
	ds_read_b128 v[96:99], v96
	v_add_u32_e32 v118, 0x182a0, v95
	ds_read_b128 v[118:121], v118
	v_and_or_b32 v162, v78, v247, s9
	s_waitcnt lgkmcnt(1)
	v_mfma_f32_16x16x32_f16 v[100:103], v[90:93], v[38:41], v[96:99]
	v_med3_f32 v105, v110, v105, v162
	v_med3_f32 v110, v104, v110, v162
	v_min_f32 v104, v104, v162
	v_mfma_f32_16x16x32_f16 v[90:93], v[90:93], v[70:73], v[96:99]
	v_and_or_b32 v228, v81, v247, s78
	ds_read_b128 v[96:99], v158
	v_and_or_b32 v226, v79, v247, s76
	v_and_or_b32 v227, v80, v247, s77
	s_waitcnt lgkmcnt(1)
	v_mfma_f32_16x16x32_f16 v[78:81], v[114:117], v[38:41], v[118:121]
	ds_read_b128 v[166:169], v155 offset:256
	v_med3_f32 v105, v110, v105, v226
	v_med3_f32 v110, v104, v110, v226
	v_mfma_f32_16x16x32_f16 v[114:117], v[114:117], v[70:73], v[118:121]
	ds_read_b128 v[118:121], v157
	v_and_or_b32 v229, v82, v247, s9
	v_and_or_b32 v231, v83, v247, s76
	s_waitcnt lgkmcnt(2)
	v_mfma_f32_16x16x32_f16 v[100:103], v[96:99], v[34:37], v[100:103]
	ds_read_b128 v[162:165], v157 offset:256
	v_med3_f32 v105, v110, v105, v227
	v_min_f32 v104, v104, v226
	v_mfma_f32_16x16x32_f16 v[90:93], v[96:99], v[66:69], v[90:93]
	v_and_or_b32 v232, v84, v247, s77
	v_and_or_b32 v233, v85, v247, s78
	ds_read_b128 v[82:85], v156
	s_waitcnt lgkmcnt(2)
	v_mfma_f32_16x16x32_f16 v[96:99], v[118:121], v[66:69], v[114:117]
	v_med3_f32 v110, v104, v110, v227
	v_med3_f32 v111, v161, v111, v229
	ds_read_b128 v[170:173], v152
	v_mfma_f32_16x16x32_f16 v[78:81], v[118:121], v[34:37], v[78:81]
	v_and_or_b32 v234, v74, v247, s24
	ds_read_b128 v[114:117], v155
	v_and_or_b32 v235, v75, v247, s79
	v_and_or_b32 v236, v76, v247, s80
	s_waitcnt lgkmcnt(2)
	v_mfma_f32_16x16x32_f16 v[100:103], v[82:85], v[30:33], v[100:103]
	ds_read_b128 v[118:121], v154 offset:256
	v_min_f32 v104, v104, v227
	ds_read_b128 v[198:201], v151
	v_mfma_f32_16x16x32_f16 v[82:85], v[82:85], v[62:65], v[90:93]
	v_and_or_b32 v237, v77, v247, s81
	v_and_or_b32 v238, v86, v247, s24
	s_waitcnt lgkmcnt(2)
	v_mfma_f32_16x16x32_f16 v[74:77], v[114:117], v[30:33], v[78:81]
	ds_read_b128 v[174:177], v150
	ds_read_b128 v[202:205], v149
	ds_read_b128 v[178:181], v148
	ds_read_b128 v[78:81], v154
	v_mfma_f32_16x16x32_f16 v[90:93], v[114:117], v[62:65], v[96:99]
	v_and_or_b32 v239, v87, v247, s79
	v_and_or_b32 v240, v88, v247, s80
	v_and_or_b32 v241, v89, v247, s81
	s_waitcnt lgkmcnt(0)
	v_mfma_f32_16x16x32_f16 v[86:89], v[78:81], v[26:29], v[100:103]
	ds_read_b128 v[96:99], v160 offset:256
	ds_read_b128 v[114:117], v159 offset:256
	s_nop 0
	ds_read_b128 v[100:103], v156 offset:256
	v_mfma_f32_16x16x32_f16 v[78:81], v[78:81], v[58:61], v[82:85]
	ds_read_b128 v[206:209], v147
	ds_read_b128 v[182:185], v146
	ds_read_b128 v[186:189], v152 offset:256
	ds_read_b128 v[82:85], v153
	s_waitcnt lgkmcnt(0)
	v_mfma_f32_16x16x32_f16 v[74:77], v[82:85], v[26:29], v[74:77]
	ds_read_b128 v[210:213], v151 offset:256
	ds_read_b128 v[214:217], v149 offset:256
	ds_read_b128 v[190:193], v148 offset:256
	v_mfma_f32_16x16x32_f16 v[82:85], v[82:85], v[58:61], v[90:93]
	ds_read_b128 v[218:221], v147 offset:256
	ds_read_b128 v[194:197], v146 offset:256
	ds_read_b128 v[222:225], v145 offset:256
	ds_read_b128 v[90:93], v158 offset:256
	v_mfma_f32_16x16x32_f16 v[86:89], v[96:99], v[22:25], v[86:89]
	s_addk_i32 s3, 0x300
	v_mfma_f32_16x16x32_f16 v[78:81], v[96:99], v[54:57], v[78:81]
	ds_read_b128 v[96:99], v153 offset:256
	v_mfma_f32_16x16x32_f16 v[74:77], v[114:117], v[22:25], v[74:77]
	v_mfma_f32_16x16x32_f16 v[82:85], v[114:117], v[54:57], v[82:85]
	ds_read_b128 v[114:117], v150 offset:256
	s_waitcnt lgkmcnt(2)
	v_mfma_f32_16x16x32_f16 v[86:89], v[90:93], v[18:21], v[86:89]
	v_mfma_f32_16x16x32_f16 v[78:81], v[90:93], v[50:53], v[78:81]
	ds_read_b128 v[90:93], v145
	v_mfma_f32_16x16x32_f16 v[74:77], v[162:165], v[18:21], v[74:77]
	v_mfma_f32_16x16x32_f16 v[82:85], v[162:165], v[50:53], v[82:85]
	v_mfma_f32_16x16x32_f16 v[86:89], v[100:103], v[14:17], v[86:89]
	v_mfma_f32_16x16x32_f16 v[78:81], v[100:103], v[46:49], v[78:81]
	v_med3_f32 v100, v230, v161, v229
	v_min_f32 v101, v230, v229
	v_med3_f32 v102, v110, v105, v228
	v_med3_f32 v103, v104, v110, v228
	v_min_f32 v104, v104, v228
	s_nop 0
	v_med3_f32 v105, v100, v111, v231
	v_med3_f32 v100, v101, v100, v231
	v_min_f32 v101, v101, v231
	v_med3_f32 v161, v103, v102, v234
	v_med3_f32 v163, v104, v103, v234
	v_min_f32 v104, v104, v234
	s_nop 0
	v_med3_f32 v105, v100, v105, v232
	v_med3_f32 v110, v101, v100, v232
	v_add_u32_e32 v100, 0x182e0, v95
	v_add_u32_e32 v95, 0x18320, v95
	v_mfma_f32_16x16x32_f16 v[74:77], v[166:169], v[14:17], v[74:77]
	v_min_f32 v111, v101, v232
	ds_read_b128 v[100:103], v100
	v_med3_f32 v161, v163, v161, v235
	v_mfma_f32_16x16x32_f16 v[82:85], v[166:169], v[46:49], v[82:85]
	v_med3_f32 v105, v110, v105, v233
	v_med3_f32 v110, v111, v110, v233
	v_min_f32 v111, v111, v233
	v_mfma_f32_16x16x32_f16 v[86:89], v[118:121], v[10:13], v[86:89]
	v_med3_f32 v163, v104, v163, v235
	v_min_f32 v104, v104, v235
	v_mfma_f32_16x16x32_f16 v[78:81], v[118:121], v[42:45], v[78:81]
	v_med3_f32 v161, v163, v161, v236
	v_med3_f32 v163, v104, v163, v236
	s_nop 6
	v_and_or_b32 v162, v86, v247, s4
	v_and_or_b32 v164, v87, v247, s88
	s_waitcnt lgkmcnt(3)
	v_mfma_f32_16x16x32_f16 v[74:77], v[96:99], v[10:13], v[74:77]
	v_mfma_f32_16x16x32_f16 v[82:85], v[96:99], v[42:45], v[82:85]
	ds_read_b128 v[96:99], v95
	v_and_or_b32 v165, v88, v247, s89
	v_and_or_b32 v166, v89, v247, s90
	s_waitcnt lgkmcnt(1)
	v_mfma_f32_16x16x32_f16 v[86:89], v[170:173], v[38:41], v[100:103]
	s_waitcnt vmcnt(4)
	s_waitcnt lgkmcnt(0)
	s_barrier
	v_mfma_f32_16x16x32_f16 v[100:103], v[170:173], v[70:73], v[100:103]
	v_and_or_b32 v95, v78, v247, s4
	v_and_or_b32 v167, v79, v247, s88
	v_and_or_b32 v168, v80, v247, s89
	s_waitcnt lgkmcnt(0)
	v_mfma_f32_16x16x32_f16 v[118:121], v[198:201], v[38:41], v[96:99]
	v_mfma_f32_16x16x32_f16 v[96:99], v[198:201], v[70:73], v[96:99]
	v_and_or_b32 v169, v81, v247, s90
	v_and_or_b32 v170, v74, v247, s23
	v_mfma_f32_16x16x32_f16 v[78:81], v[174:177], v[34:37], v[86:89]
	v_mfma_f32_16x16x32_f16 v[86:89], v[174:177], v[66:69], v[100:103]
	v_min_f32 v103, v104, v236
	v_med3_f32 v104, v163, v161, v237
	s_nop 1
	v_and_or_b32 v101, v75, v247, s91
	v_and_or_b32 v102, v76, v247, s92
	v_and_or_b32 v100, v77, v247, s93
	v_mfma_f32_16x16x32_f16 v[74:77], v[202:205], v[34:37], v[118:121]
	v_med3_f32 v118, v103, v163, v237
	v_min_f32 v103, v103, v237
	v_mfma_f32_16x16x32_f16 v[96:99], v[202:205], v[66:69], v[96:99]
	v_and_or_b32 v119, v82, v247, s23
	v_and_or_b32 v120, v83, v247, s91
	v_med3_f32 v82, v110, v105, v238
	v_med3_f32 v83, v111, v110, v238
	v_mfma_f32_16x16x32_f16 v[78:81], v[178:181], v[30:33], v[78:81]
	v_min_f32 v110, v111, v238
	v_med3_f32 v111, v83, v82, v239
	s_addk_i32 s23, 0xc0
	v_mfma_f32_16x16x32_f16 v[86:89], v[178:181], v[62:65], v[86:89]
	v_and_or_b32 v105, v84, v247, s92
	v_and_or_b32 v121, v85, v247, s93
	v_med3_f32 v161, v110, v83, v239
	v_mfma_f32_16x16x32_f16 v[74:77], v[206:209], v[30:33], v[74:77]
	s_add_u32 s0, s0, 0x18000
	s_addc_u32 s1, s1, 0
	s_add_i32 s33, s33, 6
	v_mfma_f32_16x16x32_f16 v[82:85], v[206:209], v[62:65], v[96:99]
	v_min_f32 v96, v110, v239
	v_med3_f32 v97, v161, v111, v240
	v_med3_f32 v99, v118, v104, v162
	v_mfma_f32_16x16x32_f16 v[78:81], v[182:185], v[26:29], v[78:81]
	v_med3_f32 v98, v96, v161, v240
	v_min_f32 v96, v96, v240
	v_med3_f32 v104, v103, v118, v162
	v_mfma_f32_16x16x32_f16 v[86:89], v[182:185], v[58:61], v[86:89]
	v_med3_f32 v97, v98, v97, v241
	v_med3_f32 v98, v96, v98, v241
	v_min_f32 v96, v96, v241
	v_mfma_f32_16x16x32_f16 v[74:77], v[90:93], v[26:29], v[74:77]
	s_cmpk_eq_i32 s3, 0xf00
	v_mfma_f32_16x16x32_f16 v[82:85], v[90:93], v[58:61], v[82:85]
	v_min_f32 v90, v103, v162
	v_med3_f32 v91, v104, v99, v164
	v_med3_f32 v93, v98, v97, v95
	v_mfma_f32_16x16x32_f16 v[78:81], v[186:189], v[22:25], v[78:81]
	v_med3_f32 v92, v90, v104, v164
	v_min_f32 v90, v90, v164
	v_med3_f32 v97, v96, v98, v95
	v_mfma_f32_16x16x32_f16 v[86:89], v[186:189], v[54:57], v[86:89]
	v_med3_f32 v91, v92, v91, v165
	v_med3_f32 v92, v90, v92, v165
	v_min_f32 v90, v90, v165
	v_mfma_f32_16x16x32_f16 v[74:77], v[210:213], v[22:25], v[74:77]
	v_min_f32 v95, v96, v95
	v_med3_f32 v91, v92, v91, v166
	v_med3_f32 v93, v97, v93, v167
	v_mfma_f32_16x16x32_f16 v[82:85], v[210:213], v[54:57], v[82:85]
	v_med3_f32 v96, v95, v97, v167
	v_med3_f32 v92, v90, v92, v166
	v_min_f32 v90, v90, v166
	v_mfma_f32_16x16x32_f16 v[78:81], v[114:117], v[18:21], v[78:81]
	v_min_f32 v95, v95, v167
	v_med3_f32 v93, v96, v93, v168
	v_med3_f32 v91, v92, v91, v170
	v_mfma_f32_16x16x32_f16 v[86:89], v[114:117], v[50:53], v[86:89]
	v_med3_f32 v96, v95, v96, v168
	v_min_f32 v95, v95, v168
	v_med3_f32 v92, v90, v92, v170
	v_mfma_f32_16x16x32_f16 v[74:77], v[214:217], v[18:21], v[74:77]
	v_med3_f32 v97, v96, v93, v169
	v_med3_f32 v96, v95, v96, v169
	v_min_f32 v90, v90, v170
	v_mfma_f32_16x16x32_f16 v[82:85], v[214:217], v[50:53], v[82:85]
	v_med3_f32 v91, v92, v91, v101
	v_med3_f32 v98, v90, v92, v101
	v_min_f32 v99, v90, v101
	v_min_f32 v95, v95, v169
	v_mfma_f32_16x16x32_f16 v[78:81], v[190:193], v[14:17], v[78:81]
	v_med3_f32 v101, v98, v91, v102
	v_med3_f32 v103, v95, v96, v119
	v_min_f32 v95, v95, v119
	v_mfma_f32_16x16x32_f16 v[90:93], v[190:193], v[46:49], v[86:89]
	v_med3_f32 v86, v99, v98, v102
	v_min_f32 v87, v99, v102
	v_med3_f32 v102, v96, v97, v119
	v_mfma_f32_16x16x32_f16 v[74:77], v[218:221], v[14:17], v[74:77]
	v_med3_f32 v111, v86, v101, v100
	v_med3_f32 v101, v87, v86, v100
	v_min_f32 v110, v87, v100
	v_mfma_f32_16x16x32_f16 v[96:99], v[218:221], v[46:49], v[82:85]
	v_med3_f32 v100, v103, v102, v120
	v_med3_f32 v102, v95, v103, v120
	v_min_f32 v95, v95, v120
	v_mfma_f32_16x16x32_f16 v[86:89], v[194:197], v[10:13], v[78:81]
	v_mfma_f32_16x16x32_f16 v[82:85], v[194:197], v[42:45], v[90:93]
	v_med3_f32 v90, v102, v100, v105
	v_med3_f32 v91, v95, v102, v105
	v_min_f32 v92, v95, v105
	v_mfma_f32_16x16x32_f16 v[78:81], v[222:225], v[10:13], v[74:77]
	v_med3_f32 v100, v92, v91, v121
	v_mfma_f32_16x16x32_f16 v[74:77], v[222:225], v[42:45], v[96:99]
	v_med3_f32 v98, v91, v90, v121
	v_min_f32 v99, v92, v121
	s_cbranch_scc0 .LBB1_7
	s_add_u32 s0, s26, 0x88000
	v_readfirstlane_b32 s3, v112
	v_and_b32_e32 v90, 16, v0
	s_addc_u32 s1, s27, 0
	s_add_i32 s6, s3, 0x10000
	v_mov_b32_e32 v123, 0
	v_cmp_eq_u32_e64 s[4:5], 0, v90
	v_lshl_add_u64 v[90:91], s[0:1], 0, v[122:123]
	s_mov_b32 m0, s6
	s_nop 0
	global_load_lds_dwordx4 v[90:91], off
	s_add_i32 s6, s3, 0x10400
	v_mov_b32_e32 v107, v123
	v_lshl_add_u64 v[90:91], s[0:1], 0, v[106:107]
	s_add_u32 s0, s26, 0x8c000
	s_mov_b32 m0, s6
	s_nop 0
	global_load_lds_dwordx4 v[90:91], off
	s_addc_u32 s1, s27, 0
	s_add_i32 s6, s3, 0x14000
	v_lshl_add_u64 v[90:91], s[0:1], 0, v[122:123]
	s_mov_b32 m0, s6
	s_nop 0
	global_load_lds_dwordx4 v[90:91], off
	s_add_i32 s3, s3, 0x14400
	v_lshl_add_u64 v[90:91], s[0:1], 0, v[106:107]
	s_mov_b32 m0, s3
	s_nop 0
	global_load_lds_dwordx4 v[90:91], off
	ds_read_b128 v[90:93], v144
	ds_read_b128 v[114:117], v144 offset:8192
	v_add_u32_e32 v161, 0x18060, v94
	ds_read_b128 v[94:97], v161 offset:3840
	ds_read_b128 v[118:121], v161 offset:3904
	ds_read_b128 v[162:165], v143
	s_waitcnt lgkmcnt(2)
	v_mfma_f32_16x16x32_f16 v[102:105], v[90:93], v[38:41], v[94:97]
	ds_read_b128 v[166:169], v142
	ds_read_b128 v[174:177], v142 offset:8192
	ds_read_b128 v[178:181], v144 offset:24576
	v_mfma_f32_16x16x32_f16 v[90:93], v[90:93], v[70:73], v[94:97]
	ds_read_b128 v[182:185], v161 offset:4032
	ds_read_b128 v[186:189], v143 offset:16384
	s_add_u32 s0, s26, 0x90000
	s_waitcnt lgkmcnt(6)
	v_mfma_f32_16x16x32_f16 v[94:97], v[114:117], v[38:41], v[118:121]
	s_addc_u32 s1, s27, 0
	v_cmp_gt_u32_e64 s[6:7], 32, v131
	v_mfma_f32_16x16x32_f16 v[114:117], v[114:117], v[70:73], v[118:121]
	s_nop 2
	ds_read_b128 v[118:121], v143 offset:8192
	s_waitcnt lgkmcnt(6)
	v_mfma_f32_16x16x32_f16 v[102:105], v[162:165], v[34:37], v[102:105]
	v_mfma_f32_16x16x32_f16 v[162:165], v[162:165], v[66:69], v[90:93]
	s_waitcnt lgkmcnt(0)
	v_mfma_f32_16x16x32_f16 v[92:95], v[118:121], v[34:37], v[94:97]
	v_mfma_f32_16x16x32_f16 v[170:173], v[118:121], v[66:69], v[114:117]
	v_and_b32_e32 v78, 0xfffffc00, v78
	v_or_b32_e32 v90, 0x3b0, v78
	v_and_b32_e32 v78, 0xfffffc00, v79
	v_or_b32_e32 v91, 0x3b1, v78
	v_mfma_f32_16x16x32_f16 v[102:105], v[166:169], v[30:33], v[102:105]
	v_mfma_f32_16x16x32_f16 v[162:165], v[166:169], v[62:65], v[162:165]
	v_and_b32_e32 v78, 0xfffffc00, v80
	v_or_b32_e32 v118, 0x3b2, v78
	v_and_b32_e32 v78, 0xfffffc00, v81
	v_or_b32_e32 v115, 0x3b3, v78
	v_and_b32_e32 v74, 0xfffffc00, v74
	v_mfma_f32_16x16x32_f16 v[78:81], v[174:177], v[30:33], v[92:95]
	s_nop 2
	ds_read_b128 v[92:95], v141
	v_mfma_f32_16x16x32_f16 v[166:169], v[174:177], v[62:65], v[170:173]
	v_or_b32_e32 v114, 0x3b0, v74
	v_and_b32_e32 v74, 0xfffffc00, v75
	v_or_b32_e32 v116, 0x3b1, v74
	v_and_b32_e32 v74, 0xfffffc00, v76
	v_or_b32_e32 v117, 0x3b2, v74
	v_and_b32_e32 v96, 0xfffffc00, v77
	v_or_b32_e32 v119, 0x3b3, v96
	s_waitcnt lgkmcnt(0)
	v_mfma_f32_16x16x32_f16 v[74:77], v[92:95], v[26:29], v[102:105]
	ds_read_b128 v[170:173], v144 offset:16384
	ds_read_b128 v[174:177], v161 offset:3968
	v_mfma_f32_16x16x32_f16 v[92:95], v[92:95], v[58:61], v[162:165]
	ds_read_b128 v[102:105], v141 offset:8192
	s_nop 1
	ds_read_b128 v[162:165], v144 offset:256
	s_waitcnt lgkmcnt(1)
	v_mfma_f32_16x16x32_f16 v[78:81], v[102:105], v[26:29], v[78:81]
	v_mfma_f32_16x16x32_f16 v[102:105], v[102:105], v[58:61], v[166:169]
	s_waitcnt lgkmcnt(0)
	v_mfma_f32_16x16x32_f16 v[74:77], v[162:165], v[22:25], v[74:77]
	s_nop 0
	ds_read_b128 v[166:169], v141 offset:8448
	v_mfma_f32_16x16x32_f16 v[92:95], v[162:165], v[54:57], v[92:95]
	ds_read_b128 v[162:165], v144 offset:8448
	s_waitcnt lgkmcnt(0)
	v_mfma_f32_16x16x32_f16 v[78:81], v[162:165], v[22:25], v[78:81]
	v_mfma_f32_16x16x32_f16 v[102:105], v[162:165], v[54:57], v[102:105]
	ds_read_b128 v[162:165], v143 offset:256
	s_waitcnt lgkmcnt(0)
	v_mfma_f32_16x16x32_f16 v[74:77], v[162:165], v[18:21], v[74:77]
	v_mfma_f32_16x16x32_f16 v[92:95], v[162:165], v[50:53], v[92:95]
	ds_read_b128 v[162:165], v143 offset:8448
	s_waitcnt lgkmcnt(0)
	v_mfma_f32_16x16x32_f16 v[78:81], v[162:165], v[18:21], v[78:81]
	v_mfma_f32_16x16x32_f16 v[102:105], v[162:165], v[50:53], v[102:105]
	ds_read_b128 v[162:165], v142 offset:256
	s_waitcnt lgkmcnt(0)
	v_mfma_f32_16x16x32_f16 v[74:77], v[162:165], v[14:17], v[74:77]
	v_mfma_f32_16x16x32_f16 v[92:95], v[162:165], v[46:49], v[92:95]
	ds_read_b128 v[162:165], v142 offset:8448
	s_waitcnt lgkmcnt(0)
	v_mfma_f32_16x16x32_f16 v[78:81], v[162:165], v[14:17], v[78:81]
	v_mfma_f32_16x16x32_f16 v[102:105], v[162:165], v[46:49], v[102:105]
	ds_read_b128 v[162:165], v141 offset:256
	s_waitcnt lgkmcnt(0)
	v_mfma_f32_16x16x32_f16 v[74:77], v[162:165], v[10:13], v[74:77]
	v_mfma_f32_16x16x32_f16 v[92:95], v[162:165], v[42:45], v[92:95]
	s_nop 6
	v_and_b32_e32 v74, 0xfffffc00, v74
	v_or_b32_e32 v120, 0x3c0, v74
	v_and_b32_e32 v74, 0xfffffc00, v75
	v_or_b32_e32 v121, 0x3c1, v74
	v_and_b32_e32 v74, 0xfffffc00, v76
	v_mfma_f32_16x16x32_f16 v[78:81], v[166:169], v[10:13], v[78:81]
	v_mfma_f32_16x16x32_f16 v[102:105], v[166:169], v[42:45], v[102:105]
	v_or_b32_e32 v162, 0x3c2, v74
	v_and_b32_e32 v74, 0xfffffc00, v77
	v_or_b32_e32 v163, 0x3c3, v74
	v_and_b32_e32 v74, 0xfffffc00, v92
	v_or_b32_e32 v166, 0x3c0, v74
	v_mfma_f32_16x16x32_f16 v[74:77], v[170:173], v[38:41], v[174:177]
	v_mfma_f32_16x16x32_f16 v[174:177], v[170:173], v[70:73], v[174:177]
	v_and_b32_e32 v92, 0xfffffc00, v93
	v_or_b32_e32 v168, 0x3c1, v92
	v_and_b32_e32 v92, 0xfffffc00, v94
	v_or_b32_e32 v169, 0x3c2, v92
	v_and_b32_e32 v96, 0xfffffc00, v95
	v_mfma_f32_16x16x32_f16 v[92:95], v[178:181], v[38:41], v[182:185]
	v_mfma_f32_16x16x32_f16 v[178:181], v[178:181], v[70:73], v[182:185]
	v_and_b32_e32 v78, 0xfffffc00, v78
	v_or_b32_e32 v171, 0x3d0, v78
	v_and_b32_e32 v78, 0xfffffc00, v79
	ds_read_b128 v[182:185], v143 offset:24576
	v_or_b32_e32 v170, 0x3c3, v96
	v_or_b32_e32 v172, 0x3d1, v78
	v_mfma_f32_16x16x32_f16 v[74:77], v[186:189], v[34:37], v[74:77]
	v_mfma_f32_16x16x32_f16 v[174:177], v[186:189], v[66:69], v[174:177]
	v_and_b32_e32 v78, 0xfffffc00, v80
	v_or_b32_e32 v173, 0x3d2, v78
	v_and_b32_e32 v78, 0xfffffc00, v81
	v_or_b32_e32 v198, 0x3d3, v78
	v_and_b32_e32 v96, 0xfffffc00, v102
	s_waitcnt lgkmcnt(0)
	v_mfma_f32_16x16x32_f16 v[78:81], v[182:185], v[34:37], v[92:95]
	ds_read_b128 v[186:189], v141 offset:24832
	s_nop 1
	ds_read_b128 v[92:95], v142 offset:16384
	v_mfma_f32_16x16x32_f16 v[178:181], v[182:185], v[66:69], v[178:181]
	v_or_b32_e32 v164, 0x3d0, v96
	v_and_b32_e32 v96, 0xfffffc00, v103
	v_or_b32_e32 v161, 0x3d1, v96
	v_and_b32_e32 v96, 0xfffffc00, v104
	v_or_b32_e32 v165, 0x3d2, v96
	s_waitcnt lgkmcnt(0)
	v_mfma_f32_16x16x32_f16 v[74:77], v[92:95], v[30:33], v[74:77]
	ds_read_b128 v[182:185], v141 offset:16640
	v_mfma_f32_16x16x32_f16 v[92:95], v[92:95], v[62:65], v[174:177]
	v_and_b32_e32 v96, 0xfffffc00, v105
	s_nop 1
	ds_read_b128 v[174:177], v142 offset:24576
	s_waitcnt lgkmcnt(0)
	v_mfma_f32_16x16x32_f16 v[78:81], v[174:177], v[30:33], v[78:81]
	v_mfma_f32_16x16x32_f16 v[102:105], v[174:177], v[62:65], v[178:181]
	ds_read_b128 v[174:177], v141 offset:16384
	s_waitcnt lgkmcnt(0)
	v_mfma_f32_16x16x32_f16 v[74:77], v[174:177], v[26:29], v[74:77]
	ds_read_b128 v[178:181], v142 offset:24832
	v_mfma_f32_16x16x32_f16 v[92:95], v[174:177], v[58:61], v[92:95]
	ds_read_b128 v[174:177], v141 offset:24576
	s_waitcnt lgkmcnt(0)
	v_mfma_f32_16x16x32_f16 v[78:81], v[174:177], v[26:29], v[78:81]
	v_mfma_f32_16x16x32_f16 v[102:105], v[174:177], v[58:61], v[102:105]
	ds_read_b128 v[174:177], v144 offset:16640
	s_waitcnt lgkmcnt(0)
	v_mfma_f32_16x16x32_f16 v[74:77], v[174:177], v[22:25], v[74:77]
	v_mfma_f32_16x16x32_f16 v[92:95], v[174:177], v[54:57], v[92:95]
	ds_read_b128 v[174:177], v144 offset:24832
	s_waitcnt lgkmcnt(0)
	v_mfma_f32_16x16x32_f16 v[78:81], v[174:177], v[22:25], v[78:81]
	v_mfma_f32_16x16x32_f16 v[102:105], v[174:177], v[54:57], v[102:105]
	ds_read_b128 v[174:177], v143 offset:16640
	s_waitcnt lgkmcnt(0)
	v_mfma_f32_16x16x32_f16 v[74:77], v[174:177], v[18:21], v[74:77]
	v_mfma_f32_16x16x32_f16 v[92:95], v[174:177], v[50:53], v[92:95]
	ds_read_b128 v[174:177], v143 offset:24832
	s_waitcnt lgkmcnt(0)
	v_mfma_f32_16x16x32_f16 v[78:81], v[174:177], v[18:21], v[78:81]
	v_mfma_f32_16x16x32_f16 v[78:81], v[178:181], v[14:17], v[78:81]
	v_mfma_f32_16x16x32_f16 v[78:81], v[186:189], v[10:13], v[78:81]
	v_mfma_f32_16x16x32_f16 v[102:105], v[174:177], v[50:53], v[102:105]
	ds_read_b128 v[174:177], v142 offset:16640
	s_waitcnt vmcnt(4)
	s_waitcnt lgkmcnt(0)
	s_waitcnt lgkmcnt(0)
	v_mfma_f32_16x16x32_f16 v[74:77], v[174:177], v[14:17], v[74:77]
	s_barrier
	s_nop 2
	v_and_b32_e32 v78, 0xfffffc00, v78
	v_or_b32_e32 v78, 0x3f0, v78
	v_mfma_f32_16x16x32_f16 v[92:95], v[174:177], v[46:49], v[92:95]
	v_and_b32_e32 v79, 0xfffffc00, v79
	v_or_b32_e32 v79, 0x3f1, v79
	v_mfma_f32_16x16x32_f16 v[174:177], v[178:181], v[46:49], v[102:105]
	v_mfma_f32_16x16x32_f16 v[102:105], v[182:185], v[10:13], v[74:77]
	v_or_b32_e32 v167, 0x3d3, v96
	v_readfirstlane_b32 s3, v112
	v_lshl_add_u64 v[96:97], s[0:1], 0, v[122:123]
	s_mov_b32 m0, s3
	s_nop 0
	global_load_lds_dwordx4 v[96:97], off
	s_addk_i32 s3, 0x400
	v_lshl_add_u64 v[96:97], s[0:1], 0, v[106:107]
	s_add_u32 s0, s26, 0x94000
	s_mov_b32 m0, s3
	s_nop 0
	global_load_lds_dwordx4 v[96:97], off
	s_addc_u32 s1, s27, 0
	v_readfirstlane_b32 s3, v113
	v_lshl_add_u64 v[74:75], s[0:1], 0, v[122:123]
	s_mov_b32 m0, s3
	s_nop 0
	global_load_lds_dwordx4 v[74:75], off
	s_addk_i32 s3, 0x400
	v_lshl_add_u64 v[74:75], s[0:1], 0, v[106:107]
	s_mov_b32 m0, s3
	s_nop 0
	global_load_lds_dwordx4 v[74:75], off
	v_mfma_f32_16x16x32_f16 v[74:77], v[186:189], v[42:45], v[174:177]
	ds_read_b128 v[190:193], v143 offset:32768
	ds_read_b128 v[194:197], v144 offset:41216
	s_add_u32 s0, s26, 0x98000
	ds_read_b128 v[174:177], v144 offset:32768
	v_mfma_f32_16x16x32_f16 v[94:97], v[182:185], v[42:45], v[92:95]
	ds_read_b128 v[182:185], v144 offset:40960
	v_and_b32_e32 v86, 0xfffffc00, v86
	v_or_b32_e32 v86, 0x3a0, v86
	s_waitcnt lgkmcnt(1)
	v_mfma_f32_16x16x32_f16 v[178:181], v[174:177], v[38:41], 0
	v_med3_f32 v92, v101, v111, v86
	v_med3_f32 v93, v110, v101, v86
	v_min_f32 v86, v110, v86
	v_mfma_f32_16x16x32_f16 v[174:177], v[174:177], v[70:73], 0
	ds_read_b128 v[110:113], v143 offset:33024
	v_and_b32_e32 v87, 0xfffffc00, v87
	v_or_b32_e32 v87, 0x3a1, v87
	v_mfma_f32_16x16x32_f16 v[178:181], v[190:193], v[34:37], v[178:181]
	v_and_b32_e32 v88, 0xfffffc00, v88
	v_and_b32_e32 v89, 0xfffffc00, v89
	v_and_b32_e32 v82, 0xfffffc00, v82
	v_mfma_f32_16x16x32_f16 v[174:177], v[190:193], v[66:69], v[174:177]
	ds_read_b128 v[190:193], v143 offset:40960
	v_or_b32_e32 v88, 0x3a2, v88
	v_or_b32_e32 v89, 0x3a3, v89
	s_waitcnt lgkmcnt(2)
	v_mfma_f32_16x16x32_f16 v[186:189], v[182:185], v[38:41], 0
	v_or_b32_e32 v82, 0x3a0, v82
	v_and_b32_e32 v83, 0xfffffc00, v83
	v_med3_f32 v98, v100, v98, v82
	v_mfma_f32_16x16x32_f16 v[182:185], v[182:185], v[70:73], 0
	v_or_b32_e32 v83, 0x3a1, v83
	v_med3_f32 v92, v93, v92, v87
	v_med3_f32 v93, v86, v93, v87
	s_waitcnt lgkmcnt(0)
	v_mfma_f32_16x16x32_f16 v[186:189], v[190:193], v[34:37], v[186:189]
	v_min_f32 v86, v86, v87
	v_med3_f32 v87, v93, v92, v88
	v_and_b32_e32 v84, 0xfffffc00, v84
	v_mfma_f32_16x16x32_f16 v[182:185], v[190:193], v[66:69], v[182:185]
	ds_read_b128 v[190:193], v142 offset:32768
	v_med3_f32 v92, v86, v93, v88
	v_min_f32 v86, v86, v88
	s_waitcnt lgkmcnt(0)
	v_mfma_f32_16x16x32_f16 v[178:181], v[190:193], v[30:33], v[178:181]
	v_med3_f32 v93, v92, v87, v89
	v_med3_f32 v92, v86, v92, v89
	v_and_b32_e32 v85, 0xfffffc00, v85
	v_mfma_f32_16x16x32_f16 v[174:177], v[190:193], v[62:65], v[174:177]
	ds_read_b128 v[190:193], v142 offset:40960
	v_or_b32_e32 v84, 0x3a2, v84
	v_or_b32_e32 v85, 0x3a3, v85
	s_waitcnt lgkmcnt(0)
	v_mfma_f32_16x16x32_f16 v[186:189], v[190:193], v[30:33], v[186:189]
	s_addc_u32 s1, s27, 0
	v_and_b32_e32 v102, 0xfffffc00, v102
	v_or_b32_e32 v102, 0x3e0, v102
	v_mfma_f32_16x16x32_f16 v[182:185], v[190:193], v[62:65], v[182:185]
	ds_read_b128 v[190:193], v141 offset:32768
	v_and_b32_e32 v103, 0xfffffc00, v103
	v_or_b32_e32 v103, 0x3e1, v103
	s_waitcnt lgkmcnt(0)
	v_mfma_f32_16x16x32_f16 v[178:181], v[190:193], v[26:29], v[178:181]
	v_and_b32_e32 v94, 0xfffffc00, v94
	v_or_b32_e32 v94, 0x3e0, v94
	v_and_b32_e32 v95, 0xfffffc00, v95
	v_mfma_f32_16x16x32_f16 v[174:177], v[190:193], v[58:61], v[174:177]
	ds_read_b128 v[190:193], v141 offset:40960
	v_or_b32_e32 v95, 0x3e1, v95
	v_and_b32_e32 v74, 0xfffffc00, v74
	s_waitcnt lgkmcnt(0)
	v_mfma_f32_16x16x32_f16 v[186:189], v[190:193], v[26:29], v[186:189]
	v_or_b32_e32 v74, 0x3f0, v74
	v_and_b32_e32 v75, 0xfffffc00, v75
	v_or_b32_e32 v75, 0x3f1, v75
	v_mfma_f32_16x16x32_f16 v[182:185], v[190:193], v[58:61], v[182:185]
	ds_read_b128 v[190:193], v144 offset:33024
	s_waitcnt lgkmcnt(0)
	v_mfma_f32_16x16x32_f16 v[178:181], v[190:193], v[22:25], v[178:181]
	v_mfma_f32_16x16x32_f16 v[174:177], v[190:193], v[54:57], v[174:177]
	ds_read_b128 v[190:193], v143 offset:41216
	v_mfma_f32_16x16x32_f16 v[186:189], v[194:197], v[22:25], v[186:189]
	v_mfma_f32_16x16x32_f16 v[182:185], v[194:197], v[54:57], v[182:185]
	v_min_f32 v194, v86, v89
	ds_read_b128 v[86:89], v142 offset:33024
	v_mfma_f32_16x16x32_f16 v[178:181], v[110:113], v[18:21], v[178:181]
	v_mfma_f32_16x16x32_f16 v[110:113], v[110:113], v[50:53], v[174:177]
	s_waitcnt lgkmcnt(1)
	v_mfma_f32_16x16x32_f16 v[174:177], v[190:193], v[18:21], v[186:189]
	v_med3_f32 v186, v99, v100, v82
	v_min_f32 v82, v99, v82
	s_nop 0
	v_med3_f32 v187, v186, v98, v83
	v_mfma_f32_16x16x32_f16 v[98:101], v[190:193], v[50:53], v[182:185]
	v_med3_f32 v186, v82, v186, v83
	v_min_f32 v82, v82, v83
	s_nop 0
	v_med3_f32 v83, v186, v187, v84
	v_med3_f32 v186, v82, v186, v84
	s_nop 1
	ds_read_b128 v[182:185], v142 offset:41216
	v_min_f32 v82, v82, v84
	v_med3_f32 v190, v186, v83, v85
	s_waitcnt lgkmcnt(0)
	v_mfma_f32_16x16x32_f16 v[174:177], v[182:185], v[14:17], v[174:177]
	v_med3_f32 v191, v82, v186, v85
	ds_read_b128 v[186:189], v141 offset:33024
	v_min_f32 v192, v82, v85
	v_mfma_f32_16x16x32_f16 v[82:85], v[182:185], v[46:49], v[98:101]
	ds_read_b128 v[182:185], v141 offset:41216
	v_mfma_f32_16x16x32_f16 v[178:181], v[86:89], v[14:17], v[178:181]
	v_mfma_f32_16x16x32_f16 v[110:113], v[86:89], v[46:49], v[110:113]
	v_med3_f32 v86, v92, v93, v90
	v_med3_f32 v92, v194, v92, v90
	v_min_f32 v90, v194, v90
	s_waitcnt lgkmcnt(0)
	v_mfma_f32_16x16x32_f16 v[82:85], v[182:185], v[42:45], v[82:85]
	v_med3_f32 v93, v92, v86, v91
	v_med3_f32 v98, v90, v92, v91
	v_min_f32 v99, v90, v91
	v_mfma_f32_16x16x32_f16 v[86:89], v[186:189], v[10:13], v[178:181]
	v_med3_f32 v178, v98, v93, v118
	v_med3_f32 v179, v99, v98, v118
	v_min_f32 v118, v99, v118
	v_mfma_f32_16x16x32_f16 v[90:93], v[186:189], v[42:45], v[110:113]
	v_med3_f32 v193, v179, v178, v115
	v_med3_f32 v194, v118, v179, v115
	v_min_f32 v118, v118, v115
	v_mfma_f32_16x16x32_f16 v[98:101], v[182:185], v[10:13], v[174:177]
	v_med3_f32 v115, v191, v190, v114
	s_nop 2
	ds_read_b128 v[110:113], v143 offset:49152
	v_med3_f32 v182, v192, v191, v114
	v_min_f32 v114, v192, v114
	s_waitcnt lgkmcnt(0)
	v_mfma_f32_16x16x32_f16 v[178:181], v[110:113], v[34:37], 0
	ds_read_b128 v[174:177], v143 offset:57344
	v_med3_f32 v115, v182, v115, v116
	v_med3_f32 v190, v114, v182, v116
	ds_read_b128 v[182:185], v142 offset:49152
	v_min_f32 v114, v114, v116
	v_med3_f32 v115, v190, v115, v117
	v_mfma_f32_16x16x32_f16 v[110:113], v[110:113], v[66:69], 0
	v_med3_f32 v190, v114, v190, v117
	v_min_f32 v191, v114, v117
	v_fma_mix_f32 v86, v86, v38, 0 op_sel_hi:[0,1,0]
	s_waitcnt lgkmcnt(1)
	v_mfma_f32_16x16x32_f16 v[186:189], v[174:177], v[34:37], 0
	v_med3_f32 v192, v190, v115, v119
	v_med3_f32 v190, v191, v190, v119
	v_min_f32 v191, v191, v119
	v_mfma_f32_16x16x32_f16 v[114:117], v[174:177], v[66:69], 0
	ds_read_b128 v[174:177], v142 offset:57344
	v_med3_f32 v119, v194, v193, v120
	v_med3_f32 v193, v118, v194, v120
	v_min_f32 v118, v118, v120
	s_waitcnt lgkmcnt(1)
	v_mfma_f32_16x16x32_f16 v[178:181], v[182:185], v[30:33], v[178:181]
	v_med3_f32 v119, v193, v119, v121
	v_med3_f32 v120, v118, v193, v121
	v_min_f32 v118, v118, v121
	v_mfma_f32_16x16x32_f16 v[110:113], v[182:185], v[62:65], v[110:113]
	v_med3_f32 v119, v120, v119, v162
	ds_read_b128 v[182:185], v141 offset:49152
	v_med3_f32 v193, v118, v120, v162
	v_min_f32 v162, v118, v162
	s_waitcnt lgkmcnt(1)
	v_mfma_f32_16x16x32_f16 v[186:189], v[174:177], v[30:33], v[186:189]
	v_med3_f32 v194, v193, v119, v163
	ds_read_b128 v[118:121], v141 offset:57344
	v_med3_f32 v193, v162, v193, v163
	v_mfma_f32_16x16x32_f16 v[114:117], v[174:177], v[62:65], v[114:117]
	v_min_f32 v162, v162, v163
	v_med3_f32 v163, v190, v192, v166
	v_med3_f32 v190, v191, v190, v166
	s_waitcnt lgkmcnt(1)
	v_mfma_f32_16x16x32_f16 v[174:177], v[182:185], v[26:29], v[178:181]
	v_min_f32 v166, v191, v166
	v_med3_f32 v163, v190, v163, v168
	v_fma_mix_f32 v38, v87, v38, v86 op_sel:[0,1,0] op_sel_hi:[0,1,0]
	v_mfma_f32_16x16x32_f16 v[110:113], v[182:185], v[58:61], v[110:113]
	v_fma_mix_f32 v90, v90, v70, 0 op_sel_hi:[0,1,0]
	ds_read_b128 v[178:181], v144 offset:49408
	v_fma_mix_f32 v38, v88, v39, v38 op_sel_hi:[0,1,0]
	s_waitcnt lgkmcnt(1)
	v_mfma_f32_16x16x32_f16 v[182:185], v[118:121], v[26:29], v[186:189]
	v_med3_f32 v186, v166, v190, v168
	v_min_f32 v166, v166, v168
	v_fma_mix_f32 v70, v91, v70, v90 op_sel:[0,1,0] op_sel_hi:[0,1,0]
	v_mfma_f32_16x16x32_f16 v[114:117], v[118:121], v[58:61], v[114:117]
	ds_read_b128 v[118:121], v144 offset:57600
	v_med3_f32 v163, v186, v163, v169
	v_med3_f32 v168, v166, v186, v169
	s_waitcnt lgkmcnt(1)
	v_mfma_f32_16x16x32_f16 v[174:177], v[178:181], v[22:25], v[174:177]
	v_min_f32 v166, v166, v169
	v_med3_f32 v192, v168, v163, v170
	v_med3_f32 v163, v193, v194, v171
	v_mfma_f32_16x16x32_f16 v[110:113], v[178:181], v[54:57], v[110:113]
	ds_read_b128 v[178:181], v143 offset:49408
	v_med3_f32 v195, v166, v168, v170
	v_med3_f32 v168, v162, v193, v171
	s_waitcnt lgkmcnt(1)
	v_mfma_f32_16x16x32_f16 v[182:185], v[118:121], v[22:25], v[182:185]
	v_min_f32 v162, v162, v171
	v_med3_f32 v163, v168, v163, v172
	v_min_f32 v166, v166, v170
	v_mfma_f32_16x16x32_f16 v[114:117], v[118:121], v[54:57], v[114:117]
	ds_read_b128 v[118:121], v143 offset:57600
	v_med3_f32 v186, v162, v168, v172
	v_min_f32 v162, v162, v172
	s_waitcnt lgkmcnt(1)
	v_mfma_f32_16x16x32_f16 v[168:171], v[178:181], v[18:21], v[174:177]
	v_med3_f32 v172, v162, v186, v173
	v_med3_f32 v163, v186, v163, v173
	v_min_f32 v162, v162, v173
	v_mfma_f32_16x16x32_f16 v[110:113], v[178:181], v[50:53], v[110:113]
	v_med3_f32 v193, v172, v163, v198
	v_med3_f32 v194, v162, v172, v198
	s_nop 1
	ds_read_b128 v[172:175], v142 offset:49408
	s_waitcnt lgkmcnt(1)
	v_mfma_f32_16x16x32_f16 v[176:179], v[118:121], v[18:21], v[182:185]
	v_min_f32 v196, v162, v198
	ds_read_b128 v[188:191], v141 offset:57600
	v_lshl_add_u64 v[162:163], s[0:1], 0, v[122:123]
	v_readfirstlane_b32 s3, v108
	ds_read_b128 v[184:187], v142 offset:57600
	ds_read_b128 v[180:183], v141 offset:49408
	s_waitcnt vmcnt(4)
	s_waitcnt lgkmcnt(0)
	s_barrier
	s_mov_b32 m0, s3
	s_nop 0
	global_load_lds_dwordx4 v[162:163], off
	s_addk_i32 s3, 0x400
	v_lshl_add_u64 v[162:163], s[0:1], 0, v[106:107]
	s_add_u32 s0, s26, 0x9c000
	s_mov_b32 m0, s3
	s_nop 0
	global_load_lds_dwordx4 v[162:163], off
	s_addc_u32 s1, s27, 0
	v_lshl_add_u64 v[106:107], s[0:1], 0, v[106:107]
	v_readfirstlane_b32 s3, v109
	v_lshl_add_u64 v[108:109], s[0:1], 0, v[122:123]
	s_mov_b32 m0, s3
	s_nop 0
	global_load_lds_dwordx4 v[108:109], off
	s_addk_i32 s3, 0x400
	s_mov_b32 m0, s3
	s_nop 0
	global_load_lds_dwordx4 v[106:107], off
	v_mfma_f32_16x16x32_f16 v[114:117], v[118:121], v[50:53], v[114:117]
	v_med3_f32 v122, v195, v192, v164
	v_med3_f32 v162, v166, v195, v164
	v_min_f32 v163, v166, v164
	s_waitcnt lgkmcnt(3)
	v_mfma_f32_16x16x32_f16 v[118:121], v[172:175], v[14:17], v[168:171]
	v_med3_f32 v122, v162, v122, v161
	v_med3_f32 v162, v163, v162, v161
	v_min_f32 v161, v163, v161
	s_waitcnt lgkmcnt(1)
	v_mfma_f32_16x16x32_f16 v[168:171], v[184:187], v[14:17], v[176:179]
	v_med3_f32 v122, v162, v122, v165
	v_med3_f32 v166, v161, v162, v165
	v_min_f32 v161, v161, v165
	v_mfma_f32_16x16x32_f16 v[106:109], v[188:191], v[10:13], v[168:171]
	ds_read_b128 v[162:165], v154
	s_nop 0
	ds_read_b128 v[176:179], v156
	v_med3_f32 v122, v166, v122, v167
	v_mfma_f32_16x16x32_f16 v[110:113], v[172:175], v[46:49], v[110:113]
	s_nop 2
	ds_read_b128 v[168:171], v155
	v_fma_mix_f32 v38, v89, v39, v38 op_sel:[0,1,0] op_sel_hi:[0,1,0]
	v_fma_mix_f32 v70, v92, v71, v70 op_sel_hi:[0,1,0]
	v_mfma_f32_16x16x32_f16 v[172:175], v[184:187], v[46:49], v[114:117]
	ds_read_b128 v[184:187], v153
	v_fma_mix_f32 v39, v93, v71, v70 op_sel:[0,1,0] op_sel_hi:[0,1,0]
	v_fma_mix_f32 v38, v98, v40, v38 op_sel_hi:[0,1,0]
	s_waitcnt lgkmcnt(4)
	v_mfma_f32_16x16x32_f16 v[114:117], v[180:183], v[10:13], v[118:121]
	v_fma_mix_f32 v39, v82, v72, v39 op_sel_hi:[0,1,0]
	v_fma_mix_f32 v38, v99, v40, v38 op_sel:[0,1,0] op_sel_hi:[0,1,0]
	v_fma_mix_f32 v39, v83, v72, v39 op_sel:[0,1,0] op_sel_hi:[0,1,0]
	v_mfma_f32_16x16x32_f16 v[118:121], v[180:183], v[42:45], v[110:113]
	v_fma_mix_f32 v38, v100, v41, v38 op_sel_hi:[0,1,0]
	v_fma_mix_f32 v70, v84, v73, v39 op_sel_hi:[0,1,0]
	v_fma_mix_f32 v71, v101, v41, v38 op_sel:[0,1,0] op_sel_hi:[0,1,0]
	v_mfma_f32_16x16x32_f16 v[110:113], v[188:191], v[42:45], v[172:175]
	v_med3_f32 v188, v161, v166, v167
	v_min_f32 v189, v161, v167
	v_med3_f32 v161, v194, v193, v102
	s_waitcnt lgkmcnt(2)
	v_mfma_f32_16x16x32_f16 v[172:175], v[176:179], v[30:33], 0
	v_med3_f32 v190, v196, v194, v102
	v_min_f32 v102, v196, v102
	v_med3_f32 v122, v188, v122, v94
	v_mfma_f32_16x16x32_f16 v[176:179], v[176:179], v[62:65], 0
	v_med3_f32 v161, v190, v161, v103
	v_fma_mix_f32 v70, v85, v73, v70 op_sel:[0,1,0] op_sel_hi:[0,1,0]
	v_fma_mix_f32 v82, v114, v34, v71 op_sel_hi:[0,1,0]
	s_waitcnt lgkmcnt(1)
	v_mfma_f32_16x16x32_f16 v[180:183], v[168:171], v[30:33], 0
	v_fma_mix_f32 v83, v118, v66, v70 op_sel_hi:[0,1,0]
	v_fma_mix_f32 v34, v115, v34, v82 op_sel:[0,1,0] op_sel_hi:[0,1,0]
	v_fma_mix_f32 v66, v119, v66, v83 op_sel:[0,1,0] op_sel_hi:[0,1,0]
	v_mfma_f32_16x16x32_f16 v[166:169], v[168:171], v[62:65], 0
	v_fma_mix_f32 v34, v116, v35, v34 op_sel_hi:[0,1,0]
	v_fma_mix_f32 v66, v120, v67, v66 op_sel_hi:[0,1,0]
	v_fma_mix_f32 v34, v117, v35, v34 op_sel:[0,1,0] op_sel_hi:[0,1,0]
	v_mfma_f32_16x16x32_f16 v[170:173], v[162:165], v[26:29], v[172:175]
	v_fma_mix_f32 v35, v121, v67, v66 op_sel:[0,1,0] op_sel_hi:[0,1,0]
	v_fma_mix_f32 v34, v106, v36, v34 op_sel_hi:[0,1,0]
	v_fma_mix_f32 v35, v110, v68, v35 op_sel_hi:[0,1,0]
	v_mfma_f32_16x16x32_f16 v[162:165], v[162:165], v[58:61], v[176:179]
	v_fma_mix_f32 v34, v107, v36, v34 op_sel:[0,1,0] op_sel_hi:[0,1,0]
	v_fma_mix_f32 v35, v111, v68, v35 op_sel:[0,1,0] op_sel_hi:[0,1,0]
	v_fma_mix_f32 v34, v108, v37, v34 op_sel_hi:[0,1,0]
	ds_read_b128 v[174:177], v160 offset:256
	v_med3_f32 v160, v102, v190, v103
	v_min_f32 v102, v102, v103
	v_and_b32_e32 v103, 0xfffffc00, v104
	s_waitcnt lgkmcnt(1)
	v_mfma_f32_16x16x32_f16 v[178:181], v[184:187], v[26:29], v[180:183]
	v_or_b32_e32 v103, 0x3e2, v103
	v_med3_f32 v161, v160, v161, v103
	v_fma_mix_f32 v35, v112, v69, v35 op_sel_hi:[0,1,0]
	v_mfma_f32_16x16x32_f16 v[166:169], v[184:187], v[58:61], v[166:169]
	ds_read_b128 v[182:185], v159 offset:256
	v_and_b32_e32 v159, 0xfffffc00, v105
	v_med3_f32 v186, v102, v160, v103
	s_waitcnt lgkmcnt(1)
	v_mfma_f32_16x16x32_f16 v[170:173], v[174:177], v[22:25], v[170:173]
	v_min_f32 v187, v102, v103
	v_fma_mix_f32 v34, v109, v37, v34 op_sel:[0,1,0] op_sel_hi:[0,1,0]
	v_fma_mix_f32 v66, v113, v69, v35 op_sel:[0,1,0] op_sel_hi:[0,1,0]
	v_mfma_f32_16x16x32_f16 v[102:105], v[174:177], v[54:57], v[162:165]
	v_or_b32_e32 v174, 0x3e3, v159
	v_med3_f32 v190, v186, v161, v174
	ds_read_b128 v[158:161], v158 offset:256
	s_waitcnt lgkmcnt(1)
	v_mfma_f32_16x16x32_f16 v[162:165], v[182:185], v[22:25], v[178:181]
	v_med3_f32 v178, v187, v186, v174
	v_min_f32 v179, v187, v174
	ds_read_b128 v[174:177], v157 offset:256
	s_waitcnt lgkmcnt(1)
	v_mfma_f32_16x16x32_f16 v[170:173], v[158:161], v[18:21], v[170:173]
	v_med3_f32 v180, v189, v188, v94
	v_min_f32 v94, v189, v94
	v_mfma_f32_16x16x32_f16 v[102:105], v[158:161], v[50:53], v[102:105]
	ds_read_b128 v[156:159], v156 offset:256
	v_med3_f32 v122, v180, v122, v95
	v_med3_f32 v180, v94, v180, v95
	v_mfma_f32_16x16x32_f16 v[166:169], v[182:185], v[54:57], v[166:169]
	v_min_f32 v94, v94, v95
	v_and_b32_e32 v95, 0xfffffc00, v96
	v_or_b32_e32 v95, 0x3e2, v95
	s_waitcnt lgkmcnt(1)
	v_mfma_f32_16x16x32_f16 v[160:163], v[174:177], v[18:21], v[162:165]
	v_med3_f32 v122, v180, v122, v95
	v_mfma_f32_16x16x32_f16 v[164:167], v[174:177], v[50:53], v[166:169]
	ds_read_b128 v[174:177], v155 offset:256
	v_and_b32_e32 v155, 0xfffffc00, v97
	s_waitcnt lgkmcnt(1)
	v_mfma_f32_16x16x32_f16 v[168:171], v[156:159], v[14:17], v[170:173]
	v_med3_f32 v172, v94, v180, v95
	v_min_f32 v173, v94, v95
	v_mfma_f32_16x16x32_f16 v[94:97], v[156:159], v[46:49], v[102:105]
	v_or_b32_e32 v158, 0x3e3, v155
	v_med3_f32 v122, v172, v122, v158
	v_med3_f32 v182, v173, v172, v158
	v_min_f32 v183, v173, v158
	v_med3_f32 v172, v178, v190, v78
	s_nop 1
	ds_read_b128 v[102:105], v154 offset:256
	s_waitcnt lgkmcnt(1)
	v_mfma_f32_16x16x32_f16 v[154:157], v[174:177], v[14:17], v[160:163]
	v_med3_f32 v122, v182, v122, v74
	v_med3_f32 v182, v183, v182, v74
	v_min_f32 v74, v183, v74
	v_mfma_f32_16x16x32_f16 v[158:161], v[174:177], v[46:49], v[164:167]
	v_and_b32_e32 v175, 0xfffffc00, v81
	v_med3_f32 v122, v182, v122, v75
	v_med3_f32 v182, v74, v182, v75
	s_waitcnt lgkmcnt(0)
	v_mfma_f32_16x16x32_f16 v[166:169], v[102:105], v[10:13], v[168:171]
	v_min_f32 v74, v74, v75
	ds_read_b128 v[162:165], v153 offset:256
	v_med3_f32 v153, v179, v178, v78
	v_mfma_f32_16x16x32_f16 v[94:97], v[102:105], v[42:45], v[94:97]
	ds_read_b128 v[102:105], v146
	v_min_f32 v78, v179, v78
	v_med3_f32 v170, v153, v172, v79
	s_waitcnt lgkmcnt(1)
	v_mfma_f32_16x16x32_f16 v[154:157], v[162:165], v[10:13], v[154:157]
	v_med3_f32 v153, v78, v153, v79
	v_min_f32 v78, v78, v79
	v_and_b32_e32 v79, 0xfffffc00, v80
	v_or_b32_e32 v79, 0x3f2, v79
	v_mfma_f32_16x16x32_f16 v[158:161], v[162:165], v[42:45], v[158:161]
	v_med3_f32 v174, v153, v170, v79
	ds_read_b128 v[162:165], v145
	v_med3_f32 v153, v78, v153, v79
	s_waitcnt lgkmcnt(1)
	v_mfma_f32_16x16x32_f16 v[170:173], v[102:105], v[26:29], 0
	v_min_f32 v178, v78, v79
	v_or_b32_e32 v179, 0x3f3, v175
	v_med3_f32 v184, v153, v174, v179
	v_mfma_f32_16x16x32_f16 v[78:81], v[102:105], v[58:61], 0
	ds_read_b128 v[102:105], v152 offset:256
	v_med3_f32 v185, v178, v153, v179
	v_min_f32 v186, v178, v179
	ds_read_b128 v[178:181], v151 offset:256
	s_waitcnt lgkmcnt(2)
	v_mfma_f32_16x16x32_f16 v[174:177], v[162:165], v[26:29], 0
	v_and_b32_e32 v75, 0xfffffc00, v76
	v_or_b32_e32 v75, 0x3f2, v75
	v_med3_f32 v122, v182, v122, v75
	s_waitcnt lgkmcnt(1)
	v_mfma_f32_16x16x32_f16 v[170:173], v[102:105], v[22:25], v[170:173]
	v_fma_mix_f32 v67, v166, v30, v34 op_sel_hi:[0,1,0]
	v_fma_mix_f32 v30, v167, v30, v67 op_sel:[0,1,0] op_sel_hi:[0,1,0]
	v_fma_mix_f32 v30, v168, v31, v30 op_sel_hi:[0,1,0]
	v_mfma_f32_16x16x32_f16 v[78:81], v[102:105], v[54:57], v[78:81]
	ds_read_b128 v[102:105], v150 offset:256
	v_fma_mix_f32 v30, v169, v31, v30 op_sel:[0,1,0] op_sel_hi:[0,1,0]
	v_fma_mix_f32 v30, v154, v32, v30 op_sel_hi:[0,1,0]
	s_waitcnt lgkmcnt(1)
	v_mfma_f32_16x16x32_f16 v[150:153], v[178:181], v[22:25], v[174:177]
	v_fma_mix_f32 v30, v155, v32, v30 op_sel:[0,1,0] op_sel_hi:[0,1,0]
	v_fma_mix_f32 v30, v156, v33, v30 op_sel_hi:[0,1,0]
	s_nop 0
	ds_read_b128 v[174:177], v149 offset:256
	v_mfma_f32_16x16x32_f16 v[162:165], v[162:165], v[58:61], 0
	v_med3_f32 v149, v74, v182, v75
	v_mfma_f32_16x16x32_f16 v[162:165], v[178:181], v[54:57], v[162:165]
	v_min_f32 v178, v74, v75
	v_and_b32_e32 v179, 0xfffffc00, v77
	v_or_b32_e32 v179, 0x3f3, v179
	s_waitcnt lgkmcnt(1)
	v_mfma_f32_16x16x32_f16 v[74:77], v[102:105], v[50:53], v[78:81]
	v_med3_f32 v122, v149, v122, v179
	v_mfma_f32_16x16x32_f16 v[170:173], v[102:105], v[18:21], v[170:173]
	s_nop 1
	ds_read_b128 v[78:81], v148 offset:256
	s_waitcnt lgkmcnt(1)
	v_mfma_f32_16x16x32_f16 v[102:105], v[174:177], v[18:21], v[150:153]
	v_med3_f32 v152, v178, v149, v179
	v_min_f32 v153, v178, v179
	v_mfma_f32_16x16x32_f16 v[148:151], v[174:177], v[50:53], v[162:165]
	s_nop 2
	ds_read_b128 v[162:165], v147 offset:256
	s_waitcnt lgkmcnt(1)
	v_mfma_f32_16x16x32_f16 v[170:173], v[78:81], v[14:17], v[170:173]
	v_mfma_f32_16x16x32_f16 v[74:77], v[78:81], v[46:49], v[74:77]
	ds_read_b128 v[78:81], v146 offset:256
	s_waitcnt lgkmcnt(1)
	v_mfma_f32_16x16x32_f16 v[86:89], v[162:165], v[14:17], v[102:105]
	s_nop 2
	ds_read_b128 v[102:105], v145 offset:256
	s_waitcnt vmcnt(4)
	v_mfma_f32_16x16x32_f16 v[90:93], v[162:165], v[46:49], v[148:151]
	s_waitcnt lgkmcnt(0)
	s_barrier
	ds_read_b128 v[82:85], v144 offset:8448
	s_waitcnt lgkmcnt(2)
	v_mfma_f32_16x16x32_f16 v[38:41], v[78:81], v[42:45], v[74:77]
	s_nop 2
	ds_read_b128 v[74:77], v144 offset:256
	s_waitcnt lgkmcnt(2)
	v_mfma_f32_16x16x32_f16 v[70:73], v[102:105], v[42:45], v[90:93]
	s_nop 2
	ds_read_b128 v[90:93], v143 offset:256
	v_mfma_f32_16x16x32_f16 v[146:149], v[78:81], v[10:13], v[170:173]
	v_mfma_f32_16x16x32_f16 v[78:81], v[102:105], v[10:13], v[86:89]
	ds_read_b128 v[102:105], v143 offset:8448
	s_waitcnt lgkmcnt(2)
	v_mfma_f32_16x16x32_f16 v[86:89], v[74:77], v[22:25], 0
	v_mfma_f32_16x16x32_f16 v[74:77], v[74:77], v[54:57], 0
	s_waitcnt lgkmcnt(1)
	v_mfma_f32_16x16x32_f16 v[86:89], v[90:93], v[18:21], v[86:89]
	v_mfma_f32_16x16x32_f16 v[34:37], v[90:93], v[50:53], v[74:77]
	v_fma_mix_f32 v90, v94, v62, v66 op_sel_hi:[0,1,0]
	ds_read_b128 v[66:69], v142 offset:256
	v_fma_mix_f32 v62, v95, v62, v90 op_sel:[0,1,0] op_sel_hi:[0,1,0]
	ds_read_b128 v[90:93], v142 offset:8448
	v_mfma_f32_16x16x32_f16 v[98:101], v[82:85], v[22:25], 0
	v_fma_mix_f32 v62, v96, v63, v62 op_sel_hi:[0,1,0]
	v_fma_mix_f32 v31, v97, v63, v62 op_sel:[0,1,0] op_sel_hi:[0,1,0]
	v_fma_mix_f32 v31, v158, v64, v31 op_sel_hi:[0,1,0]
	v_mfma_f32_16x16x32_f16 v[82:85], v[82:85], v[54:57], 0
	v_fma_mix_f32 v31, v159, v64, v31 op_sel:[0,1,0] op_sel_hi:[0,1,0]
	v_fma_mix_f32 v31, v160, v65, v31 op_sel_hi:[0,1,0]
	v_fma_mix_f32 v62, v157, v33, v30 op_sel:[0,1,0] op_sel_hi:[0,1,0]
	s_waitcnt lgkmcnt(1)
	v_mfma_f32_16x16x32_f16 v[86:89], v[66:69], v[14:17], v[86:89]
	v_fma_mix_f32 v63, v161, v65, v31 op_sel:[0,1,0] op_sel_hi:[0,1,0]
	v_fma_mix_f32 v38, v38, v58, v63 op_sel_hi:[0,1,0]
	v_fma_mix_f32 v38, v39, v58, v38 op_sel:[0,1,0] op_sel_hi:[0,1,0]
	v_mfma_f32_16x16x32_f16 v[34:37], v[66:69], v[46:49], v[34:37]
	ds_read_b128 v[66:69], v141 offset:256
	v_fma_mix_f32 v38, v40, v59, v38 op_sel_hi:[0,1,0]
	v_mfma_f32_16x16x32_f16 v[74:77], v[102:105], v[18:21], v[98:101]
	v_mfma_f32_16x16x32_f16 v[82:85], v[102:105], v[50:53], v[82:85]
	s_waitcnt lgkmcnt(1)
	v_mfma_f32_16x16x32_f16 v[74:77], v[90:93], v[14:17], v[74:77]
	v_mfma_f32_16x16x32_f16 v[30:33], v[90:93], v[46:49], v[82:85]
	v_fma_mix_f32 v90, v146, v26, v62 op_sel_hi:[0,1,0]
	v_fma_mix_f32 v26, v147, v26, v90 op_sel:[0,1,0] op_sel_hi:[0,1,0]
	v_fma_mix_f32 v26, v148, v27, v26 op_sel_hi:[0,1,0]
	v_fma_mix_f32 v26, v149, v27, v26 op_sel:[0,1,0] op_sel_hi:[0,1,0]
	ds_read_b128 v[62:65], v141 offset:8448
	s_waitcnt lgkmcnt(1)
	v_mfma_f32_16x16x32_f16 v[82:85], v[66:69], v[10:13], v[86:89]
	v_fma_mix_f32 v27, v41, v59, v38 op_sel:[0,1,0] op_sel_hi:[0,1,0]
	v_fma_mix_f32 v26, v78, v28, v26 op_sel_hi:[0,1,0]
	v_fma_mix_f32 v27, v70, v60, v27 op_sel_hi:[0,1,0]
	v_mfma_f32_16x16x32_f16 v[34:37], v[66:69], v[42:45], v[34:37]
	ds_read_b128 v[66:69], v143 offset:16640
	v_fma_mix_f32 v26, v79, v28, v26 op_sel:[0,1,0] op_sel_hi:[0,1,0]
	v_fma_mix_f32 v27, v71, v60, v27 op_sel:[0,1,0] op_sel_hi:[0,1,0]
	v_fma_mix_f32 v26, v80, v29, v26 op_sel_hi:[0,1,0]
	v_fma_mix_f32 v58, v72, v61, v27 op_sel_hi:[0,1,0]
	v_fma_mix_f32 v59, v81, v29, v26 op_sel:[0,1,0] op_sel_hi:[0,1,0]
	v_fma_mix_f32 v70, v73, v61, v58 op_sel:[0,1,0] op_sel_hi:[0,1,0]
	v_fma_mix_f32 v71, v82, v22, v59 op_sel_hi:[0,1,0]
	ds_read_b128 v[58:61], v142 offset:16640
	v_fma_mix_f32 v34, v34, v54, v70 op_sel_hi:[0,1,0]
	v_fma_mix_f32 v22, v83, v22, v71 op_sel:[0,1,0] op_sel_hi:[0,1,0]
	v_fma_mix_f32 v34, v35, v54, v34 op_sel:[0,1,0] op_sel_hi:[0,1,0]
	v_fma_mix_f32 v22, v84, v23, v22 op_sel_hi:[0,1,0]
	v_fma_mix_f32 v34, v36, v55, v34 op_sel_hi:[0,1,0]
	ds_read_b128 v[38:41], v143 offset:24832
	v_fma_mix_f32 v22, v85, v23, v22 op_sel:[0,1,0] op_sel_hi:[0,1,0]
	v_fma_mix_f32 v23, v37, v55, v34 op_sel:[0,1,0] op_sel_hi:[0,1,0]
	ds_read_b128 v[34:37], v141 offset:16640
	s_waitcnt lgkmcnt(4)
	v_mfma_f32_16x16x32_f16 v[74:77], v[62:65], v[10:13], v[74:77]
	ds_read_b128 v[70:73], v142 offset:24832
	v_mfma_f32_16x16x32_f16 v[30:33], v[62:65], v[42:45], v[30:33]
	s_waitcnt lgkmcnt(4)
	v_mfma_f32_16x16x32_f16 v[62:65], v[66:69], v[18:21], 0
	s_nop 3
	v_fma_mix_f32 v22, v74, v24, v22 op_sel_hi:[0,1,0]
	s_nop 0
	v_fma_mix_f32 v23, v30, v56, v23 op_sel_hi:[0,1,0]
	v_fma_mix_f32 v22, v75, v24, v22 op_sel:[0,1,0] op_sel_hi:[0,1,0]
	v_mfma_f32_16x16x32_f16 v[26:29], v[66:69], v[50:53], 0
	v_fma_mix_f32 v23, v31, v56, v23 op_sel:[0,1,0] op_sel_hi:[0,1,0]
	v_fma_mix_f32 v22, v76, v25, v22 op_sel_hi:[0,1,0]
	v_fma_mix_f32 v23, v32, v57, v23 op_sel_hi:[0,1,0]
	s_waitcnt lgkmcnt(3)
	v_mfma_f32_16x16x32_f16 v[62:65], v[58:61], v[14:17], v[62:65]
	v_fma_mix_f32 v30, v77, v25, v22 op_sel:[0,1,0] op_sel_hi:[0,1,0]
	v_fma_mix_f32 v31, v33, v57, v23 op_sel:[0,1,0] op_sel_hi:[0,1,0]
	ds_read_b128 v[22:25], v141 offset:24832
	v_mfma_f32_16x16x32_f16 v[26:29], v[58:61], v[46:49], v[26:29]
	s_waitcnt vmcnt(0)
	s_waitcnt lgkmcnt(0)
	s_barrier
	s_waitcnt lgkmcnt(3)
	v_mfma_f32_16x16x32_f16 v[66:69], v[38:41], v[18:21], 0
	v_mfma_f32_16x16x32_f16 v[38:41], v[38:41], v[50:53], 0
	s_waitcnt lgkmcnt(2)
	v_mfma_f32_16x16x32_f16 v[62:65], v[34:37], v[10:13], v[62:65]
	v_mfma_f32_16x16x32_f16 v[26:29], v[34:37], v[42:45], v[26:29]
	ds_read_b128 v[34:37], v142 offset:33024
	s_nop 5
	v_fma_mix_f32 v54, v62, v18, v30 op_sel_hi:[0,1,0]
	v_fma_mix_f32 v18, v63, v18, v54 op_sel:[0,1,0] op_sel_hi:[0,1,0]
	s_waitcnt lgkmcnt(2)
	v_mfma_f32_16x16x32_f16 v[58:61], v[70:73], v[14:17], v[66:69]
	v_fma_mix_f32 v18, v64, v19, v18 op_sel_hi:[0,1,0]
	v_fma_mix_f32 v26, v26, v50, v31 op_sel_hi:[0,1,0]
	v_fma_mix_f32 v26, v27, v50, v26 op_sel:[0,1,0] op_sel_hi:[0,1,0]
	v_mfma_f32_16x16x32_f16 v[30:33], v[70:73], v[46:49], v[38:41]
	v_fma_mix_f32 v26, v28, v51, v26 op_sel_hi:[0,1,0]
	v_fma_mix_f32 v18, v65, v19, v18 op_sel:[0,1,0] op_sel_hi:[0,1,0]
	v_fma_mix_f32 v19, v29, v51, v26 op_sel:[0,1,0] op_sel_hi:[0,1,0]
	s_waitcnt lgkmcnt(1)
	v_mfma_f32_16x16x32_f16 v[38:41], v[22:25], v[10:13], v[58:61]
	ds_read_b128 v[26:29], v141 offset:33024
	v_mfma_f32_16x16x32_f16 v[22:25], v[22:25], v[42:45], v[30:33]
	s_nop 2
	ds_read_b128 v[30:33], v142 offset:41216
	s_waitcnt lgkmcnt(2)
	v_mfma_f32_16x16x32_f16 v[54:57], v[34:37], v[14:17], 0
	s_nop 1
	v_fma_mix_f32 v19, v22, v52, v19 op_sel_hi:[0,1,0]
	v_fma_mix_f32 v19, v23, v52, v19 op_sel:[0,1,0] op_sel_hi:[0,1,0]
	v_fma_mix_f32 v18, v38, v20, v18 op_sel_hi:[0,1,0]
	v_mfma_f32_16x16x32_f16 v[34:37], v[34:37], v[46:49], 0
	v_fma_mix_f32 v22, v24, v53, v19 op_sel_hi:[0,1,0]
	v_fma_mix_f32 v18, v39, v20, v18 op_sel:[0,1,0] op_sel_hi:[0,1,0]
	v_fma_mix_f32 v39, v25, v53, v22 op_sel:[0,1,0] op_sel_hi:[0,1,0]
	ds_read_b128 v[22:25], v141 offset:41216
	v_fma_mix_f32 v18, v40, v21, v18 op_sel_hi:[0,1,0]
	v_fma_mix_f32 v38, v41, v21, v18 op_sel:[0,1,0] op_sel_hi:[0,1,0]
	s_waitcnt lgkmcnt(2)
	v_mfma_f32_16x16x32_f16 v[18:21], v[26:29], v[10:13], v[54:57]
	v_mfma_f32_16x16x32_f16 v[26:29], v[26:29], v[42:45], v[34:37]
	s_waitcnt lgkmcnt(1)
	v_mfma_f32_16x16x32_f16 v[58:61], v[30:33], v[14:17], 0
	s_nop 4
	v_fma_mix_f32 v18, v18, v14, v38 op_sel_hi:[0,1,0]
	v_fma_mix_f32 v26, v26, v46, v39 op_sel_hi:[0,1,0]
	v_fma_mix_f32 v14, v19, v14, v18 op_sel:[0,1,0] op_sel_hi:[0,1,0]
	v_mfma_f32_16x16x32_f16 v[30:33], v[30:33], v[46:49], 0
	v_fma_mix_f32 v18, v27, v46, v26 op_sel:[0,1,0] op_sel_hi:[0,1,0]
	v_fma_mix_f32 v14, v20, v15, v14 op_sel_hi:[0,1,0]
	v_fma_mix_f32 v26, v28, v47, v18 op_sel_hi:[0,1,0]
	v_fma_mix_f32 v14, v21, v15, v14 op_sel:[0,1,0] op_sel_hi:[0,1,0]
	s_waitcnt lgkmcnt(0)
	v_mfma_f32_16x16x32_f16 v[18:21], v[22:25], v[10:13], v[58:61]
	v_fma_mix_f32 v15, v29, v47, v26 op_sel:[0,1,0] op_sel_hi:[0,1,0]
	ds_read_b128 v[26:29], v141 offset:49408
	v_mfma_f32_16x16x32_f16 v[22:25], v[22:25], v[42:45], v[30:33]
	s_nop 4
	v_fma_mix_f32 v14, v18, v16, v14 op_sel_hi:[0,1,0]
	s_nop 1
	v_fma_mix_f32 v15, v22, v48, v15 op_sel_hi:[0,1,0]
	v_fma_mix_f32 v14, v19, v16, v14 op_sel:[0,1,0] op_sel_hi:[0,1,0]
	v_fma_mix_f32 v15, v23, v48, v15 op_sel:[0,1,0] op_sel_hi:[0,1,0]
	v_fma_mix_f32 v14, v20, v17, v14 op_sel_hi:[0,1,0]
	v_fma_mix_f32 v18, v24, v49, v15 op_sel_hi:[0,1,0]
	v_fma_mix_f32 v22, v21, v17, v14 op_sel:[0,1,0] op_sel_hi:[0,1,0]
	v_fma_mix_f32 v30, v25, v49, v18 op_sel:[0,1,0] op_sel_hi:[0,1,0]
	ds_read_b128 v[18:21], v141 offset:57600
	s_waitcnt lgkmcnt(1)
	v_mfma_f32_16x16x32_f16 v[14:17], v[26:29], v[10:13], 0
	s_nop 7
	v_fma_mix_f32 v14, v14, v10, v22 op_sel_hi:[0,1,0]
	v_mfma_f32_16x16x32_f16 v[22:25], v[26:29], v[42:45], 0
	v_fma_mix_f32 v14, v15, v10, v14 op_sel:[0,1,0] op_sel_hi:[0,1,0]
	v_fma_mix_f32 v14, v16, v11, v14 op_sel_hi:[0,1,0]
	s_waitcnt lgkmcnt(0)
	v_mfma_f32_16x16x32_f16 v[26:29], v[18:21], v[10:13], 0
	v_fma_mix_f32 v10, v17, v11, v14 op_sel:[0,1,0] op_sel_hi:[0,1,0]
	s_nop 2
	v_fma_mix_f32 v22, v22, v42, v30 op_sel_hi:[0,1,0]
	v_fma_mix_f32 v15, v23, v42, v22 op_sel:[0,1,0] op_sel_hi:[0,1,0]
	v_fma_mix_f32 v15, v24, v43, v15 op_sel_hi:[0,1,0]
	v_fma_mix_f32 v11, v25, v43, v15 op_sel:[0,1,0] op_sel_hi:[0,1,0]
	v_fma_mix_f32 v10, v26, v12, v10 op_sel_hi:[0,1,0]
	v_mfma_f32_16x16x32_f16 v[14:17], v[18:21], v[42:45], 0
	v_fma_mix_f32 v10, v27, v12, v10 op_sel:[0,1,0] op_sel_hi:[0,1,0]
	v_fma_mix_f32 v10, v28, v13, v10 op_sel_hi:[0,1,0]
	v_lshlrev_b32_e32 v12, 2, v125
	v_fma_mix_f32 v10, v29, v13, v10 op_sel:[0,1,0] op_sel_hi:[0,1,0]
	v_or_b32_e32 v13, v12, v186
	v_mov_b32_e32 v18, v13
	v_mov_b32_e32 v19, v13
	s_nop 0
	v_fma_mix_f32 v11, v14, v44, v11 op_sel_hi:[0,1,0]
	v_or_b32_e32 v14, v12, v185
	v_permlane16_swap_b32_e32 v18, v19
	v_cndmask_b32_e64 v18, v18, v19, s[4:5]
	v_mov_b32_e32 v19, v14
	v_mov_b32_e32 v20, v14
	v_fma_mix_f32 v11, v15, v44, v11 op_sel:[0,1,0] op_sel_hi:[0,1,0]
	v_or_b32_e32 v15, v12, v184
	v_permlane16_swap_b32_e32 v19, v20
	v_cndmask_b32_e64 v19, v19, v20, s[4:5]
	v_mov_b32_e32 v20, v15
	v_mov_b32_e32 v21, v15
	v_fma_mix_f32 v11, v16, v45, v11 op_sel_hi:[0,1,0]
	v_or_b32_e32 v16, v12, v153
	v_permlane16_swap_b32_e32 v20, v21
	v_cndmask_b32_e64 v20, v20, v21, s[4:5]
	v_mov_b32_e32 v21, v16
	v_mov_b32_e32 v22, v16
	v_fma_mix_f32 v11, v17, v45, v11 op_sel:[0,1,0] op_sel_hi:[0,1,0]
	v_or_b32_e32 v17, v12, v152
	v_permlane16_swap_b32_e32 v21, v22
	v_cndmask_b32_e64 v21, v21, v22, s[4:5]
	v_mov_b32_e32 v22, v17
	v_mov_b32_e32 v23, v17
	v_med3_f32 v15, v14, v15, v18
	v_med3_f32 v14, v13, v14, v18
	v_or_b32_e32 v12, v12, v122
	s_nop 0
	v_permlane16_swap_b32_e32 v22, v23
	v_min_f32 v13, v13, v18
	v_med3_f32 v15, v14, v15, v19
	v_cndmask_b32_e64 v22, v22, v23, s[4:5]
	v_med3_f32 v14, v13, v14, v19
	v_mov_b32_e32 v23, v12
	v_mov_b32_e32 v24, v12
	v_min_f32 v13, v13, v19
	v_med3_f32 v18, v14, v15, v20
	v_med3_f32 v12, v17, v12, v21
	s_nop 1
	v_permlane16_swap_b32_e32 v23, v24
	v_med3_f32 v19, v13, v14, v20
	v_med3_f32 v14, v16, v17, v21
	v_min_f32 v15, v16, v21
	v_cndmask_b32_e64 v23, v23, v24, s[4:5]
	v_med3_f32 v12, v14, v12, v22
	v_med3_f32 v14, v15, v14, v22
	v_min_f32 v15, v15, v22
	v_min_f32 v13, v13, v20
	v_mov_b32_e32 v20, v19
	v_med3_f32 v12, v14, v12, v23
	v_med3_f32 v16, v15, v14, v23
	v_mov_b32_e32 v14, v10
	s_nop 1
	v_permlane16_swap_b32_e32 v10, v14
	v_add_f32_e32 v14, v10, v14
	v_mov_b32_e32 v10, v11
	s_nop 1
	v_permlane16_swap_b32_e32 v11, v10
	v_min_f32 v17, v15, v23
	v_add_f32_e32 v15, v11, v10
	v_mov_b32_e32 v10, v13
	v_mov_b32_e32 v11, v13
	s_nop 1
	v_permlane32_swap_b32_e32 v10, v11
	v_cndmask_b32_e64 v10, v10, v11, s[6:7]
	v_mov_b32_e32 v11, v19
	s_nop 1
	v_permlane32_swap_b32_e32 v11, v20
	v_cndmask_b32_e64 v11, v11, v20, s[6:7]
	v_mov_b32_e32 v20, v18
	v_mov_b32_e32 v21, v18
	s_nop 1
	v_permlane32_swap_b32_e32 v20, v21
	v_cndmask_b32_e64 v20, v20, v21, s[6:7]
	v_mov_b32_e32 v21, v17
	v_mov_b32_e32 v22, v17
	s_nop 1
	v_permlane32_swap_b32_e32 v21, v22
	v_cndmask_b32_e64 v21, v21, v22, s[6:7]
	v_mov_b32_e32 v22, v16
	v_mov_b32_e32 v23, v16
	v_med3_f32 v18, v19, v18, v10
	s_nop 1
	v_permlane32_swap_b32_e32 v22, v23
	v_med3_f32 v19, v13, v19, v10
	v_min_f32 v10, v13, v10
	v_cndmask_b32_e64 v22, v22, v23, s[6:7]
	v_med3_f32 v13, v19, v18, v11
	v_med3_f32 v18, v10, v19, v11
	v_min_f32 v11, v10, v11
	v_mov_b32_e32 v23, v12
	v_mov_b32_e32 v24, v12
	v_med3_f32 v10, v18, v13, v20
	v_med3_f32 v13, v11, v18, v20
	v_min_f32 v19, v11, v20
	v_med3_f32 v11, v16, v12, v21
	v_med3_f32 v12, v17, v16, v21
	s_nop 1
	v_permlane32_swap_b32_e32 v23, v24
	v_min_f32 v16, v17, v21
	v_med3_f32 v11, v12, v11, v22
	v_cndmask_b32_e64 v23, v23, v24, s[6:7]
	v_med3_f32 v12, v16, v12, v22
	v_min_f32 v17, v16, v22
	v_mov_b32_e32 v18, v15
	v_med3_f32 v11, v12, v11, v23
	v_med3_f32 v16, v17, v12, v23
	v_min_f32 v12, v17, v23
	v_mov_b32_e32 v17, v14
	s_nop 1
	v_permlane32_swap_b32_e32 v14, v17
	v_permlane32_swap_b32_e32 v15, v18
	v_cndmask_b32_e64 v12, v12, v19, s[4:5]
	s_and_saveexec_b64 s[0:1], s[6:7]
	s_cbranch_execz .LBB1_10
	s_load_dword s3, s[12:13], 0x0
	v_add_f32_e32 v19, v137, v138
	v_add_f32_e32 v20, v139, v140
	v_add_f32_e32 v14, v14, v17
	v_add_f32_e32 v15, v15, v18
	v_cndmask_b32_e64 v19, v20, v19, s[4:5]
	v_cndmask_b32_e64 v14, v15, v14, s[4:5]
	v_fmac_f32_e32 v14, 2.0, v19
	s_waitcnt lgkmcnt(0)
	v_add_f32_e32 v14, s3, v14
	v_add_f32_e32 v14, v132, v14
	v_add_f32_e32 v123, v12, v14

	.amdhsa_kernel _Z6k_mainPKfS0_S0_PKDF16_S0_S0_S0_S0_S0_S0_PfP15HIP_vector_typeIiLj4EEPiS3_
		.amdhsa_group_segment_fixed_size 105056
		.amdhsa_private_segment_fixed_size 0
		.amdhsa_kernarg_size 112
		.amdhsa_user_sgpr_count 2
		.amdhsa_user_sgpr_dispatch_ptr 0
		.amdhsa_user_sgpr_queue_ptr 0
		.amdhsa_user_sgpr_kernarg_segment_ptr 1
		.amdhsa_user_sgpr_dispatch_id 0
		.amdhsa_user_sgpr_kernarg_preload_length 0
		.amdhsa_user_sgpr_kernarg_preload_offset 0
		.amdhsa_user_sgpr_private_segment_size 0
		.amdhsa_uses_dynamic_stack 0
		.amdhsa_enable_private_segment 0
		.amdhsa_system_sgpr_workgroup_id_x 1
		.amdhsa_system_sgpr_workgroup_id_y 0
		.amdhsa_system_sgpr_workgroup_id_z 0
		.amdhsa_system_sgpr_workgroup_info 0
		.amdhsa_system_vgpr_workitem_id 0
		.amdhsa_next_free_vgpr 248
		.amdhsa_next_free_sgpr 96
		.amdhsa_accum_offset 248
		.amdhsa_reserve_vcc 1
		.amdhsa_float_round_mode_32 0
		.amdhsa_float_round_mode_16_64 0
		.amdhsa_float_denorm_mode_32 3
		.amdhsa_float_denorm_mode_16_64 3
		.amdhsa_dx10_clamp 1
		.amdhsa_ieee_mode 1
		.amdhsa_fp16_overflow 0
		.amdhsa_tg_split 0
		.amdhsa_exception_fp_ieee_invalid_op 0
		.amdhsa_exception_fp_denorm_src 0
		.amdhsa_exception_fp_ieee_div_zero 0
		.amdhsa_exception_fp_ieee_overflow 0
		.amdhsa_exception_fp_ieee_underflow 0
		.amdhsa_exception_fp_ieee_inexact 0
		.amdhsa_exception_int_div_zero 0
	.end_amdhsa_kernel

amdhsa.kernels:
  - .agpr_count:     0
    .args:
      - .actual_access:  read_only
        .address_space:  global
        .offset:         0
        .size:           8
        .value_kind:     global_buffer
      - .actual_access:  read_only
        .address_space:  global
        .offset:         8
        .size:           8
        .value_kind:     global_buffer
      - .actual_access:  read_only
        .address_space:  global
        .offset:         16
        .size:           8
        .value_kind:     global_buffer
      - .actual_access:  read_only
        .address_space:  global
        .offset:         24
        .size:           8
        .value_kind:     global_buffer
      - .actual_access:  read_only
        .address_space:  global
        .offset:         32
        .size:           8
        .value_kind:     global_buffer
      - .actual_access:  write_only
        .address_space:  global
        .offset:         40
        .size:           8
        .value_kind:     global_buffer
      - .actual_access:  write_only
        .address_space:  global
        .offset:         48
        .size:           8
        .value_kind:     global_buffer
      - .actual_access:  write_only
        .address_space:  global
        .offset:         56
        .size:           8
        .value_kind:     global_buffer
      - .actual_access:  write_only
        .address_space:  global
        .offset:         64
        .size:           8
        .value_kind:     global_buffer
      - .actual_access:  write_only
        .address_space:  global
        .offset:         72
        .size:           8
        .value_kind:     global_buffer
      - .actual_access:  write_only
        .address_space:  global
        .offset:         80
        .size:           8
        .value_kind:     global_buffer
      - .actual_access:  write_only
        .address_space:  global
        .offset:         88
        .size:           8
        .value_kind:     global_buffer
      - .actual_access:  write_only
        .address_space:  global
        .offset:         96
        .size:           8
        .value_kind:     global_buffer
    .group_segment_fixed_size: 73760
    .kernarg_segment_align: 8
    .kernarg_segment_size: 104
    .language:       OpenCL C
    .language_version:
      - 2
      - 0
    .max_flat_workgroup_size: 512
    .name:           _Z6k_prepPKfS0_S0_S0_S0_PfPDF16_S1_S1_S1_S1_S1_Pi
    .private_segment_fixed_size: 0
    .sgpr_count:     35
    .sgpr_spill_count: 0
    .symbol:         _Z6k_prepPKfS0_S0_S0_S0_PfPDF16_S1_S1_S1_S1_S1_Pi.kd
    .uniform_work_group_size: 1
    .uses_dynamic_stack: false
    .vgpr_count:     127
    .vgpr_spill_count: 0
    .wavefront_size: 64
  - .agpr_count:     0
    .args:
      - .actual_access:  read_only
        .address_space:  global
        .offset:         0
        .size:           8
        .value_kind:     global_buffer
      - .actual_access:  read_only
        .address_space:  global
        .offset:         8
        .size:           8
        .value_kind:     global_buffer
      - .actual_access:  read_only
        .address_space:  global
        .offset:         16
        .size:           8
        .value_kind:     global_buffer
      - .address_space:  global
        .offset:         24
        .size:           8
        .value_kind:     global_buffer
      - .actual_access:  read_only
        .address_space:  global
        .offset:         32
        .size:           8
        .value_kind:     global_buffer
      - .actual_access:  read_only
        .address_space:  global
        .offset:         40
        .size:           8
        .value_kind:     global_buffer
      - .actual_access:  read_only
        .address_space:  global
        .offset:         48
        .size:           8
        .value_kind:     global_buffer
      - .actual_access:  read_only
        .address_space:  global
        .offset:         56
        .size:           8
        .value_kind:     global_buffer
      - .actual_access:  read_only
        .address_space:  global
        .offset:         64
        .size:           8
        .value_kind:     global_buffer
      - .actual_access:  read_only
        .address_space:  global
        .offset:         72
        .size:           8
        .value_kind:     global_buffer
      - .actual_access:  write_only
        .address_space:  global
        .offset:         80
        .size:           8
        .value_kind:     global_buffer
      - .actual_access:  write_only
        .address_space:  global
        .offset:         88
        .size:           8
        .value_kind:     global_buffer
      - .address_space:  global
        .offset:         96
        .size:           8
        .value_kind:     global_buffer
      - .actual_access:  write_only
        .address_space:  global
        .offset:         104
        .size:           8
        .value_kind:     global_buffer
    .group_segment_fixed_size: 105056
    .kernarg_segment_align: 8
    .kernarg_segment_size: 112
    .language:       OpenCL C
    .language_version:
      - 2
      - 0
    .max_flat_workgroup_size: 512
    .name:           _Z6k_mainPKfS0_S0_PKDF16_S0_S0_S0_S0_S0_S0_PfP15HIP_vector_typeIiLj4EEPiS3_
    .private_segment_fixed_size: 0
    .sgpr_count:     100
    .sgpr_spill_count: 0
    .symbol:         _Z6k_mainPKfS0_S0_PKDF16_S0_S0_S0_S0_S0_S0_PfP15HIP_vector_typeIiLj4EEPiS3_.kd
    .uniform_work_group_size: 1
    .uses_dynamic_stack: false
    .vgpr_count:     248
    .vgpr_spill_count: 0
    .wavefront_size: 64
  - .agpr_count:     0
    .args:
      - .actual_access:  read_only
        .address_space:  global
        .offset:         0
        .size:           8
        .value_kind:     global_buffer
      - .actual_access:  read_only
        .address_space:  global
        .offset:         8
        .size:           8
        .value_kind:     global_buffer
      - .actual_access:  read_only
        .address_space:  global
        .offset:         16
        .size:           8
        .value_kind:     global_buffer
      - .actual_access:  read_only
        .address_space:  global
        .offset:         24
        .size:           8
        .value_kind:     global_buffer
      - .actual_access:  read_only
        .address_space:  global
        .offset:         32
        .size:           8
        .value_kind:     global_buffer
      - .actual_access:  read_only
        .address_space:  global
        .offset:         40
        .size:           8
        .value_kind:     global_buffer
      - .actual_access:  read_only
        .address_space:  global
        .offset:         48
        .size:           8
        .value_kind:     global_buffer
      - .actual_access:  read_only
        .address_space:  global
        .offset:         56
        .size:           8
        .value_kind:     global_buffer
      - .address_space:  global
        .offset:         64
        .size:           8
        .value_kind:     global_buffer
      - .address_space:  global
        .offset:         72
        .size:           8
        .value_kind:     global_buffer
      - .actual_access:  read_only
        .address_space:  global
        .offset:         80
        .size:           8
        .value_kind:     global_buffer
      - .actual_access:  read_only
        .address_space:  global
        .offset:         88
        .size:           8
        .value_kind:     global_buffer
      - .actual_access:  write_only
        .address_space:  global
        .offset:         96
        .size:           8
        .value_kind:     global_buffer
      - .offset:         104
        .size:           4
        .value_kind:     hidden_block_count_x
      - .offset:         108
        .size:           4
        .value_kind:     hidden_block_count_y
      - .offset:         112
        .size:           4
        .value_kind:     hidden_block_count_z
      - .offset:         116
        .size:           2
        .value_kind:     hidden_group_size_x
      - .offset:         118
        .size:           2
        .value_kind:     hidden_group_size_y
      - .offset:         120
        .size:           2
        .value_kind:     hidden_group_size_z
      - .offset:         122
        .size:           2
        .value_kind:     hidden_remainder_x
      - .offset:         124
        .size:           2
        .value_kind:     hidden_remainder_y
      - .offset:         126
        .size:           2
        .value_kind:     hidden_remainder_z
      - .offset:         144
        .size:           8
        .value_kind:     hidden_global_offset_x
      - .offset:         152
        .size:           8
        .value_kind:     hidden_global_offset_y
      - .offset:         160
        .size:           8
        .value_kind:     hidden_global_offset_z
      - .offset:         168
        .size:           2
        .value_kind:     hidden_grid_dims
    .group_segment_fixed_size: 4120
    .kernarg_segment_align: 8
    .kernarg_segment_size: 360
    .language:       OpenCL C
    .language_version:
      - 2
      - 0
    .max_flat_workgroup_size: 256
    .name:           _Z4k_t2PKfS0_S0_S0_S0_S0_PK15HIP_vector_typeIiLj4EEPKiPdPiS0_S0_Pf
    .private_segment_fixed_size: 0
    .sgpr_count:     106
    .sgpr_spill_count: 0
    .symbol:         _Z4k_t2PKfS0_S0_S0_S0_S0_PK15HIP_vector_typeIiLj4EEPKiPdPiS0_S0_Pf.kd
    .uniform_work_group_size: 1
    .uses_dynamic_stack: false
    .vgpr_count:     158
    .vgpr_spill_count: 0
    .wavefront_size: 64
